# diff-attn: initial P offset 3.5 (fewer rescale events) + row-sum MFMA as 16x16x128 instead of 32x32x64
# speedup vs baseline: 1.0431x; 1.0431x over previous
.LBB0_1200:
	s_or_b64 exec, exec, s[28:29]
	s_waitcnt lgkmcnt(0)
	v_add_u32_e32 v126, s78, v186
	ds_read_b128 v[114:117], v126 offset:49248
	ds_read_b128 v[118:121], v126 offset:49216
	ds_read_b128 v[122:125], v126 offset:49184
	ds_read_b128 v[126:129], v126 offset:49152
	ds_read_b128 v[244:247], v250 offset:49152
	s_waitcnt lgkmcnt(0)
	v_pk_mul_f32 v[14:15], v[14:15], v[114:115]
	v_pk_mul_f32 v[10:11], v[10:11], v[118:119]
	v_pk_mul_f32 v[6:7], v[6:7], v[122:123]
	v_pk_mul_f32 v[16:17], v[16:17], v[116:117]
	v_pk_mul_f32 v[12:13], v[12:13], v[120:121]
	v_pk_mul_f32 v[8:9], v[8:9], v[124:125]
	v_pk_mul_f32 v[4:5], v[4:5], v[128:129]
	v_pk_mul_f32 v[2:3], v[2:3], v[126:127]
	v_pk_mul_f32 v[46:47], v[46:47], v[114:115]
	v_pk_mul_f32 v[42:43], v[42:43], v[118:119]
	v_pk_mul_f32 v[38:39], v[38:39], v[122:123]
	v_pk_mul_f32 v[48:49], v[48:49], v[116:117]
	v_pk_mul_f32 v[44:45], v[44:45], v[120:121]
	v_pk_mul_f32 v[40:41], v[40:41], v[124:125]
	v_pk_mul_f32 v[36:37], v[36:37], v[128:129]
	v_pk_mul_f32 v[34:35], v[34:35], v[126:127]
	v_pk_mul_f32 v[62:63], v[62:63], v[114:115]
	v_pk_mul_f32 v[58:59], v[58:59], v[118:119]
	v_pk_mul_f32 v[54:55], v[54:55], v[122:123]
	v_pk_mul_f32 v[64:65], v[64:65], v[116:117]
	v_pk_mul_f32 v[60:61], v[60:61], v[120:121]
	v_pk_mul_f32 v[56:57], v[56:57], v[124:125]
	v_pk_mul_f32 v[52:53], v[52:53], v[128:129]
	v_pk_mul_f32 v[50:51], v[50:51], v[126:127]
	v_pk_mul_f32 v[78:79], v[78:79], v[114:115]
	v_pk_mul_f32 v[74:75], v[74:75], v[118:119]
	v_pk_mul_f32 v[70:71], v[70:71], v[122:123]
	v_pk_mul_f32 v[80:81], v[80:81], v[116:117]
	v_pk_mul_f32 v[76:77], v[76:77], v[120:121]
	v_pk_mul_f32 v[72:73], v[72:73], v[124:125]
	v_pk_mul_f32 v[68:69], v[68:69], v[128:129]
	v_pk_mul_f32 v[66:67], v[66:67], v[126:127]
	v_pk_mul_f32 v[18:19], v[18:19], v[244:245]
	v_pk_mul_f32 v[20:21], v[20:21], v[246:247]
.LBB0_1201:
	v_cvt_pk_fp8_f32 v162, v98, v99
	v_cvt_pk_fp8_f32 v163, v102, v103
	v_cvt_pk_fp8_f32 v164, v106, v107
	v_cvt_pk_fp8_f32 v165, v110, v111
	v_cvt_pk_fp8_f32 v166, v82, v83
	v_cvt_pk_fp8_f32 v167, v86, v87
	v_cvt_pk_fp8_f32 v168, v90, v91
	v_cvt_pk_fp8_f32 v169, v94, v95
	v_cvt_pk_fp8_f32 v162, v100, v101 op_sel:[0,0,1]
	v_cvt_pk_fp8_f32 v163, v104, v105 op_sel:[0,0,1]
	v_cvt_pk_fp8_f32 v164, v108, v109 op_sel:[0,0,1]
	v_cvt_pk_fp8_f32 v165, v112, v113 op_sel:[0,0,1]
	v_cvt_pk_fp8_f32 v166, v84, v85 op_sel:[0,0,1]
	v_cvt_pk_fp8_f32 v167, v88, v89 op_sel:[0,0,1]
	v_cvt_pk_fp8_f32 v168, v92, v93 op_sel:[0,0,1]
	v_cvt_pk_fp8_f32 v169, v96, v97 op_sel:[0,0,1]
	s_waitcnt vmcnt(0) lgkmcnt(0)
	s_barrier
	ds_read_b128 v[82:85], v194 offset:0
	ds_read_b128 v[86:89], v195 offset:0
	ds_read_b128 v[90:93], v194 offset:0x800
	ds_read_b128 v[94:97], v195 offset:0x800
	s_nop 1
	v_mfma_f32_16x16x128_f8f6f4 v[18:21], v[162:169], v[146:153], v[18:21]
	ds_read_b128 v[98:101], v194 offset:0x1000
	ds_read_b128 v[102:105], v195 offset:0x1000
	s_waitcnt lgkmcnt(4)
	v_mfma_f32_32x32x64_f8f6f4 v[2:17], v[162:169], v[82:89], v[2:17]
	s_waitcnt lgkmcnt(2)
	v_mfma_f32_32x32x64_f8f6f4 v[34:49], v[162:169], v[90:97], v[34:49]
	s_nop 7
	s_nop 7
	ds_read_b128 v[82:85], v194 offset:0x1800
	ds_read_b128 v[86:89], v195 offset:0x1800
	s_waitcnt lgkmcnt(2)
	v_mfma_f32_32x32x64_f8f6f4 v[50:65], v[162:169], v[98:105], v[50:65]
	s_waitcnt lgkmcnt(0)
	v_mfma_f32_32x32x64_f8f6f4 v[66:81], v[162:169], v[82:89], v[66:81]
.LBB0_1202:
	s_mov_b32 s98, 0x30003
	s_mov_b32 s99, 0x30003
	s_nop 15
	s_mov_b64 s[100:101], exec
	s_mov_b64 exec, s[98:99]
	ds_write_b128 v250, v[18:21] offset:49152
	s_mov_b64 exec, s[100:101]
	v_add_u32_e32 v249, s78, v186
	s_waitcnt lgkmcnt(0)
	ds_read_b128 v[30:33], v249 offset:49248
	ds_read_b128 v[26:29], v249 offset:49216
	ds_read_b128 v[22:25], v249 offset:49184
	ds_read_b128 v[18:21], v249 offset:49152
	s_waitcnt lgkmcnt(0)
	v_rcp_f32_e32 v18, v18
	v_rcp_f32_e32 v19, v19
	v_mov_b32_e32 v92, v179
	s_waitcnt vmcnt(0) lgkmcnt(0)
	s_barrier
	v_mul_f32_e32 v2, v2, v18
	v_mul_f32_e32 v34, v34, v18
	v_mul_f32_e32 v50, v50, v18
	v_mul_f32_e32 v82, v66, v18
	v_mul_f32_e32 v18, v3, v19
	v_rcp_f32_e32 v3, v20
	v_mul_f32_e32 v35, v35, v19
	v_mul_f32_e32 v83, v51, v19
	v_mul_f32_e32 v19, v67, v19
	v_mul_f32_e32 v20, v4, v3
	v_rcp_f32_e32 v4, v21
	v_mul_f32_e32 v21, v36, v3
	v_mul_f32_e32 v52, v52, v3
	v_mul_f32_e32 v67, v68, v3
	v_rcp_f32_e32 v3, v22
	v_mul_f32_e32 v36, v5, v4
	v_mul_f32_e32 v22, v37, v4
	v_mul_f32_e32 v84, v53, v4
	v_mul_f32_e32 v85, v69, v4
	v_rcp_f32_e32 v4, v23
	v_mul_f32_e32 v37, v6, v3
	v_mul_f32_e32 v23, v38, v3
	v_mul_f32_e32 v38, v54, v3
	v_mul_f32_e32 v70, v70, v3
	v_rcp_f32_e32 v3, v24
	v_mul_f32_e32 v51, v7, v4
	v_mul_f32_e32 v39, v39, v4
	v_mul_f32_e32 v54, v55, v4
	v_mul_f32_e32 v55, v71, v4
	v_rcp_f32_e32 v4, v25
	v_mul_f32_e32 v8, v8, v3
	v_mul_f32_e32 v25, v40, v3
	v_mul_f32_e32 v40, v56, v3
	v_mul_f32_e32 v72, v72, v3
	v_rcp_f32_e32 v3, v26
	v_mul_f32_e32 v9, v9, v4
	v_mul_f32_e32 v26, v41, v4
	v_mul_f32_e32 v57, v57, v4
	v_mul_f32_e32 v86, v73, v4
	v_rcp_f32_e32 v4, v27
	v_mul_f32_e32 v10, v10, v3
	v_mul_f32_e32 v27, v42, v3
	v_mul_f32_e32 v87, v58, v3
	v_mul_f32_e32 v88, v74, v3
	v_rcp_f32_e32 v3, v28
	v_mul_f32_e32 v11, v11, v4
	v_mul_f32_e32 v43, v43, v4
	v_mul_f32_e32 v74, v59, v4
	v_mul_f32_e32 v75, v75, v4
	v_rcp_f32_e32 v4, v29
	v_mul_f32_e32 v12, v12, v3
	v_mul_f32_e32 v44, v44, v3
	v_mul_f32_e32 v60, v60, v3
	v_mul_f32_e32 v89, v76, v3
	v_rcp_f32_e32 v3, v30
	v_mul_f32_e32 v13, v13, v4
	v_mul_f32_e32 v30, v45, v4
	v_mul_f32_e32 v45, v61, v4
	v_mul_f32_e32 v77, v77, v4
	v_rcp_f32_e32 v4, v31
	v_mul_f32_e32 v14, v14, v3
	v_mul_f32_e32 v31, v46, v3
	v_mul_f32_e32 v62, v62, v3
	v_mul_f32_e32 v78, v78, v3
	v_rcp_f32_e32 v3, v32
	v_mul_f32_e32 v15, v15, v4
	v_mul_f32_e32 v32, v47, v4
	v_mul_f32_e32 v90, v63, v4
	v_mul_f32_e32 v79, v79, v4
	ds_read2st64_b32 v[4:5], v92 offset1:8
	v_mul_f32_e32 v29, v16, v3
	v_mul_f32_e32 v48, v48, v3
	v_mul_f32_e32 v91, v64, v3
	v_mul_f32_e32 v80, v80, v3
	v_rcp_f32_e32 v3, v33
	ds_read2st64_b32 v[6:7], v92 offset0:16 offset1:24
	v_mul_f32_e32 v17, v17, v3
	v_mul_f32_e32 v33, v49, v3
	v_mul_f32_e32 v65, v65, v3
	v_mul_f32_e32 v81, v81, v3
	s_waitcnt lgkmcnt(0)
	v_lshlrev_b32_e32 v3, 16, v4
	v_fma_f32 v3, -v1, v2, v3
	v_and_b32_e32 v2, 0xffff0000, v4
	v_fma_f32 v68, -v1, v18, v2
	v_lshlrev_b32_e32 v2, 16, v5
	v_fma_f32 v63, -v1, v20, v2
	v_and_b32_e32 v2, 0xffff0000, v5
	ds_read2st64_b32 v[4:5], v92 offset0:32 offset1:40
	v_fma_f32 v58, -v1, v36, v2
	v_lshlrev_b32_e32 v2, 16, v6
	v_fma_f32 v53, -v1, v37, v2
	v_and_b32_e32 v2, 0xffff0000, v6
	v_fma_f32 v47, -v1, v51, v2
	v_lshlrev_b32_e32 v2, 16, v7
	v_fma_f32 v42, -v1, v8, v2
	v_and_b32_e32 v2, 0xffff0000, v7
	v_fma_f32 v36, -v1, v9, v2
	s_waitcnt lgkmcnt(0)
	v_lshlrev_b32_e32 v2, 16, v4
	v_fma_f32 v28, -v1, v10, v2
	v_and_b32_e32 v2, 0xffff0000, v4
	v_fma_f32 v24, -v1, v11, v2
	ds_read2st64_b32 v[10:11], v92 offset0:48 offset1:56
	v_lshlrev_b32_e32 v2, 16, v5
	v_fma_f32 v20, -v1, v12, v2
	v_and_b32_e32 v2, 0xffff0000, v5
	ds_read2st64_b32 v[4:5], v92 offset0:64 offset1:72
	v_fma_f32 v16, -v1, v13, v2
	s_waitcnt lgkmcnt(0)
	v_lshlrev_b32_e32 v2, 16, v10
	v_fma_f32 v12, -v1, v14, v2
	v_and_b32_e32 v2, 0xffff0000, v10
	v_fma_f32 v9, -v1, v15, v2
	v_lshlrev_b32_e32 v2, 16, v11
	v_fma_f32 v7, -v1, v29, v2
	v_and_b32_e32 v2, 0xffff0000, v11
	v_fma_f32 v6, -v1, v17, v2
	v_lshlrev_b32_e32 v2, 16, v4
	v_fma_f32 v76, -v1, v34, v2
	v_and_b32_e32 v2, 0xffff0000, v4
	v_lshlrev_b32_e32 v4, 16, v5
	v_fma_f32 v66, -v1, v21, v4
	v_and_b32_e32 v4, 0xffff0000, v5
	v_fma_f32 v61, -v1, v22, v4
	ds_read2st64_b32 v[4:5], v92 offset0:80 offset1:88
	ds_read2st64_b32 v[14:15], v92 offset0:144 offset1:152
	v_fma_f32 v71, -v1, v35, v2
	v_mul_f32_e32 v2, v76, v76
	v_fmac_f32_e32 v2, v3, v3
	s_waitcnt lgkmcnt(0)
	v_lshlrev_b32_e32 v8, 16, v4
	v_and_b32_e32 v4, 0xffff0000, v4
	v_fma_f32 v51, -v1, v39, v4
	v_lshlrev_b32_e32 v4, 16, v5
	v_fma_f32 v46, -v1, v25, v4
	v_and_b32_e32 v4, 0xffff0000, v5
	v_fma_f32 v41, -v1, v26, v4
	ds_read2st64_b32 v[4:5], v92 offset0:96 offset1:104
	v_fma_f32 v56, -v1, v23, v8
	v_mul_f32_e32 v34, v71, v71
	v_fmac_f32_e32 v34, v68, v68
	v_mul_f32_e32 v93, v66, v66
	s_waitcnt lgkmcnt(0)
	v_lshlrev_b32_e32 v8, 16, v4
	v_and_b32_e32 v4, 0xffff0000, v4
	v_fma_f32 v29, -v1, v43, v4
	v_lshlrev_b32_e32 v4, 16, v5
	v_fma_f32 v25, -v1, v44, v4
	v_and_b32_e32 v4, 0xffff0000, v5
	v_fma_f32 v21, -v1, v30, v4
	ds_read2st64_b32 v[4:5], v92 offset0:112 offset1:120
	v_fma_f32 v37, -v1, v27, v8
	v_fmac_f32_e32 v93, v63, v63
	v_mul_f32_e32 v94, v61, v61
	v_fmac_f32_e32 v94, v58, v58
	s_waitcnt lgkmcnt(0)
	v_lshlrev_b32_e32 v8, 16, v4
	v_and_b32_e32 v4, 0xffff0000, v4
	v_fma_f32 v13, -v1, v32, v4
	v_lshlrev_b32_e32 v4, 16, v5
	v_fma_f32 v10, -v1, v48, v4
	v_and_b32_e32 v4, 0xffff0000, v5
	v_fma_f32 v17, -v1, v31, v8
	v_fma_f32 v8, -v1, v33, v4
	ds_read2st64_b32 v[4:5], v92 offset0:128 offset1:136
	ds_read2st64_b32 v[30:31], v92 offset0:208 offset1:216
	v_mul_f32_e32 v95, v56, v56
	v_fmac_f32_e32 v95, v53, v53
	v_mul_f32_e32 v96, v51, v51
	s_waitcnt lgkmcnt(0)
	v_lshlrev_b32_e32 v11, 16, v4
	v_and_b32_e32 v4, 0xffff0000, v4
	v_fma_f32 v83, -v1, v83, v4
	v_lshlrev_b32_e32 v4, 16, v5
	v_fma_f32 v73, -v1, v52, v4
	v_and_b32_e32 v4, 0xffff0000, v5
	v_fma_f32 v69, -v1, v84, v4
	v_lshlrev_b32_e32 v4, 16, v14
	v_fma_f32 v64, -v1, v38, v4
	v_and_b32_e32 v4, 0xffff0000, v14
	v_fma_f32 v59, -v1, v54, v4
	v_lshlrev_b32_e32 v4, 16, v15
	v_fma_f32 v54, -v1, v40, v4
	ds_read2st64_b32 v[4:5], v92 offset0:160 offset1:168
	v_fma_f32 v105, -v1, v50, v11
	v_and_b32_e32 v11, 0xffff0000, v15
	ds_read2st64_b32 v[14:15], v92 offset0:176 offset1:184
	v_fma_f32 v49, -v1, v57, v11
	s_waitcnt lgkmcnt(0)
	v_lshlrev_b32_e32 v11, 16, v4
	v_and_b32_e32 v4, 0xffff0000, v4
	v_fma_f32 v39, -v1, v74, v4
	v_lshlrev_b32_e32 v4, 16, v5
	v_fma_f32 v33, -v1, v60, v4
	v_and_b32_e32 v4, 0xffff0000, v5
	v_fma_f32 v26, -v1, v45, v4
	v_lshlrev_b32_e32 v4, 16, v14
	v_fma_f32 v22, -v1, v62, v4
	v_and_b32_e32 v4, 0xffff0000, v14
	v_fma_f32 v18, -v1, v90, v4
	v_lshlrev_b32_e32 v4, 16, v15
	v_fma_f32 v14, -v1, v91, v4
	ds_read2st64_b32 v[4:5], v92 offset0:192 offset1:200
	v_fma_f32 v44, -v1, v87, v11
	v_and_b32_e32 v11, 0xffff0000, v15
	v_fma_f32 v11, -v1, v65, v11
	v_fmac_f32_e32 v2, v105, v105
	s_waitcnt lgkmcnt(0)
	v_lshlrev_b32_e32 v15, 16, v4
	v_and_b32_e32 v4, 0xffff0000, v4
	v_fma_f32 v84, -v1, v19, v4
	v_lshlrev_b32_e32 v4, 16, v5
	v_fma_f32 v87, -v1, v67, v4
	v_and_b32_e32 v4, 0xffff0000, v5
	v_fma_f32 v74, -v1, v85, v4
	v_lshlrev_b32_e32 v4, 16, v30
	v_fma_f32 v70, -v1, v70, v4
	v_and_b32_e32 v4, 0xffff0000, v30
	v_fma_f32 v65, -v1, v55, v4
	v_lshlrev_b32_e32 v4, 16, v31
	v_fma_f32 v60, -v1, v72, v4
	ds_read2st64_b32 v[4:5], v92 offset0:224 offset1:232
	v_fma_f32 v82, -v1, v82, v15
	v_and_b32_e32 v15, 0xffff0000, v31
	ds_read2st64_b32 v[30:31], v92 offset0:240 offset1:248
	v_fma_f32 v55, -v1, v86, v15
	s_waitcnt lgkmcnt(0)
	v_lshlrev_b32_e32 v15, 16, v4
	v_and_b32_e32 v4, 0xffff0000, v4
	v_fma_f32 v45, -v1, v75, v4
	v_lshlrev_b32_e32 v4, 16, v5
	v_fmac_f32_e32 v2, v82, v82
	v_fma_f32 v40, -v1, v89, v4
	v_and_b32_e32 v4, 0xffff0000, v5
	v_fma_f32 v35, -v1, v77, v4
	v_lshlrev_b32_e32 v4, 16, v30
	v_add_f32_dpp v2, v2, v2 quad_perm:[1,0,3,2] row_mask:0xf bank_mask:0xf bound_ctrl:1
	v_fma_f32 v27, -v1, v78, v4
	v_and_b32_e32 v4, 0xffff0000, v30
	v_add_f32_dpp v2, v2, v2 quad_perm:[2,3,0,1] row_mask:0xf bank_mask:0xf bound_ctrl:1
	v_fma_f32 v23, -v1, v79, v4
	v_lshlrev_b32_e32 v4, 16, v31
	v_add_f32_dpp v2, v2, v2 row_half_mirror row_mask:0xf bank_mask:0xf bound_ctrl:1
	v_fma_f32 v19, -v1, v80, v4
	v_and_b32_e32 v4, 0xffff0000, v31
	v_add_f32_dpp v2, v2, v2 row_mirror row_mask:0xf bank_mask:0xf bound_ctrl:1
	v_fmac_f32_e32 v34, v83, v83
	v_fma_f32 v50, -v1, v88, v15
	v_fma_f32 v15, -v1, v81, v4
	v_mov_b32_e32 v4, v2
	v_fmac_f32_e32 v34, v84, v84
	s_nop 0
	v_permlane16_swap_b32_e32 v2, v4
	v_add_f32_e32 v2, v2, v4
	s_nop 0
	v_add_f32_dpp v4, v34, v34 quad_perm:[1,0,3,2] row_mask:0xf bank_mask:0xf bound_ctrl:1
	v_fmac_f32_e32 v93, v73, v73
	v_fmac_f32_e32 v93, v87, v87
	v_add_f32_dpp v4, v4, v4 quad_perm:[2,3,0,1] row_mask:0xf bank_mask:0xf bound_ctrl:1
	v_fmac_f32_e32 v94, v69, v69
	v_fmac_f32_e32 v94, v74, v74
	v_add_f32_dpp v4, v4, v4 row_half_mirror row_mask:0xf bank_mask:0xf bound_ctrl:1
	v_fmac_f32_e32 v95, v64, v64
	v_fmac_f32_e32 v95, v70, v70
	v_add_f32_dpp v4, v4, v4 row_mirror row_mask:0xf bank_mask:0xf bound_ctrl:1
	v_mov_b32_e32 v5, v4
	s_nop 1
	v_permlane16_swap_b32_e32 v4, v5
	v_add_f32_e32 v77, v4, v5
	s_nop 0
	v_add_f32_dpp v4, v93, v93 quad_perm:[1,0,3,2] row_mask:0xf bank_mask:0xf bound_ctrl:1
	v_fmac_f32_e32 v96, v47, v47
	v_fmac_f32_e32 v96, v59, v59
	v_add_f32_dpp v4, v4, v4 quad_perm:[2,3,0,1] row_mask:0xf bank_mask:0xf bound_ctrl:1
	v_fmac_f32_e32 v96, v65, v65
	v_mul_f32_e32 v97, v46, v46
	v_add_f32_dpp v4, v4, v4 row_half_mirror row_mask:0xf bank_mask:0xf bound_ctrl:1
	v_fmac_f32_e32 v97, v42, v42
	v_fmac_f32_e32 v97, v54, v54
	v_add_f32_dpp v4, v4, v4 row_mirror row_mask:0xf bank_mask:0xf bound_ctrl:1
	v_mov_b32_e32 v5, v4
	s_nop 1
	v_permlane16_swap_b32_e32 v4, v5
	v_add_f32_e32 v80, v4, v5
	s_nop 0
	v_add_f32_dpp v4, v94, v94 quad_perm:[1,0,3,2] row_mask:0xf bank_mask:0xf bound_ctrl:1
	v_fmac_f32_e32 v97, v60, v60
	v_mul_f32_e32 v98, v41, v41
	v_add_f32_dpp v4, v4, v4 quad_perm:[2,3,0,1] row_mask:0xf bank_mask:0xf bound_ctrl:1
	v_fmac_f32_e32 v98, v36, v36
	v_fmac_f32_e32 v98, v49, v49
	v_add_f32_dpp v4, v4, v4 row_half_mirror row_mask:0xf bank_mask:0xf bound_ctrl:1
	v_fmac_f32_e32 v98, v55, v55
	v_mul_f32_e32 v43, v37, v37
	v_add_f32_dpp v4, v4, v4 row_mirror row_mask:0xf bank_mask:0xf bound_ctrl:1
	v_mov_b32_e32 v5, v4
	s_nop 1
	v_permlane16_swap_b32_e32 v4, v5
	v_add_f32_e32 v81, v4, v5
	s_nop 0
	v_add_f32_dpp v4, v95, v95 quad_perm:[1,0,3,2] row_mask:0xf bank_mask:0xf bound_ctrl:1
	v_fmac_f32_e32 v43, v28, v28
	v_fmac_f32_e32 v43, v44, v44
	v_add_f32_dpp v4, v4, v4 quad_perm:[2,3,0,1] row_mask:0xf bank_mask:0xf bound_ctrl:1
	v_fmac_f32_e32 v43, v50, v50
	v_mul_f32_e32 v99, v29, v29
	v_add_f32_dpp v4, v4, v4 row_half_mirror row_mask:0xf bank_mask:0xf bound_ctrl:1
	v_fmac_f32_e32 v99, v24, v24
	v_fmac_f32_e32 v99, v39, v39
	v_add_f32_dpp v4, v4, v4 row_mirror row_mask:0xf bank_mask:0xf bound_ctrl:1
	v_mov_b32_e32 v5, v4
	s_nop 1
	v_permlane16_swap_b32_e32 v4, v5
	v_add_f32_e32 v85, v4, v5
	s_nop 0
	v_add_f32_dpp v4, v96, v96 quad_perm:[1,0,3,2] row_mask:0xf bank_mask:0xf bound_ctrl:1
	v_fmac_f32_e32 v99, v45, v45
	v_mul_f32_e32 v100, v25, v25
	v_add_f32_dpp v4, v4, v4 quad_perm:[2,3,0,1] row_mask:0xf bank_mask:0xf bound_ctrl:1
	v_fmac_f32_e32 v100, v20, v20
	v_fmac_f32_e32 v100, v33, v33
	v_add_f32_dpp v4, v4, v4 row_half_mirror row_mask:0xf bank_mask:0xf bound_ctrl:1
	v_fmac_f32_e32 v100, v40, v40
	v_mul_f32_e32 v101, v21, v21
	v_add_f32_dpp v4, v4, v4 row_mirror row_mask:0xf bank_mask:0xf bound_ctrl:1
	v_mov_b32_e32 v5, v4
	s_nop 1
	v_permlane16_swap_b32_e32 v4, v5
	v_add_f32_e32 v86, v4, v5
	v_mov_b32_e32 v5, v178
	s_load_dwordx2 s[6:7], s[10:11], 0x98
	v_and_b32_e32 v180, 31, v5
	v_lshlrev_b32_e32 v30, 2, v180
	s_waitcnt lgkmcnt(0)
	global_load_dword v31, v30, s[6:7]
	global_load_dword v78, v30, s[6:7] offset:128
	global_load_dword v79, v30, s[6:7] offset:256
	s_nop 0
	global_load_dword v30, v30, s[6:7] offset:384
	v_add_f32_dpp v4, v97, v97 quad_perm:[1,0,3,2] row_mask:0xf bank_mask:0xf bound_ctrl:1
	v_fmac_f32_e32 v101, v16, v16
	v_fmac_f32_e32 v101, v26, v26
	v_add_f32_dpp v4, v4, v4 quad_perm:[2,3,0,1] row_mask:0xf bank_mask:0xf bound_ctrl:1
	v_fmac_f32_e32 v101, v35, v35
	v_mul_f32_e32 v32, v17, v17
	v_add_f32_dpp v4, v4, v4 row_half_mirror row_mask:0xf bank_mask:0xf bound_ctrl:1
	v_fmac_f32_e32 v32, v12, v12
	v_fmac_f32_e32 v32, v22, v22
	v_add_f32_dpp v4, v4, v4 row_mirror row_mask:0xf bank_mask:0xf bound_ctrl:1
	v_mov_b32_e32 v34, v4
	s_nop 1
	v_permlane16_swap_b32_e32 v4, v34
	v_add_f32_e32 v88, v4, v34
	s_nop 0
	v_add_f32_dpp v4, v98, v98 quad_perm:[1,0,3,2] row_mask:0xf bank_mask:0xf bound_ctrl:1
	v_fmac_f32_e32 v32, v27, v27
	v_mul_f32_e32 v102, v13, v13
	v_add_f32_dpp v4, v4, v4 quad_perm:[2,3,0,1] row_mask:0xf bank_mask:0xf bound_ctrl:1
	v_fmac_f32_e32 v102, v9, v9
	v_fmac_f32_e32 v102, v18, v18
	v_add_f32_dpp v4, v4, v4 row_half_mirror row_mask:0xf bank_mask:0xf bound_ctrl:1
	v_fmac_f32_e32 v102, v23, v23
	v_mul_f32_e32 v103, v10, v10
	v_add_f32_dpp v4, v4, v4 row_mirror row_mask:0xf bank_mask:0xf bound_ctrl:1
	v_mov_b32_e32 v34, v4
	s_nop 1
	v_permlane16_swap_b32_e32 v4, v34
	v_add_f32_e32 v75, v4, v34
	s_nop 0
	v_add_f32_dpp v4, v43, v43 quad_perm:[1,0,3,2] row_mask:0xf bank_mask:0xf bound_ctrl:1
	v_fmac_f32_e32 v103, v7, v7
	v_fmac_f32_e32 v103, v14, v14
	v_add_f32_dpp v4, v4, v4 quad_perm:[2,3,0,1] row_mask:0xf bank_mask:0xf bound_ctrl:1
	v_fmac_f32_e32 v103, v19, v19
	v_mul_f32_e32 v104, v8, v8
	v_add_f32_dpp v4, v4, v4 row_half_mirror row_mask:0xf bank_mask:0xf bound_ctrl:1
	v_fmac_f32_e32 v104, v6, v6
	v_fmac_f32_e32 v104, v11, v11
	v_add_f32_dpp v4, v4, v4 row_mirror row_mask:0xf bank_mask:0xf bound_ctrl:1
	v_mov_b32_e32 v34, v4
	s_nop 1
	v_permlane16_swap_b32_e32 v4, v34
	v_add_f32_e32 v72, v4, v34
	s_nop 0
	v_add_f32_dpp v4, v99, v99 quad_perm:[1,0,3,2] row_mask:0xf bank_mask:0xf bound_ctrl:1
	v_fmac_f32_e32 v104, v15, v15
	v_fmamk_f32 v2, v2, 0x3c000000, v184
	v_add_f32_dpp v4, v4, v4 quad_perm:[2,3,0,1] row_mask:0xf bank_mask:0xf bound_ctrl:1
	v_cmp_gt_f32_e32 vcc, s55, v2
	v_fmamk_f32 v77, v77, 0x3c000000, v184
	v_add_f32_dpp v4, v4, v4 row_half_mirror row_mask:0xf bank_mask:0xf bound_ctrl:1
	s_waitcnt vmcnt(0)
	v_mul_f32_e32 v30, 0x3f24fd5c, v30
	v_add_f32_dpp v4, v4, v4 row_mirror row_mask:0xf bank_mask:0xf bound_ctrl:1
	v_mov_b32_e32 v34, v4
	s_nop 1
	v_permlane16_swap_b32_e32 v4, v34
	v_add_f32_e32 v67, v4, v34
	s_nop 0
	v_add_f32_dpp v4, v100, v100 quad_perm:[1,0,3,2] row_mask:0xf bank_mask:0xf bound_ctrl:1
	s_nop 1
	v_add_f32_dpp v4, v4, v4 quad_perm:[2,3,0,1] row_mask:0xf bank_mask:0xf bound_ctrl:1
	s_nop 1
	v_add_f32_dpp v4, v4, v4 row_half_mirror row_mask:0xf bank_mask:0xf bound_ctrl:1
	s_nop 1
	v_add_f32_dpp v4, v4, v4 row_mirror row_mask:0xf bank_mask:0xf bound_ctrl:1
	v_mov_b32_e32 v34, v4
	s_nop 1
	v_permlane16_swap_b32_e32 v4, v34
	v_add_f32_e32 v62, v4, v34
	s_nop 0
	v_add_f32_dpp v4, v101, v101 quad_perm:[1,0,3,2] row_mask:0xf bank_mask:0xf bound_ctrl:1
	s_nop 1
	v_add_f32_dpp v4, v4, v4 quad_perm:[2,3,0,1] row_mask:0xf bank_mask:0xf bound_ctrl:1
	s_nop 1
	v_add_f32_dpp v4, v4, v4 row_half_mirror row_mask:0xf bank_mask:0xf bound_ctrl:1
	s_nop 1
	v_add_f32_dpp v4, v4, v4 row_mirror row_mask:0xf bank_mask:0xf bound_ctrl:1
	v_mov_b32_e32 v34, v4
	s_nop 1
	v_permlane16_swap_b32_e32 v4, v34
	v_add_f32_e32 v57, v4, v34
	s_nop 0
	v_add_f32_dpp v4, v32, v32 quad_perm:[1,0,3,2] row_mask:0xf bank_mask:0xf bound_ctrl:1
	v_mul_f32_e32 v34, 0x3f24fd5c, v31
	v_mul_f32_e32 v31, 0x3f24fd5c, v79
	v_add_f32_dpp v4, v4, v4 quad_perm:[2,3,0,1] row_mask:0xf bank_mask:0xf bound_ctrl:1
	s_nop 1
	v_add_f32_dpp v4, v4, v4 row_half_mirror row_mask:0xf bank_mask:0xf bound_ctrl:1
	s_nop 1
	v_add_f32_dpp v4, v4, v4 row_mirror row_mask:0xf bank_mask:0xf bound_ctrl:1
	v_mov_b32_e32 v32, v4
	s_nop 1
	v_permlane16_swap_b32_e32 v4, v32
	v_add_f32_e32 v52, v4, v32
	s_nop 0
	v_add_f32_dpp v4, v102, v102 quad_perm:[1,0,3,2] row_mask:0xf bank_mask:0xf bound_ctrl:1
	s_nop 1
	v_add_f32_dpp v4, v4, v4 quad_perm:[2,3,0,1] row_mask:0xf bank_mask:0xf bound_ctrl:1
	s_nop 1
	v_add_f32_dpp v4, v4, v4 row_half_mirror row_mask:0xf bank_mask:0xf bound_ctrl:1
	s_nop 1
	v_add_f32_dpp v4, v4, v4 row_mirror row_mask:0xf bank_mask:0xf bound_ctrl:1
	v_mov_b32_e32 v32, v4
	s_nop 1
	v_permlane16_swap_b32_e32 v4, v32
	v_add_f32_e32 v48, v4, v32
	s_nop 0
	v_add_f32_dpp v4, v103, v103 quad_perm:[1,0,3,2] row_mask:0xf bank_mask:0xf bound_ctrl:1
	s_nop 1
	v_add_f32_dpp v4, v4, v4 quad_perm:[2,3,0,1] row_mask:0xf bank_mask:0xf bound_ctrl:1
	s_nop 1
	v_add_f32_dpp v4, v4, v4 row_half_mirror row_mask:0xf bank_mask:0xf bound_ctrl:1
	s_nop 1
	v_add_f32_dpp v4, v4, v4 row_mirror row_mask:0xf bank_mask:0xf bound_ctrl:1
	v_mov_b32_e32 v32, v4
	s_nop 1
	v_permlane16_swap_b32_e32 v4, v32
	v_add_f32_e32 v43, v4, v32
	s_nop 0
	v_add_f32_dpp v4, v104, v104 quad_perm:[1,0,3,2] row_mask:0xf bank_mask:0xf bound_ctrl:1
	s_nop 1
	v_add_f32_dpp v4, v4, v4 quad_perm:[2,3,0,1] row_mask:0xf bank_mask:0xf bound_ctrl:1
	s_nop 1
	v_add_f32_dpp v4, v4, v4 row_half_mirror row_mask:0xf bank_mask:0xf bound_ctrl:1
	s_nop 1
	v_add_f32_dpp v4, v4, v4 row_mirror row_mask:0xf bank_mask:0xf bound_ctrl:1
	v_mov_b32_e32 v32, v4
	s_nop 1
	v_permlane16_swap_b32_e32 v4, v32
	v_add_f32_e32 v38, v4, v32
	v_mul_f32_e32 v4, 0x4f800000, v2
	v_cndmask_b32_e32 v4, v2, v4, vcc
	v_mul_f32_e32 v32, 0x3f24fd5c, v78
	v_sqrt_f32_e32 v78, v4
	v_ashrrev_i32_e32 v2, 3, v5
	v_and_b32_e32 v2, -4, v2
	v_add_u32_e32 v2, s86, v2
	v_add_u32_e32 v5, -1, v78
	v_fma_f32 v79, -v5, v78, v4
	v_cmp_ge_f32_e64 s[6:7], 0, v79
	v_add_u32_e32 v79, 1, v78
	s_nop 0
	v_cndmask_b32_e64 v5, v78, v5, s[6:7]
	v_fma_f32 v78, -v79, v78, v4
	v_cmp_lt_f32_e64 s[6:7], 0, v78
	s_nop 1
	v_cndmask_b32_e64 v5, v5, v79, s[6:7]
	v_mul_f32_e32 v78, 0x37800000, v5
	v_cndmask_b32_e32 v5, v5, v78, vcc
	v_cmp_class_f32_e32 vcc, v4, v185
	s_nop 1
	v_cndmask_b32_e32 v78, v5, v4, vcc
	v_div_scale_f32 v79, s[6:7], v78, v78, 1.0
	v_rcp_f32_e32 v89, v79
	s_add_u32 s6, s27, s87
	s_addc_u32 s7, s23, s76
	v_lshl_add_u64 v[4:5], s[6:7], 0, v[180:181]
	v_fma_f32 v90, -v79, v89, 1.0
	v_fmac_f32_e32 v89, v90, v89
	v_div_scale_f32 v90, vcc, 1.0, v78, 1.0
	v_mul_f32_e32 v91, v90, v89
	v_fma_f32 v92, -v79, v91, v90
	v_fmac_f32_e32 v91, v92, v89
	v_fma_f32 v79, -v79, v91, v90
	v_div_fmas_f32 v79, v79, v89, v91
	v_div_fixup_f32 v89, v79, v78, 1.0
	v_mul_f32_e32 v3, v3, v89
	v_mul_f32_e32 v3, v3, v34
	v_mov_b32_e32 v90, v181
	v_cvt_pk_fp8_f32 v90, v3, 0
	v_ashrrev_i32_e32 v3, 31, v2
	v_lshlrev_b64 v[78:79], 10, v[2:3]
	v_mul_f32_e32 v3, v76, v89
	v_mul_f32_e32 v3, v3, v32
	v_mov_b32_e32 v76, v181
	v_lshl_add_u64 v[78:79], v[4:5], 0, v[78:79]
	v_cvt_pk_fp8_f32 v76, v3, 0
	v_mul_f32_e32 v3, v105, v89
	global_store_byte v[78:79], v90, off
	v_mul_f32_e32 v3, v3, v31
	v_mov_b32_e32 v90, v181
	v_cvt_pk_fp8_f32 v90, v3, 0
	v_mul_f32_e32 v3, v82, v89
	v_mul_f32_e32 v82, 0x4f800000, v77
	v_cmp_gt_f32_e32 vcc, s55, v77
	v_mul_f32_e32 v3, v3, v30
	v_mov_b32_e32 v89, v181
	v_cndmask_b32_e32 v77, v77, v82, vcc
	v_sqrt_f32_e32 v82, v77
	v_cvt_pk_fp8_f32 v89, v3, 0
	global_store_byte v[78:79], v76, off offset:32
	global_store_byte v[78:79], v90, off offset:64
	global_store_byte v[78:79], v89, off offset:96
	v_add_u32_e32 v3, -1, v82
	v_fma_f32 v91, -v3, v82, v77
	v_cmp_ge_f32_e64 s[6:7], 0, v91
	v_add_u32_e32 v91, 1, v82
	s_add_i32 s53, s53, s18
	v_cndmask_b32_e64 v3, v82, v3, s[6:7]
	v_fma_f32 v82, -v91, v82, v77
	v_cmp_lt_f32_e64 s[6:7], 0, v82
	s_cmp_lt_i32 s53, s35
	s_nop 0
	v_cndmask_b32_e64 v3, v3, v91, s[6:7]
	v_mul_f32_e32 v82, 0x37800000, v3
	v_cndmask_b32_e32 v3, v3, v82, vcc
	v_cmp_class_f32_e32 vcc, v77, v185
	s_nop 1
	v_cndmask_b32_e32 v3, v3, v77, vcc
	v_div_scale_f32 v77, s[6:7], v3, v3, 1.0
	v_rcp_f32_e32 v82, v77
	s_nop 0
	v_fma_f32 v76, -v77, v82, 1.0
	v_fmac_f32_e32 v82, v76, v82
	v_div_scale_f32 v76, vcc, 1.0, v3, 1.0
	v_mul_f32_e32 v78, v76, v82
	v_fma_f32 v79, -v77, v78, v76
	v_fmac_f32_e32 v78, v79, v82
	v_fma_f32 v76, -v77, v78, v76
	v_div_fmas_f32 v76, v76, v82, v78
	v_div_fixup_f32 v3, v76, v3, 1.0
	v_mul_f32_e32 v68, v68, v3
	v_mul_f32_e32 v68, v68, v34
	v_mov_b32_e32 v78, v181
	v_or_b32_e32 v76, 1, v2
	v_cvt_pk_fp8_f32 v78, v68, 0
	v_ashrrev_i32_e32 v77, 31, v76
	v_mul_f32_e32 v68, v71, v3
	v_lshlrev_b64 v[76:77], 10, v[76:77]
	v_mul_f32_e32 v68, v68, v32
	v_mov_b32_e32 v71, v181
	v_lshl_add_u64 v[76:77], v[4:5], 0, v[76:77]
	v_cvt_pk_fp8_f32 v71, v68, 0
	v_mul_f32_e32 v68, v83, v3
	global_store_byte v[76:77], v78, off
	v_mul_f32_e32 v68, v68, v31
	v_mov_b32_e32 v78, v181
	v_cvt_pk_fp8_f32 v78, v68, 0
	v_fmamk_f32 v68, v80, 0x3c000000, v184
	v_mul_f32_e32 v79, 0x4f800000, v68
	v_cmp_gt_f32_e32 vcc, s55, v68
	v_mul_f32_e32 v3, v84, v3
	v_mul_f32_e32 v3, v3, v30
	v_cndmask_b32_e32 v68, v68, v79, vcc
	v_sqrt_f32_e32 v79, v68
	v_mov_b32_e32 v80, v181
	v_cvt_pk_fp8_f32 v80, v3, 0
	global_store_byte v[76:77], v71, off offset:32
	global_store_byte v[76:77], v78, off offset:64
	global_store_byte v[76:77], v80, off offset:96
	v_add_u32_e32 v3, -1, v79
	v_fma_f32 v82, -v3, v79, v68
	v_cmp_ge_f32_e64 s[6:7], 0, v82
	v_add_u32_e32 v82, 1, v79
	s_nop 0
	v_cndmask_b32_e64 v3, v79, v3, s[6:7]
	v_fma_f32 v79, -v82, v79, v68
	v_cmp_lt_f32_e64 s[6:7], 0, v79
	s_nop 1
	v_cndmask_b32_e64 v3, v3, v82, s[6:7]
	v_mul_f32_e32 v79, 0x37800000, v3
	v_cndmask_b32_e32 v3, v3, v79, vcc
	v_cmp_class_f32_e32 vcc, v68, v185
	s_nop 1
	v_cndmask_b32_e32 v3, v3, v68, vcc
	v_div_scale_f32 v68, s[6:7], v3, v3, 1.0
	v_rcp_f32_e32 v79, v68
	s_nop 0
	v_fma_f32 v71, -v68, v79, 1.0
	v_fmac_f32_e32 v79, v71, v79
	v_div_scale_f32 v71, vcc, 1.0, v3, 1.0
	v_mul_f32_e32 v76, v71, v79
	v_fma_f32 v77, -v68, v76, v71
	v_fmac_f32_e32 v76, v77, v79
	v_fma_f32 v68, -v68, v76, v71
	v_div_fmas_f32 v68, v68, v79, v76
	v_div_fixup_f32 v3, v68, v3, 1.0
	v_mul_f32_e32 v63, v63, v3
	v_mul_f32_e32 v63, v63, v34
	v_mov_b32_e32 v68, v181
	v_or_b32_e32 v76, 2, v2
	v_cvt_pk_fp8_f32 v68, v63, 0
	v_ashrrev_i32_e32 v77, 31, v76
	v_mul_f32_e32 v63, v66, v3
	v_lshlrev_b64 v[76:77], 10, v[76:77]
	v_mul_f32_e32 v63, v63, v32
	v_mov_b32_e32 v66, v181
	v_lshl_add_u64 v[76:77], v[4:5], 0, v[76:77]
	v_cvt_pk_fp8_f32 v66, v63, 0
	v_mul_f32_e32 v63, v73, v3
	global_store_byte v[76:77], v68, off
	v_mul_f32_e32 v63, v63, v31
	v_mov_b32_e32 v68, v181
	v_cvt_pk_fp8_f32 v68, v63, 0
	v_fmamk_f32 v63, v81, 0x3c000000, v184
	v_mul_f32_e32 v71, 0x4f800000, v63
	v_cmp_gt_f32_e32 vcc, s55, v63
	v_mul_f32_e32 v3, v87, v3
	v_mul_f32_e32 v3, v3, v30
	v_cndmask_b32_e32 v63, v63, v71, vcc
	v_sqrt_f32_e32 v71, v63
	v_mov_b32_e32 v73, v181
	v_cvt_pk_fp8_f32 v73, v3, 0
	global_store_byte v[76:77], v66, off offset:32
	global_store_byte v[76:77], v68, off offset:64
	global_store_byte v[76:77], v73, off offset:96
	v_add_u32_e32 v3, -1, v71
	v_fma_f32 v78, -v3, v71, v63
	v_cmp_ge_f32_e64 s[6:7], 0, v78
	v_add_u32_e32 v78, 1, v71
	v_or_b32_e32 v76, 3, v2
	v_cndmask_b32_e64 v3, v71, v3, s[6:7]
	v_fma_f32 v71, -v78, v71, v63
	v_cmp_lt_f32_e64 s[6:7], 0, v71
	v_ashrrev_i32_e32 v77, 31, v76
	v_lshlrev_b64 v[76:77], 10, v[76:77]
	v_cndmask_b32_e64 v3, v3, v78, s[6:7]
	v_mul_f32_e32 v71, 0x37800000, v3
	v_cndmask_b32_e32 v3, v3, v71, vcc
	v_cmp_class_f32_e32 vcc, v63, v185
	v_lshl_add_u64 v[76:77], v[4:5], 0, v[76:77]
	s_nop 0
	v_cndmask_b32_e32 v3, v3, v63, vcc
	v_div_scale_f32 v63, s[6:7], v3, v3, 1.0
	v_rcp_f32_e32 v71, v63
	s_nop 0
	v_fma_f32 v66, -v63, v71, 1.0
	v_fmac_f32_e32 v71, v66, v71
	v_div_scale_f32 v66, vcc, 1.0, v3, 1.0
	v_mul_f32_e32 v68, v66, v71
	v_fma_f32 v73, -v63, v68, v66
	v_fmac_f32_e32 v68, v73, v71
	v_fma_f32 v63, -v63, v68, v66
	v_div_fmas_f32 v63, v63, v71, v68
	v_div_fixup_f32 v3, v63, v3, 1.0
	v_mul_f32_e32 v58, v58, v3
	v_mul_f32_e32 v58, v58, v34
	v_mov_b32_e32 v63, v181
	v_cvt_pk_fp8_f32 v63, v58, 0
	v_mul_f32_e32 v58, v61, v3
	v_mul_f32_e32 v58, v58, v32
	v_mov_b32_e32 v61, v181
	v_cvt_pk_fp8_f32 v61, v58, 0
	v_mul_f32_e32 v58, v69, v3
	global_store_byte v[76:77], v63, off
	v_mul_f32_e32 v58, v58, v31
	v_mov_b32_e32 v63, v181
	v_cvt_pk_fp8_f32 v63, v58, 0
	v_fmamk_f32 v58, v85, 0x3c000000, v184
	v_mul_f32_e32 v66, 0x4f800000, v58
	v_cmp_gt_f32_e32 vcc, s55, v58
	v_mul_f32_e32 v3, v74, v3
	v_mul_f32_e32 v3, v3, v30
	v_cndmask_b32_e32 v58, v58, v66, vcc
	v_sqrt_f32_e32 v66, v58
	v_mov_b32_e32 v68, v181
	v_cvt_pk_fp8_f32 v68, v3, 0
	global_store_byte v[76:77], v61, off offset:32
	global_store_byte v[76:77], v63, off offset:64
	global_store_byte v[76:77], v68, off offset:96
	v_add_u32_e32 v3, -1, v66
	v_fma_f32 v69, -v3, v66, v58
	v_cmp_ge_f32_e64 s[6:7], 0, v69
	v_add_u32_e32 v69, 1, v66
	s_nop 0
	v_cndmask_b32_e64 v3, v66, v3, s[6:7]
	v_fma_f32 v66, -v69, v66, v58
	v_cmp_lt_f32_e64 s[6:7], 0, v66
	s_nop 1
	v_cndmask_b32_e64 v3, v3, v69, s[6:7]
	v_mul_f32_e32 v66, 0x37800000, v3
	v_cndmask_b32_e32 v3, v3, v66, vcc
	v_cmp_class_f32_e32 vcc, v58, v185
	s_nop 1
	v_cndmask_b32_e32 v3, v3, v58, vcc
	v_div_scale_f32 v58, s[6:7], v3, v3, 1.0
	v_rcp_f32_e32 v66, v58
	s_nop 0
	v_fma_f32 v61, -v58, v66, 1.0
	v_fmac_f32_e32 v66, v61, v66
	v_div_scale_f32 v61, vcc, 1.0, v3, 1.0
	v_mul_f32_e32 v63, v61, v66
	v_fma_f32 v68, -v58, v63, v61
	v_fmac_f32_e32 v63, v68, v66
	v_fma_f32 v58, -v58, v63, v61
	v_div_fmas_f32 v58, v58, v66, v63
	v_div_fixup_f32 v3, v58, v3, 1.0
	v_mul_f32_e32 v53, v53, v3
	v_mul_f32_e32 v53, v53, v34
	v_mov_b32_e32 v58, v181
	v_add_u32_e32 v68, 8, v2
	v_cvt_pk_fp8_f32 v58, v53, 0
	v_ashrrev_i32_e32 v69, 31, v68
	v_mul_f32_e32 v53, v56, v3
	v_lshlrev_b64 v[68:69], 10, v[68:69]
	v_mul_f32_e32 v53, v53, v32
	v_mov_b32_e32 v56, v181
	v_lshl_add_u64 v[68:69], v[4:5], 0, v[68:69]
	v_cvt_pk_fp8_f32 v56, v53, 0
	v_mul_f32_e32 v53, v64, v3
	global_store_byte v[68:69], v58, off
	v_mul_f32_e32 v53, v53, v31
	v_mov_b32_e32 v58, v181
	v_cvt_pk_fp8_f32 v58, v53, 0
	v_fmamk_f32 v53, v86, 0x3c000000, v184
	v_mul_f32_e32 v61, 0x4f800000, v53
	v_cmp_gt_f32_e32 vcc, s55, v53
	v_mul_f32_e32 v3, v70, v3
	v_mul_f32_e32 v3, v3, v30
	v_cndmask_b32_e32 v53, v53, v61, vcc
	v_sqrt_f32_e32 v61, v53
	v_mov_b32_e32 v63, v181
	v_cvt_pk_fp8_f32 v63, v3, 0
	global_store_byte v[68:69], v56, off offset:32
	global_store_byte v[68:69], v58, off offset:64
	global_store_byte v[68:69], v63, off offset:96
	v_add_u32_e32 v3, -1, v61
	v_fma_f32 v64, -v3, v61, v53
	v_cmp_ge_f32_e64 s[6:7], 0, v64
	v_add_u32_e32 v64, 1, v61
	v_add_u32_e32 v68, 9, v2
	v_cndmask_b32_e64 v3, v61, v3, s[6:7]
	v_fma_f32 v61, -v64, v61, v53
	v_cmp_lt_f32_e64 s[6:7], 0, v61
	v_ashrrev_i32_e32 v69, 31, v68
	v_lshlrev_b64 v[68:69], 10, v[68:69]
	v_cndmask_b32_e64 v3, v3, v64, s[6:7]
	v_mul_f32_e32 v61, 0x37800000, v3
	v_cndmask_b32_e32 v3, v3, v61, vcc
	v_cmp_class_f32_e32 vcc, v53, v185
	v_lshl_add_u64 v[68:69], v[4:5], 0, v[68:69]
	s_nop 0
	v_cndmask_b32_e32 v3, v3, v53, vcc
	v_div_scale_f32 v53, s[6:7], v3, v3, 1.0
	v_rcp_f32_e32 v61, v53
	s_nop 0
	v_fma_f32 v56, -v53, v61, 1.0
	v_fmac_f32_e32 v61, v56, v61
	v_div_scale_f32 v56, vcc, 1.0, v3, 1.0
	v_mul_f32_e32 v58, v56, v61
	v_fma_f32 v63, -v53, v58, v56
	v_fmac_f32_e32 v58, v63, v61
	v_fma_f32 v53, -v53, v58, v56
	v_div_fmas_f32 v53, v53, v61, v58
	v_div_fixup_f32 v3, v53, v3, 1.0
	v_mul_f32_e32 v47, v47, v3
	v_mul_f32_e32 v47, v47, v34
	v_mov_b32_e32 v53, v181
	v_cvt_pk_fp8_f32 v53, v47, 0
	v_mul_f32_e32 v47, v51, v3
	v_mul_f32_e32 v47, v47, v32
	v_mov_b32_e32 v51, v181
	v_cvt_pk_fp8_f32 v51, v47, 0
	v_mul_f32_e32 v47, v59, v3
	global_store_byte v[68:69], v53, off
	v_mul_f32_e32 v47, v47, v31
	v_mov_b32_e32 v53, v181
	v_cvt_pk_fp8_f32 v53, v47, 0
	v_fmamk_f32 v47, v88, 0x3c000000, v184
	v_mul_f32_e32 v56, 0x4f800000, v47
	v_cmp_gt_f32_e32 vcc, s55, v47
	v_mul_f32_e32 v3, v65, v3
	v_mul_f32_e32 v3, v3, v30
	v_cndmask_b32_e32 v47, v47, v56, vcc
	v_sqrt_f32_e32 v56, v47
	v_mov_b32_e32 v58, v181
	v_cvt_pk_fp8_f32 v58, v3, 0
	global_store_byte v[68:69], v51, off offset:32
	global_store_byte v[68:69], v53, off offset:64
	global_store_byte v[68:69], v58, off offset:96
	v_add_u32_e32 v3, -1, v56
	v_fma_f32 v59, -v3, v56, v47
	v_cmp_ge_f32_e64 s[6:7], 0, v59
	v_add_u32_e32 v59, 1, v56
	s_nop 0
	v_cndmask_b32_e64 v3, v56, v3, s[6:7]
	v_fma_f32 v56, -v59, v56, v47
	v_cmp_lt_f32_e64 s[6:7], 0, v56
	s_nop 1
	v_cndmask_b32_e64 v3, v3, v59, s[6:7]
	v_mul_f32_e32 v56, 0x37800000, v3
	v_cndmask_b32_e32 v3, v3, v56, vcc
	v_cmp_class_f32_e32 vcc, v47, v185
	s_nop 1
	v_cndmask_b32_e32 v3, v3, v47, vcc
	v_div_scale_f32 v47, s[6:7], v3, v3, 1.0
	v_rcp_f32_e32 v56, v47
	s_nop 0
	v_fma_f32 v51, -v47, v56, 1.0
	v_fmac_f32_e32 v56, v51, v56
	v_div_scale_f32 v51, vcc, 1.0, v3, 1.0
	v_mul_f32_e32 v53, v51, v56
	v_fma_f32 v58, -v47, v53, v51
	v_fmac_f32_e32 v53, v58, v56
	v_fma_f32 v47, -v47, v53, v51
	v_div_fmas_f32 v47, v47, v56, v53
	v_div_fixup_f32 v3, v47, v3, 1.0
	v_mul_f32_e32 v42, v42, v3
	v_mul_f32_e32 v42, v42, v34
	v_mov_b32_e32 v47, v181
	v_add_u32_e32 v58, 10, v2
	v_cvt_pk_fp8_f32 v47, v42, 0
	v_ashrrev_i32_e32 v59, 31, v58
	v_mul_f32_e32 v42, v46, v3
	v_lshlrev_b64 v[58:59], 10, v[58:59]
	v_mul_f32_e32 v42, v42, v32
	v_mov_b32_e32 v46, v181
	v_lshl_add_u64 v[58:59], v[4:5], 0, v[58:59]
	v_cvt_pk_fp8_f32 v46, v42, 0
	v_mul_f32_e32 v42, v54, v3
	global_store_byte v[58:59], v47, off
	v_mul_f32_e32 v42, v42, v31
	v_mov_b32_e32 v47, v181
	v_cvt_pk_fp8_f32 v47, v42, 0
	v_fmamk_f32 v42, v75, 0x3c000000, v184
	v_mul_f32_e32 v51, 0x4f800000, v42
	v_cmp_gt_f32_e32 vcc, s55, v42
	v_mul_f32_e32 v3, v60, v3
	v_mul_f32_e32 v3, v3, v30
	v_cndmask_b32_e32 v42, v42, v51, vcc
	v_sqrt_f32_e32 v51, v42
	v_mov_b32_e32 v53, v181
	v_cvt_pk_fp8_f32 v53, v3, 0
	global_store_byte v[58:59], v46, off offset:32
	global_store_byte v[58:59], v47, off offset:64
	global_store_byte v[58:59], v53, off offset:96
	v_add_u32_e32 v3, -1, v51
	v_fma_f32 v54, -v3, v51, v42
	v_cmp_ge_f32_e64 s[6:7], 0, v54
	v_add_u32_e32 v54, 1, v51
	s_nop 0
	v_cndmask_b32_e64 v3, v51, v3, s[6:7]
	v_fma_f32 v51, -v54, v51, v42
	v_cmp_lt_f32_e64 s[6:7], 0, v51
	s_nop 1
	v_cndmask_b32_e64 v3, v3, v54, s[6:7]
	v_mul_f32_e32 v51, 0x37800000, v3
	v_cndmask_b32_e32 v3, v3, v51, vcc
	v_cmp_class_f32_e32 vcc, v42, v185
	s_nop 1
	v_cndmask_b32_e32 v3, v3, v42, vcc
	v_div_scale_f32 v42, s[6:7], v3, v3, 1.0
	v_rcp_f32_e32 v51, v42
	s_nop 0
	v_fma_f32 v46, -v42, v51, 1.0
	v_fmac_f32_e32 v51, v46, v51
	v_div_scale_f32 v46, vcc, 1.0, v3, 1.0
	v_mul_f32_e32 v47, v46, v51
	v_fma_f32 v53, -v42, v47, v46
	v_fmac_f32_e32 v47, v53, v51
	v_fma_f32 v42, -v42, v47, v46
	v_div_fmas_f32 v42, v42, v51, v47
	v_div_fixup_f32 v3, v42, v3, 1.0
	v_mul_f32_e32 v36, v36, v3
	v_mul_f32_e32 v36, v36, v34
	v_mov_b32_e32 v42, v181
	v_add_u32_e32 v46, 11, v2
	v_cvt_pk_fp8_f32 v42, v36, 0
	v_ashrrev_i32_e32 v47, 31, v46
	v_mul_f32_e32 v36, v41, v3
	v_lshlrev_b64 v[46:47], 10, v[46:47]
	v_mul_f32_e32 v36, v36, v32
	v_mov_b32_e32 v41, v181
	v_lshl_add_u64 v[46:47], v[4:5], 0, v[46:47]
	v_cvt_pk_fp8_f32 v41, v36, 0
	v_mul_f32_e32 v36, v49, v3
	global_store_byte v[46:47], v42, off
	v_mul_f32_e32 v36, v36, v31
	v_mov_b32_e32 v42, v181
	v_cvt_pk_fp8_f32 v42, v36, 0
	v_fmamk_f32 v36, v72, 0x3c000000, v184
	v_mul_f32_e32 v49, 0x4f800000, v36
	v_cmp_gt_f32_e32 vcc, s55, v36
	v_mul_f32_e32 v3, v55, v3
	v_mul_f32_e32 v3, v3, v30
	v_cndmask_b32_e32 v36, v36, v49, vcc
	v_sqrt_f32_e32 v49, v36
	v_mov_b32_e32 v51, v181
	v_cvt_pk_fp8_f32 v51, v3, 0
	global_store_byte v[46:47], v41, off offset:32
	global_store_byte v[46:47], v42, off offset:64
	global_store_byte v[46:47], v51, off offset:96
	v_add_u32_e32 v3, -1, v49
	v_fma_f32 v53, -v3, v49, v36
	v_cmp_ge_f32_e64 s[6:7], 0, v53
	v_add_u32_e32 v53, 1, v49
	s_nop 0
	v_cndmask_b32_e64 v3, v49, v3, s[6:7]
	v_fma_f32 v49, -v53, v49, v36
	v_cmp_lt_f32_e64 s[6:7], 0, v49
	s_nop 1
	v_cndmask_b32_e64 v3, v3, v53, s[6:7]
	v_mul_f32_e32 v49, 0x37800000, v3
	v_cndmask_b32_e32 v3, v3, v49, vcc
	v_cmp_class_f32_e32 vcc, v36, v185
	s_nop 1
	v_cndmask_b32_e32 v3, v3, v36, vcc
	v_div_scale_f32 v36, s[6:7], v3, v3, 1.0
	v_rcp_f32_e32 v49, v36
	s_nop 0
	v_fma_f32 v41, -v36, v49, 1.0
	v_fmac_f32_e32 v49, v41, v49
	v_div_scale_f32 v41, vcc, 1.0, v3, 1.0
	v_mul_f32_e32 v42, v41, v49
	v_fma_f32 v46, -v36, v42, v41
	v_fmac_f32_e32 v42, v46, v49
	v_fma_f32 v36, -v36, v42, v41
	v_div_fmas_f32 v36, v36, v49, v42
	v_div_fixup_f32 v3, v36, v3, 1.0
	v_mul_f32_e32 v28, v28, v3
	v_mul_f32_e32 v28, v28, v34
	v_mov_b32_e32 v36, v181
	v_add_u32_e32 v46, 16, v2
	v_cvt_pk_fp8_f32 v36, v28, 0
	v_ashrrev_i32_e32 v47, 31, v46
	v_lshlrev_b64 v[46:47], 10, v[46:47]
	v_lshl_add_u64 v[46:47], v[4:5], 0, v[46:47]
	v_mul_f32_e32 v28, v37, v3
	global_store_byte v[46:47], v36, off
	v_mul_f32_e32 v28, v28, v32
	v_mov_b32_e32 v36, v181
	v_cvt_pk_fp8_f32 v36, v28, 0
	v_mul_f32_e32 v28, v44, v3
	v_mul_f32_e32 v28, v28, v31
	v_mov_b32_e32 v37, v181
	v_cvt_pk_fp8_f32 v37, v28, 0
	v_fmamk_f32 v28, v67, 0x3c000000, v184
	v_mul_f32_e32 v41, 0x4f800000, v28
	v_cmp_gt_f32_e32 vcc, s55, v28
	v_mul_f32_e32 v3, v50, v3
	v_mul_f32_e32 v3, v3, v30
	v_cndmask_b32_e32 v28, v28, v41, vcc
	v_sqrt_f32_e32 v41, v28
	v_mov_b32_e32 v42, v181
	v_cvt_pk_fp8_f32 v42, v3, 0
	global_store_byte v[46:47], v36, off offset:32
	global_store_byte v[46:47], v37, off offset:64
	global_store_byte v[46:47], v42, off offset:96
	v_add_u32_e32 v3, -1, v41
	v_fma_f32 v44, -v3, v41, v28
	v_cmp_ge_f32_e64 s[6:7], 0, v44
	v_add_u32_e32 v44, 1, v41
	s_nop 0
	v_cndmask_b32_e64 v3, v41, v3, s[6:7]
	v_fma_f32 v41, -v44, v41, v28
	v_cmp_lt_f32_e64 s[6:7], 0, v41
	s_nop 1
	v_cndmask_b32_e64 v3, v3, v44, s[6:7]
	v_mul_f32_e32 v41, 0x37800000, v3
	v_cndmask_b32_e32 v3, v3, v41, vcc
	v_cmp_class_f32_e32 vcc, v28, v185
	s_nop 1
	v_cndmask_b32_e32 v3, v3, v28, vcc
	v_div_scale_f32 v28, s[6:7], v3, v3, 1.0
	v_rcp_f32_e32 v41, v28
	s_nop 0
	v_fma_f32 v36, -v28, v41, 1.0
	v_fmac_f32_e32 v41, v36, v41
	v_div_scale_f32 v36, vcc, 1.0, v3, 1.0
	v_mul_f32_e32 v37, v36, v41
	v_fma_f32 v42, -v28, v37, v36
	v_fmac_f32_e32 v37, v42, v41
	v_fma_f32 v28, -v28, v37, v36
	v_div_fmas_f32 v28, v28, v41, v37
	v_div_fixup_f32 v3, v28, v3, 1.0
	v_mul_f32_e32 v24, v24, v3
	v_mul_f32_e32 v24, v24, v34
	v_mov_b32_e32 v28, v181
	v_add_u32_e32 v36, 17, v2
	v_cvt_pk_fp8_f32 v28, v24, 0
	v_ashrrev_i32_e32 v37, 31, v36
	v_lshlrev_b64 v[36:37], 10, v[36:37]
	v_lshl_add_u64 v[36:37], v[4:5], 0, v[36:37]
	v_mul_f32_e32 v24, v29, v3
	global_store_byte v[36:37], v28, off
	v_mul_f32_e32 v24, v24, v32
	v_mov_b32_e32 v28, v181
	v_cvt_pk_fp8_f32 v28, v24, 0
	v_mul_f32_e32 v24, v39, v3
	v_mul_f32_e32 v24, v24, v31
	v_mov_b32_e32 v29, v181
	v_cvt_pk_fp8_f32 v29, v24, 0
	v_fmamk_f32 v24, v62, 0x3c000000, v184
	v_mul_f32_e32 v39, 0x4f800000, v24
	v_cmp_gt_f32_e32 vcc, s55, v24
	v_mul_f32_e32 v3, v45, v3
	v_mul_f32_e32 v3, v3, v30
	v_cndmask_b32_e32 v24, v24, v39, vcc
	v_sqrt_f32_e32 v39, v24
	v_mov_b32_e32 v41, v181
	v_cvt_pk_fp8_f32 v41, v3, 0
	global_store_byte v[36:37], v28, off offset:32
	global_store_byte v[36:37], v29, off offset:64
	global_store_byte v[36:37], v41, off offset:96
	v_add_u32_e32 v3, -1, v39
	v_fma_f32 v42, -v3, v39, v24
	v_cmp_ge_f32_e64 s[6:7], 0, v42
	v_add_u32_e32 v42, 1, v39
	s_nop 0
	v_cndmask_b32_e64 v3, v39, v3, s[6:7]
	v_fma_f32 v39, -v42, v39, v24
	v_cmp_lt_f32_e64 s[6:7], 0, v39
	s_nop 1
	v_cndmask_b32_e64 v3, v3, v42, s[6:7]
	v_mul_f32_e32 v39, 0x37800000, v3
	v_cndmask_b32_e32 v3, v3, v39, vcc
	v_cmp_class_f32_e32 vcc, v24, v185
	s_nop 1
	v_cndmask_b32_e32 v3, v3, v24, vcc
	v_div_scale_f32 v24, s[6:7], v3, v3, 1.0
	v_rcp_f32_e32 v39, v24
	s_nop 0
	v_fma_f32 v28, -v24, v39, 1.0
	v_fmac_f32_e32 v39, v28, v39
	v_div_scale_f32 v28, vcc, 1.0, v3, 1.0
	v_mul_f32_e32 v29, v28, v39
	v_fma_f32 v36, -v24, v29, v28
	v_fmac_f32_e32 v29, v36, v39
	v_fma_f32 v24, -v24, v29, v28
	v_div_fmas_f32 v24, v24, v39, v29
	v_div_fixup_f32 v3, v24, v3, 1.0
	v_mul_f32_e32 v20, v20, v3
	v_mul_f32_e32 v20, v20, v34
	v_mov_b32_e32 v24, v181
	v_add_u32_e32 v28, 18, v2
	v_cvt_pk_fp8_f32 v24, v20, 0
	v_ashrrev_i32_e32 v29, 31, v28
	v_lshlrev_b64 v[28:29], 10, v[28:29]
	v_lshl_add_u64 v[28:29], v[4:5], 0, v[28:29]
	v_mul_f32_e32 v20, v25, v3
	global_store_byte v[28:29], v24, off
	v_mul_f32_e32 v20, v20, v32
	v_mov_b32_e32 v24, v181
	v_cvt_pk_fp8_f32 v24, v20, 0
	v_mul_f32_e32 v20, v33, v3
	v_mul_f32_e32 v20, v20, v31
	v_mov_b32_e32 v25, v181
	v_cvt_pk_fp8_f32 v25, v20, 0
	v_fmamk_f32 v20, v57, 0x3c000000, v184
	v_mul_f32_e32 v33, 0x4f800000, v20
	v_cmp_gt_f32_e32 vcc, s55, v20
	v_mul_f32_e32 v3, v40, v3
	v_mul_f32_e32 v3, v3, v30
	v_cndmask_b32_e32 v20, v20, v33, vcc
	v_sqrt_f32_e32 v33, v20
	v_mov_b32_e32 v36, v181
	v_cvt_pk_fp8_f32 v36, v3, 0
	global_store_byte v[28:29], v24, off offset:32
	global_store_byte v[28:29], v25, off offset:64
	global_store_byte v[28:29], v36, off offset:96
	v_add_u32_e32 v3, -1, v33
	v_fma_f32 v37, -v3, v33, v20
	v_cmp_ge_f32_e64 s[6:7], 0, v37
	v_add_u32_e32 v37, 1, v33
	s_nop 0
	v_cndmask_b32_e64 v3, v33, v3, s[6:7]
	v_fma_f32 v33, -v37, v33, v20
	v_cmp_lt_f32_e64 s[6:7], 0, v33
	s_nop 1
	v_cndmask_b32_e64 v3, v3, v37, s[6:7]
	v_mul_f32_e32 v33, 0x37800000, v3
	v_cndmask_b32_e32 v3, v3, v33, vcc
	v_cmp_class_f32_e32 vcc, v20, v185
	s_nop 1
	v_cndmask_b32_e32 v3, v3, v20, vcc
	v_div_scale_f32 v20, s[6:7], v3, v3, 1.0
	v_rcp_f32_e32 v33, v20
	s_nop 0
	v_fma_f32 v24, -v20, v33, 1.0
	v_fmac_f32_e32 v33, v24, v33
	v_div_scale_f32 v24, vcc, 1.0, v3, 1.0
	v_mul_f32_e32 v25, v24, v33
	v_fma_f32 v28, -v20, v25, v24
	v_fmac_f32_e32 v25, v28, v33
	v_fma_f32 v20, -v20, v25, v24
	v_div_fmas_f32 v20, v20, v33, v25
	v_div_fixup_f32 v3, v20, v3, 1.0
	v_mul_f32_e32 v16, v16, v3
	v_mul_f32_e32 v16, v16, v34
	v_mov_b32_e32 v20, v181
	v_add_u32_e32 v24, 19, v2
	v_cvt_pk_fp8_f32 v20, v16, 0
	v_ashrrev_i32_e32 v25, 31, v24
	v_lshlrev_b64 v[24:25], 10, v[24:25]
	v_lshl_add_u64 v[24:25], v[4:5], 0, v[24:25]
	v_mul_f32_e32 v16, v21, v3
	global_store_byte v[24:25], v20, off
	v_mul_f32_e32 v16, v16, v32
	v_mov_b32_e32 v20, v181
	v_cvt_pk_fp8_f32 v20, v16, 0
	v_mul_f32_e32 v16, v26, v3
	v_mul_f32_e32 v16, v16, v31
	v_mov_b32_e32 v21, v181
	v_cvt_pk_fp8_f32 v21, v16, 0
	v_fmamk_f32 v16, v52, 0x3c000000, v184
	v_mul_f32_e32 v26, 0x4f800000, v16
	v_cmp_gt_f32_e32 vcc, s55, v16
	v_mul_f32_e32 v3, v35, v3
	v_mul_f32_e32 v3, v3, v30
	v_cndmask_b32_e32 v16, v16, v26, vcc
	v_sqrt_f32_e32 v26, v16
	v_mov_b32_e32 v28, v181
	v_cvt_pk_fp8_f32 v28, v3, 0
	global_store_byte v[24:25], v20, off offset:32
	global_store_byte v[24:25], v21, off offset:64
	global_store_byte v[24:25], v28, off offset:96
	v_add_u32_e32 v3, -1, v26
	v_fma_f32 v29, -v3, v26, v16
	v_cmp_ge_f32_e64 s[6:7], 0, v29
	v_add_u32_e32 v29, 1, v26
	s_nop 0
	v_cndmask_b32_e64 v3, v26, v3, s[6:7]
	v_fma_f32 v26, -v29, v26, v16
	v_cmp_lt_f32_e64 s[6:7], 0, v26
	s_nop 1
	v_cndmask_b32_e64 v3, v3, v29, s[6:7]
	v_mul_f32_e32 v26, 0x37800000, v3
	v_cndmask_b32_e32 v3, v3, v26, vcc
	v_cmp_class_f32_e32 vcc, v16, v185
	s_nop 1
	v_cndmask_b32_e32 v3, v3, v16, vcc
	v_div_scale_f32 v16, s[6:7], v3, v3, 1.0
	v_rcp_f32_e32 v26, v16
	s_nop 0
	v_fma_f32 v20, -v16, v26, 1.0
	v_fmac_f32_e32 v26, v20, v26
	v_div_scale_f32 v20, vcc, 1.0, v3, 1.0
	v_mul_f32_e32 v21, v20, v26
	v_fma_f32 v24, -v16, v21, v20
	v_fmac_f32_e32 v21, v24, v26
	v_fma_f32 v16, -v16, v21, v20
	v_div_fmas_f32 v16, v16, v26, v21
	v_div_fixup_f32 v3, v16, v3, 1.0
	v_mul_f32_e32 v12, v12, v3
	v_mul_f32_e32 v12, v12, v34
	v_mov_b32_e32 v16, v181
	v_add_u32_e32 v20, 24, v2
	v_cvt_pk_fp8_f32 v16, v12, 0
	v_ashrrev_i32_e32 v21, 31, v20
	v_lshlrev_b64 v[20:21], 10, v[20:21]
	v_lshl_add_u64 v[20:21], v[4:5], 0, v[20:21]
	v_mul_f32_e32 v12, v17, v3
	global_store_byte v[20:21], v16, off
	v_mul_f32_e32 v12, v12, v32
	v_mov_b32_e32 v16, v181
	v_cvt_pk_fp8_f32 v16, v12, 0
	v_mul_f32_e32 v12, v22, v3
	v_mul_f32_e32 v12, v12, v31
	v_mov_b32_e32 v17, v181
	v_cvt_pk_fp8_f32 v17, v12, 0
	v_fmamk_f32 v12, v48, 0x3c000000, v184
	v_mul_f32_e32 v22, 0x4f800000, v12
	v_cmp_gt_f32_e32 vcc, s55, v12
	v_mul_f32_e32 v3, v27, v3
	v_mul_f32_e32 v3, v3, v30
	v_cndmask_b32_e32 v12, v12, v22, vcc
	v_sqrt_f32_e32 v22, v12
	v_mov_b32_e32 v24, v181
	v_cvt_pk_fp8_f32 v24, v3, 0
	global_store_byte v[20:21], v16, off offset:32
	global_store_byte v[20:21], v17, off offset:64
	global_store_byte v[20:21], v24, off offset:96
	v_add_u32_e32 v3, -1, v22
	v_fma_f32 v25, -v3, v22, v12
	v_cmp_ge_f32_e64 s[6:7], 0, v25
	v_add_u32_e32 v25, 1, v22
	s_nop 0
	v_cndmask_b32_e64 v3, v22, v3, s[6:7]
	v_fma_f32 v22, -v25, v22, v12
	v_cmp_lt_f32_e64 s[6:7], 0, v22
	s_nop 1
	v_cndmask_b32_e64 v3, v3, v25, s[6:7]
	v_mul_f32_e32 v22, 0x37800000, v3
	v_cndmask_b32_e32 v3, v3, v22, vcc
	v_cmp_class_f32_e32 vcc, v12, v185
	s_nop 1
	v_cndmask_b32_e32 v3, v3, v12, vcc
	v_div_scale_f32 v12, s[6:7], v3, v3, 1.0
	v_rcp_f32_e32 v22, v12
	s_nop 0
	v_fma_f32 v16, -v12, v22, 1.0
	v_fmac_f32_e32 v22, v16, v22
	v_div_scale_f32 v16, vcc, 1.0, v3, 1.0
	v_mul_f32_e32 v17, v16, v22
	v_fma_f32 v20, -v12, v17, v16
	v_fmac_f32_e32 v17, v20, v22
	v_fma_f32 v12, -v12, v17, v16
	v_div_fmas_f32 v12, v12, v22, v17
	v_div_fixup_f32 v3, v12, v3, 1.0
	v_mul_f32_e32 v9, v9, v3
	v_mul_f32_e32 v9, v9, v34
	v_mov_b32_e32 v12, v181
	v_add_u32_e32 v16, 25, v2
	v_cvt_pk_fp8_f32 v12, v9, 0
	v_ashrrev_i32_e32 v17, 31, v16
	v_lshlrev_b64 v[16:17], 10, v[16:17]
	v_lshl_add_u64 v[16:17], v[4:5], 0, v[16:17]
	v_mul_f32_e32 v9, v13, v3
	global_store_byte v[16:17], v12, off
	v_mul_f32_e32 v9, v9, v32
	v_mov_b32_e32 v12, v181
	v_cvt_pk_fp8_f32 v12, v9, 0
	v_mul_f32_e32 v9, v18, v3
	v_mul_f32_e32 v9, v9, v31
	v_mov_b32_e32 v13, v181
	v_cvt_pk_fp8_f32 v13, v9, 0
	v_fmamk_f32 v9, v43, 0x3c000000, v184
	v_mul_f32_e32 v18, 0x4f800000, v9
	v_cmp_gt_f32_e32 vcc, s55, v9
	v_mul_f32_e32 v3, v23, v3
	v_mul_f32_e32 v3, v3, v30
	v_cndmask_b32_e32 v9, v9, v18, vcc
	v_sqrt_f32_e32 v18, v9
	v_mov_b32_e32 v20, v181
	v_cvt_pk_fp8_f32 v20, v3, 0
	global_store_byte v[16:17], v12, off offset:32
	global_store_byte v[16:17], v13, off offset:64
	global_store_byte v[16:17], v20, off offset:96
	v_add_u32_e32 v3, -1, v18
	v_fma_f32 v21, -v3, v18, v9
	v_cmp_ge_f32_e64 s[6:7], 0, v21
	v_add_u32_e32 v21, 1, v18
	s_nop 0
	v_cndmask_b32_e64 v3, v18, v3, s[6:7]
	v_fma_f32 v18, -v21, v18, v9
	v_cmp_lt_f32_e64 s[6:7], 0, v18
	s_nop 1
	v_cndmask_b32_e64 v3, v3, v21, s[6:7]
	v_mul_f32_e32 v18, 0x37800000, v3
	v_cndmask_b32_e32 v3, v3, v18, vcc
	v_cmp_class_f32_e32 vcc, v9, v185
	s_nop 1
	v_cndmask_b32_e32 v3, v3, v9, vcc
	v_div_scale_f32 v9, s[6:7], v3, v3, 1.0
	v_rcp_f32_e32 v18, v9
	s_nop 0
	v_fma_f32 v12, -v9, v18, 1.0
	v_fmac_f32_e32 v18, v12, v18
	v_div_scale_f32 v12, vcc, 1.0, v3, 1.0
	v_mul_f32_e32 v13, v12, v18
	v_fma_f32 v16, -v9, v13, v12
	v_fmac_f32_e32 v13, v16, v18
	v_fma_f32 v9, -v9, v13, v12
	v_div_fmas_f32 v9, v9, v18, v13
	v_div_fixup_f32 v3, v9, v3, 1.0
	v_mul_f32_e32 v7, v7, v3
	v_mul_f32_e32 v7, v7, v34
	v_mov_b32_e32 v9, v181
	v_add_u32_e32 v12, 26, v2
	v_cvt_pk_fp8_f32 v9, v7, 0
	v_ashrrev_i32_e32 v13, 31, v12
	v_lshlrev_b64 v[12:13], 10, v[12:13]
	v_lshl_add_u64 v[12:13], v[4:5], 0, v[12:13]
	v_mul_f32_e32 v7, v10, v3
	global_store_byte v[12:13], v9, off
	v_mul_f32_e32 v7, v7, v32
	v_mov_b32_e32 v9, v181
	v_cvt_pk_fp8_f32 v9, v7, 0
	v_mul_f32_e32 v7, v14, v3
	v_mul_f32_e32 v7, v7, v31
	v_mov_b32_e32 v10, v181
	v_cvt_pk_fp8_f32 v10, v7, 0
	v_fmamk_f32 v7, v38, 0x3c000000, v184
	v_mul_f32_e32 v14, 0x4f800000, v7
	v_cmp_gt_f32_e32 vcc, s55, v7
	v_mul_f32_e32 v3, v19, v3
	v_mul_f32_e32 v3, v3, v30
	v_cndmask_b32_e32 v7, v7, v14, vcc
	v_sqrt_f32_e32 v14, v7
	v_mov_b32_e32 v16, v181
	v_cvt_pk_fp8_f32 v16, v3, 0
	global_store_byte v[12:13], v9, off offset:32
	global_store_byte v[12:13], v10, off offset:64
	global_store_byte v[12:13], v16, off offset:96
	v_add_u32_e32 v3, -1, v14
	v_fma_f32 v17, -v3, v14, v7
	v_cmp_ge_f32_e64 s[6:7], 0, v17
	v_add_u32_e32 v17, 1, v14
	v_add_u32_e32 v2, 27, v2
	v_cndmask_b32_e64 v3, v14, v3, s[6:7]
	v_fma_f32 v14, -v17, v14, v7
	v_cmp_lt_f32_e64 s[6:7], 0, v14
	s_nop 1
	v_cndmask_b32_e64 v3, v3, v17, s[6:7]
	v_mul_f32_e32 v14, 0x37800000, v3
	v_cndmask_b32_e32 v3, v3, v14, vcc
	v_cmp_class_f32_e32 vcc, v7, v185
	s_nop 1
	v_cndmask_b32_e32 v3, v3, v7, vcc
	v_div_scale_f32 v7, s[6:7], v3, v3, 1.0
	v_rcp_f32_e32 v14, v7
	s_nop 0
	v_fma_f32 v9, -v7, v14, 1.0
	v_fmac_f32_e32 v14, v9, v14
	v_div_scale_f32 v9, vcc, 1.0, v3, 1.0
	v_mul_f32_e32 v10, v9, v14
	v_fma_f32 v12, -v7, v10, v9
	v_fmac_f32_e32 v10, v12, v14
	v_fma_f32 v7, -v7, v10, v9
	v_div_fmas_f32 v7, v7, v14, v10
	v_div_fixup_f32 v7, v7, v3, 1.0
	v_ashrrev_i32_e32 v3, 31, v2
	v_mul_f32_e32 v6, v6, v7
	v_lshlrev_b64 v[2:3], 10, v[2:3]
	v_mul_f32_e32 v6, v34, v6
	v_mov_b32_e32 v9, v181
	v_lshl_add_u64 v[2:3], v[4:5], 0, v[2:3]
	v_mul_f32_e32 v4, v11, v7
	v_cvt_pk_fp8_f32 v9, v6, 0
	v_mul_f32_e32 v6, v8, v7
	v_mul_f32_e32 v4, v31, v4
	v_mov_b32_e32 v5, v181
	v_mul_f32_e32 v6, v32, v6
	v_mov_b32_e32 v8, v181
	v_cvt_pk_fp8_f32 v5, v4, 0
	v_mul_f32_e32 v4, v15, v7
	v_cvt_pk_fp8_f32 v8, v6, 0
	v_mul_f32_e32 v4, v30, v4
	v_mov_b32_e32 v6, v181
	v_cvt_pk_fp8_f32 v6, v4, 0
	global_store_byte v[2:3], v9, off
	global_store_byte v[2:3], v8, off offset:32
	global_store_byte v[2:3], v5, off offset:64
	global_store_byte v[2:3], v6, off offset:96
	s_cbranch_scc0 .LBB0_1427

.LBB0_1211:
	s_and_b32 s37, s95, 0xffffffc0
	v_lshlrev_b32_e32 v6, 2, v5
	v_lshlrev_b32_e32 v3, 6, v4
	v_and_b32_e32 v6, 48, v6
	s_cmp_lg_u32 0, -1
	v_bitop3_b32 v194, v6, v3, v2 bitop3:0xde
	s_cselect_b32 s38, 0, 0
	v_lshlrev_b32_e32 v2, 3, v5
	v_and_b32_e32 v193, 63, v5
	v_add_u32_e32 v183, s38, v194
	s_addk_i32 s38, 0x4000
	v_and_b32_e32 v2, 32, v2
	s_lshl_b32 s37, s37, 2
	v_add_u32_e32 v188, s38, v194
	v_sub_u32_e32 v195, 16, v2
	v_lshrrev_b32_e32 v2, 5, v193
	s_add_i32 s78, s37, 0
	v_add_u32_e32 v190, v183, v195
	s_mov_b64 s[38:39], -1
	s_and_b64 vcc, exec, s[6:7]
	v_add_u32_e32 v189, v188, v195
	v_cmp_gt_u32_e64 s[6:7], 32, v193
	v_lshlrev_b32_e32 v186, 4, v2
	v_lshl_add_u32 v187, v4, 2, s78
	v_and_b32_e32 v248, 31, v193
	v_mov_b32_e32 v249, 0x38383838
	v_cmp_eq_u32_e64 s[98:99], 0, v248
	v_cmp_eq_u32_e64 s[100:101], 17, v248
	v_and_b32_e32 v248, 15, v193
	v_lshrrev_b32_e32 v250, 4, v193
	s_or_b64 s[98:99], s[98:99], s[100:101]
	v_lshlrev_b32_e32 v248, 6, v248
	v_lshl_add_u32 v250, v250, 4, v248
	v_cndmask_b32_e64 v146, 0, v249, s[98:99]
	v_add_u32_e32 v250, s78, v250
	v_mov_b32_e32 v147, v146
	v_mov_b32_e32 v148, v146
	v_mov_b32_e32 v149, v146
	v_mov_b32_e32 v150, v146
	v_mov_b32_e32 v151, v146
	v_mov_b32_e32 v152, v146
	v_mov_b32_e32 v153, v146
	s_cbranch_vccz .LBB0_1264
	ds_read_b128 v[18:21], v183 offset:0
	ds_read_b128 v[22:25], v190 offset:0
	ds_read_b128 v[34:37], v183 offset:0x800
	ds_read_b128 v[38:41], v190 offset:0x800
	s_waitcnt lgkmcnt(0)
	s_waitcnt vmcnt(0)
	v_mfma_f32_32x32x64_f8f6f4 v[18:33], v[18:25], v[154:161], 0
	s_mov_b32 s37, s36
	s_mov_b32 s38, s36
	s_mov_b32 s39, s36
	s_mov_b32 s40, s36
	s_mov_b32 s41, s36
	s_mov_b32 s42, s36
	s_mov_b32 s43, s36
	s_mov_b32 s44, s36
	s_mov_b32 s45, s36
	s_mov_b32 s46, s36
	s_mov_b32 s47, s36
	s_mov_b32 s48, s36
	s_mov_b32 s49, s36
	s_mov_b32 s50, s36
	s_mov_b32 s51, s36
	v_mov_b64_e32 v[2:3], s[36:37]
	v_mov_b64_e32 v[4:5], s[38:39]
	v_mov_b64_e32 v[6:7], s[40:41]
	v_mov_b64_e32 v[8:9], s[42:43]
	v_mov_b64_e32 v[10:11], s[44:45]
	v_mov_b64_e32 v[12:13], s[46:47]
	v_mov_b64_e32 v[14:15], s[48:49]
	v_mov_b64_e32 v[16:17], s[50:51]
	v_max_f32_e32 v42, v19, v19
	v_max_f32_e32 v43, v18, v18
	v_max_f32_e32 v42, v43, v42
	v_max3_f32 v42, v42, v20, v21
	v_max3_f32 v42, v42, v22, v23
	v_max3_f32 v42, v42, v24, v25
	v_max3_f32 v42, v42, v26, v27
	v_max3_f32 v42, v42, v28, v29
	v_max3_f32 v50, v42, v30, v31
	v_mfma_f32_32x32x64_f8f6f4 v[34:49], v[34:41], v[154:161], 0
	v_max3_f32 v50, v50, v32, v33
	s_cmp_lg_u32 0, -1
	s_cselect_b32 s37, 0, 0
	v_mov_b32_e32 v130, v181
	v_mov_b32_e32 v131, v181
	s_add_i32 s38, s37, 0x1000
	s_waitcnt vmcnt(0) lgkmcnt(0)
	s_barrier
	v_add_u32_e32 v207, s38, v194
	v_add_u32_e32 v209, v207, v195
	s_nop 11
	v_max3_f32 v50, v50, v34, v35
	v_max3_f32 v50, v50, v36, v37
	v_max3_f32 v50, v50, v38, v39
	v_max3_f32 v50, v50, v40, v41
	v_max3_f32 v50, v50, v42, v43
	v_max3_f32 v50, v50, v44, v45
	v_max3_f32 v50, v50, v46, v47
	v_max3_f32 v50, v50, v48, v49
	v_mov_b32_e32 v51, v50
	s_nop 1
	v_permlane32_swap_b32_e32 v50, v51
	v_max_f32_e32 v51, v51, v51
	v_max_f32_e32 v50, v50, v50
	v_max_f32_e32 v50, v50, v51
	v_add_f32_e32 v198, 0xc0600000, v50
	v_sub_f32_e32 v18, v18, v198
	v_sub_f32_e32 v19, v19, v198
	v_sub_f32_e32 v22, v22, v198
	v_sub_f32_e32 v23, v23, v198
	v_exp_f32_e32 v50, v18
	v_exp_f32_e32 v51, v19
	v_exp_f32_e32 v54, v22
	v_exp_f32_e32 v55, v23
	v_xor_b32_e32 v82, 0x80000000, v198
	v_sub_f32_e32 v20, v20, v198
	v_sub_f32_e32 v21, v21, v198
	v_sub_f32_e32 v24, v24, v198
	v_sub_f32_e32 v25, v25, v198
	v_mov_b32_e32 v83, v82
	v_mov_b32_e32 v84, v82
	v_mov_b32_e32 v85, v82
	v_mov_b32_e32 v86, v82
	v_mov_b32_e32 v87, v82
	v_mov_b32_e32 v88, v82
	v_mov_b32_e32 v89, v82
	v_mov_b32_e32 v90, v82
	v_mov_b32_e32 v91, v82
	v_mov_b32_e32 v92, v82
	v_mov_b32_e32 v93, v82
	v_mov_b32_e32 v94, v82
	v_mov_b32_e32 v95, v82
	v_mov_b32_e32 v96, v82
	v_mov_b32_e32 v97, v82
	v_exp_f32_e32 v52, v20
	v_exp_f32_e32 v53, v21
	v_exp_f32_e32 v56, v24
	v_exp_f32_e32 v57, v25
	v_cvt_pk_fp8_f32 v130, v50, v51
	v_cvt_pk_fp8_f32 v131, v54, v55
	ds_read_b128 v[18:21], v207 offset:0
	v_sub_f32_e32 v26, v26, v198
	v_sub_f32_e32 v27, v27, v198
	v_sub_f32_e32 v28, v28, v198
	v_sub_f32_e32 v29, v29, v198
	ds_read_b128 v[22:25], v209 offset:0
	v_sub_f32_e32 v34, v34, v198
	v_sub_f32_e32 v35, v35, v198
	v_sub_f32_e32 v36, v36, v198
	v_sub_f32_e32 v37, v37, v198
	v_sub_f32_e32 v38, v38, v198
	v_sub_f32_e32 v39, v39, v198
	v_sub_f32_e32 v40, v40, v198
	v_sub_f32_e32 v41, v41, v198
	v_sub_f32_e32 v42, v42, v198
	v_sub_f32_e32 v43, v43, v198
	v_sub_f32_e32 v44, v44, v198
	v_sub_f32_e32 v45, v45, v198
	v_sub_f32_e32 v30, v30, v198
	v_sub_f32_e32 v46, v46, v198
	v_sub_f32_e32 v31, v31, v198
	v_sub_f32_e32 v47, v47, v198
	v_sub_f32_e32 v32, v32, v198
	v_sub_f32_e32 v48, v48, v198
	v_sub_f32_e32 v33, v33, v198
	v_sub_f32_e32 v49, v49, v198
	v_exp_f32_e32 v58, v26
	v_exp_f32_e32 v59, v27
	v_exp_f32_e32 v60, v28
	v_exp_f32_e32 v61, v29
	ds_read_b128 v[26:29], v207 offset:0x800
	v_exp_f32_e32 v34, v34
	v_exp_f32_e32 v35, v35
	v_exp_f32_e32 v36, v36
	v_exp_f32_e32 v37, v37
	v_exp_f32_e32 v38, v38
	v_exp_f32_e32 v39, v39
	v_exp_f32_e32 v40, v40
	v_exp_f32_e32 v41, v41
	v_exp_f32_e32 v42, v42
	v_exp_f32_e32 v43, v43
	v_exp_f32_e32 v44, v44
	v_exp_f32_e32 v45, v45
	v_exp_f32_e32 v62, v30
	v_exp_f32_e32 v46, v46
	v_exp_f32_e32 v63, v31
	v_exp_f32_e32 v47, v47
	v_exp_f32_e32 v64, v32
	v_exp_f32_e32 v48, v48
	v_exp_f32_e32 v65, v33
	v_exp_f32_e32 v49, v49
	ds_read_b128 v[30:33], v209 offset:0x800
	v_cvt_pk_fp8_f32 v130, v52, v53 op_sel:[0,0,1]
	v_cvt_pk_fp8_f32 v131, v56, v57 op_sel:[0,0,1]
	s_waitcnt lgkmcnt(2)
	v_mfma_f32_32x32x64_f8f6f4 v[98:113], v[18:25], v[154:161], v[82:97]
	v_mov_b32_e32 v132, v181
	v_mov_b32_e32 v133, v181
	v_cvt_pk_fp8_f32 v132, v58, v59
	v_cvt_pk_fp8_f32 v133, v62, v63
	ds_read_b128 v[170:173], v188 offset:0
	ds_read_b128 v[174:177], v189 offset:0
	v_cvt_pk_fp8_f32 v132, v60, v61 op_sel:[0,0,1]
	v_cvt_pk_fp8_f32 v133, v64, v65 op_sel:[0,0,1]
	s_waitcnt lgkmcnt(2)
	v_mov_b64_e32 v[128:129], v[96:97]
	v_mov_b64_e32 v[126:127], v[94:95]
	v_mov_b64_e32 v[124:125], v[92:93]
	v_mov_b64_e32 v[122:123], v[90:91]
	v_mov_b64_e32 v[120:121], v[88:89]
	v_mov_b64_e32 v[118:119], v[86:87]
	v_mov_b64_e32 v[116:117], v[84:85]
	v_mov_b64_e32 v[114:115], v[82:83]
	v_mov_b32_e32 v134, v181
	v_mov_b32_e32 v135, v181
	v_mfma_f32_32x32x64_f8f6f4 v[114:129], v[26:33], v[154:161], v[114:129]
	v_mov_b32_e32 v136, v181
	v_mov_b32_e32 v137, v181
	v_cvt_pk_fp8_f32 v134, v34, v35
	v_cvt_pk_fp8_f32 v135, v38, v39
	v_cvt_pk_fp8_f32 v136, v42, v43
	v_cvt_pk_fp8_f32 v137, v46, v47
	v_cvt_pk_fp8_f32 v134, v36, v37 op_sel:[0,0,1]
	v_cvt_pk_fp8_f32 v135, v40, v41 op_sel:[0,0,1]
	v_cvt_pk_fp8_f32 v136, v44, v45 op_sel:[0,0,1]
	v_cvt_pk_fp8_f32 v137, v48, v49 op_sel:[0,0,1]
	s_nop 0
	ds_read_b128 v[138:141], v188 offset:0x800
	ds_read_b128 v[142:145], v189 offset:0x800
	s_nop 0
	v_mfma_f32_16x16x128_f8f6f4 v[18:21], v[130:137], v[146:153], 0
	s_add_i32 s38, s37, 0x2000
	v_add_u32_e32 v205, s38, v194
	s_add_i32 s38, s37, 0x6000
	v_add_u32_e32 v203, s38, v194
	s_add_i32 s38, s37, 0x3000
	s_waitcnt vmcnt(0) lgkmcnt(0)
	s_barrier
	v_add_u32_e32 v201, s38, v194
	s_add_i32 s38, s37, 0x8000
	s_add_i32 s37, s37, 0xa000
	v_add_u32_e32 v199, s38, v194
	v_add_u32_e32 v196, s37, v194
	v_mov_b64_e32 v[48:49], v[16:17]
	v_mov_b64_e32 v[64:65], v[16:17]
	v_mov_b64_e32 v[80:81], v[16:17]
	v_add_u32_e32 v206, v205, v195
	v_add_u32_e32 v204, v203, v195
	v_add_u32_e32 v202, v201, v195
	v_add_u32_e32 v200, v199, v195
	v_add_u32_e32 v197, v196, v195
	s_mov_b32 s37, -2
	v_mov_b64_e32 v[46:47], v[14:15]
	v_mov_b64_e32 v[44:45], v[12:13]
	v_mov_b64_e32 v[42:43], v[10:11]
	v_mov_b64_e32 v[40:41], v[8:9]
	v_mov_b64_e32 v[38:39], v[6:7]
	v_mov_b64_e32 v[36:37], v[4:5]
	v_mov_b64_e32 v[34:35], v[2:3]
	v_mov_b64_e32 v[62:63], v[14:15]
	v_mov_b64_e32 v[60:61], v[12:13]
	v_mov_b64_e32 v[58:59], v[10:11]
	v_mov_b64_e32 v[56:57], v[8:9]
	v_mov_b64_e32 v[54:55], v[6:7]
	v_mov_b64_e32 v[52:53], v[4:5]
	v_mov_b64_e32 v[50:51], v[2:3]
	v_mov_b64_e32 v[78:79], v[14:15]
	v_mov_b64_e32 v[76:77], v[12:13]
	v_mov_b64_e32 v[74:75], v[10:11]
	v_mov_b64_e32 v[72:73], v[8:9]
	v_mov_b64_e32 v[70:71], v[6:7]
	v_mov_b64_e32 v[68:69], v[4:5]
	v_mov_b64_e32 v[66:67], v[2:3]
	s_branch .LBB0_1215
.LBB0_1213:
	s_or_b64 exec, exec, s[38:39]
	s_waitcnt lgkmcnt(0)
	v_add_u32_e32 v166, s78, v186
	ds_read_b128 v[138:141], v166 offset:49248
	ds_read_b128 v[142:145], v166 offset:49216
	ds_read_b128 v[162:165], v166 offset:49184
	ds_read_b128 v[166:169], v166 offset:49152
	ds_read_b128 v[244:247], v250 offset:49152
	s_waitcnt lgkmcnt(0)
	v_pk_mul_f32 v[14:15], v[14:15], v[138:139]
	v_pk_mul_f32 v[10:11], v[10:11], v[142:143]
	v_pk_mul_f32 v[6:7], v[6:7], v[162:163]
	v_pk_mul_f32 v[16:17], v[16:17], v[140:141]
	v_pk_mul_f32 v[12:13], v[12:13], v[144:145]
	v_pk_mul_f32 v[8:9], v[8:9], v[164:165]
	v_pk_mul_f32 v[4:5], v[4:5], v[168:169]
	v_pk_mul_f32 v[2:3], v[2:3], v[166:167]
	v_pk_mul_f32 v[46:47], v[46:47], v[138:139]
	v_pk_mul_f32 v[42:43], v[42:43], v[142:143]
	v_pk_mul_f32 v[38:39], v[38:39], v[162:163]
	v_pk_mul_f32 v[48:49], v[48:49], v[140:141]
	v_pk_mul_f32 v[44:45], v[44:45], v[144:145]
	v_pk_mul_f32 v[40:41], v[40:41], v[164:165]
	v_pk_mul_f32 v[36:37], v[36:37], v[168:169]
	v_pk_mul_f32 v[34:35], v[34:35], v[166:167]
	v_pk_mul_f32 v[62:63], v[62:63], v[138:139]
	v_pk_mul_f32 v[58:59], v[58:59], v[142:143]
	v_pk_mul_f32 v[54:55], v[54:55], v[162:163]
	v_pk_mul_f32 v[64:65], v[64:65], v[140:141]
	v_pk_mul_f32 v[60:61], v[60:61], v[144:145]
	v_pk_mul_f32 v[56:57], v[56:57], v[164:165]
	v_pk_mul_f32 v[52:53], v[52:53], v[168:169]
	v_pk_mul_f32 v[50:51], v[50:51], v[166:167]
	v_pk_mul_f32 v[78:79], v[78:79], v[138:139]
	v_pk_mul_f32 v[74:75], v[74:75], v[142:143]
	v_pk_mul_f32 v[70:71], v[70:71], v[162:163]
	v_pk_mul_f32 v[80:81], v[80:81], v[140:141]
	v_pk_mul_f32 v[76:77], v[76:77], v[144:145]
	v_pk_mul_f32 v[72:73], v[72:73], v[164:165]
	v_pk_mul_f32 v[68:69], v[68:69], v[168:169]
	v_pk_mul_f32 v[66:67], v[66:67], v[166:167]
	v_pk_mul_f32 v[18:19], v[18:19], v[244:245]
	v_pk_mul_f32 v[20:21], v[20:21], v[246:247]
.LBB0_1214:
	v_cvt_pk_fp8_f32 v130, v98, v99
	v_cvt_pk_fp8_f32 v131, v102, v103
	ds_read_b128 v[138:141], v207 offset:0
	ds_read_b128 v[142:145], v209 offset:0
	ds_read_b128 v[162:165], v207 offset:0x800
	ds_read_b128 v[166:169], v209 offset:0x800
	v_cvt_pk_fp8_f32 v130, v100, v101 op_sel:[0,0,1]
	v_cvt_pk_fp8_f32 v131, v104, v105 op_sel:[0,0,1]
	s_waitcnt lgkmcnt(2)
	v_cvt_pk_fp8_f32 v132, v106, v107
	v_cvt_pk_fp8_f32 v133, v110, v111
	ds_read_b128 v[170:173], v188 offset:0
	ds_read_b128 v[174:177], v189 offset:0
	v_cvt_pk_fp8_f32 v132, v108, v109 op_sel:[0,0,1]
	v_cvt_pk_fp8_f32 v133, v112, v113 op_sel:[0,0,1]
	v_mfma_f32_32x32x64_f8f6f4 v[98:113], v[138:145], v[154:161], v[82:97]
	s_waitcnt lgkmcnt(2)
	v_cvt_pk_fp8_f32 v134, v114, v115
	v_cvt_pk_fp8_f32 v135, v118, v119
	v_cvt_pk_fp8_f32 v136, v122, v123
	v_cvt_pk_fp8_f32 v137, v126, v127
	v_cvt_pk_fp8_f32 v134, v116, v117 op_sel:[0,0,1]
	v_cvt_pk_fp8_f32 v135, v120, v121 op_sel:[0,0,1]
	v_cvt_pk_fp8_f32 v136, v124, v125 op_sel:[0,0,1]
	v_cvt_pk_fp8_f32 v137, v128, v129 op_sel:[0,0,1]
	v_mfma_f32_32x32x64_f8f6f4 v[114:129], v[162:169], v[154:161], v[82:97]
	ds_read_b128 v[138:141], v188 offset:0x800
	ds_read_b128 v[142:145], v189 offset:0x800
	s_nop 0
	v_mfma_f32_16x16x128_f8f6f4 v[18:21], v[130:137], v[146:153], v[18:21]
	s_waitcnt vmcnt(0) lgkmcnt(0)
	s_barrier
	s_add_i32 s37, s37, 4
	s_cmpk_lt_u32 s37, 0xfb
	s_cbranch_scc0 .LBB0_1242

.LBB0_1218:
	s_waitcnt lgkmcnt(2)
	v_mfma_f32_32x32x64_f8f6f4 v[34:49], v[130:137], v[138:145], v[34:49]
	ds_read_b128 v[138:141], v188 offset:0x1800
	ds_read_b128 v[142:145], v189 offset:0x1800
	v_exp_f32_e32 v98, v98
	v_exp_f32_e32 v99, v99
	v_exp_f32_e32 v100, v100
	v_exp_f32_e32 v101, v101
	v_exp_f32_e32 v102, v102
	v_exp_f32_e32 v103, v103
	v_exp_f32_e32 v104, v104
	v_exp_f32_e32 v105, v105
	v_exp_f32_e32 v106, v106
	v_exp_f32_e32 v107, v107
	v_exp_f32_e32 v108, v108
	s_waitcnt lgkmcnt(2)
	v_mfma_f32_32x32x64_f8f6f4 v[50:65], v[130:137], v[162:169], v[50:65]
	v_exp_f32_e32 v109, v109
	v_exp_f32_e32 v110, v110
	v_exp_f32_e32 v111, v111
	v_exp_f32_e32 v112, v112
	v_exp_f32_e32 v113, v113
	v_exp_f32_e32 v114, v114
	v_exp_f32_e32 v115, v115
	v_exp_f32_e32 v116, v116
	v_exp_f32_e32 v117, v117
	v_exp_f32_e32 v118, v118
	v_exp_f32_e32 v119, v119
	s_waitcnt lgkmcnt(0)
	v_mfma_f32_32x32x64_f8f6f4 v[66:81], v[130:137], v[138:145], v[66:81]
	v_exp_f32_e32 v120, v120
	v_exp_f32_e32 v121, v121
	v_exp_f32_e32 v122, v122
	v_exp_f32_e32 v123, v123
	v_exp_f32_e32 v124, v124
	v_exp_f32_e32 v125, v125
	v_exp_f32_e32 v126, v126
	v_exp_f32_e32 v127, v127
	v_exp_f32_e32 v128, v128
	v_exp_f32_e32 v129, v129
	s_andn2_b64 vcc, exec, s[38:39]
	s_cbranch_vccnz .LBB0_1222
	s_and_saveexec_b64 s[38:39], s[6:7]
	ds_write_b32 v187, v170 offset:49152
	s_or_b64 exec, exec, s[38:39]
	s_waitcnt lgkmcnt(0)
	v_add_u32_e32 v166, s78, v186
	ds_read_b128 v[138:141], v166 offset:49248
	ds_read_b128 v[142:145], v166 offset:49216
	ds_read_b128 v[162:165], v166 offset:49184
	ds_read_b128 v[166:169], v166 offset:49152
	ds_read_b128 v[244:247], v250 offset:49152
	s_waitcnt lgkmcnt(0)
	v_pk_mul_f32 v[14:15], v[14:15], v[138:139]
	v_pk_mul_f32 v[10:11], v[10:11], v[142:143]
	v_pk_mul_f32 v[6:7], v[6:7], v[162:163]
	v_pk_mul_f32 v[16:17], v[16:17], v[140:141]
	v_pk_mul_f32 v[12:13], v[12:13], v[144:145]
	v_pk_mul_f32 v[8:9], v[8:9], v[164:165]
	v_pk_mul_f32 v[4:5], v[4:5], v[168:169]
	v_pk_mul_f32 v[2:3], v[2:3], v[166:167]
	v_pk_mul_f32 v[46:47], v[46:47], v[138:139]
	v_pk_mul_f32 v[42:43], v[42:43], v[142:143]
	v_pk_mul_f32 v[38:39], v[38:39], v[162:163]
	v_pk_mul_f32 v[48:49], v[48:49], v[140:141]
	v_pk_mul_f32 v[44:45], v[44:45], v[144:145]
	v_pk_mul_f32 v[40:41], v[40:41], v[164:165]
	v_pk_mul_f32 v[36:37], v[36:37], v[168:169]
	v_pk_mul_f32 v[34:35], v[34:35], v[166:167]
	v_pk_mul_f32 v[62:63], v[62:63], v[138:139]
	v_pk_mul_f32 v[58:59], v[58:59], v[142:143]
	v_pk_mul_f32 v[54:55], v[54:55], v[162:163]
	v_pk_mul_f32 v[64:65], v[64:65], v[140:141]
	v_pk_mul_f32 v[60:61], v[60:61], v[144:145]
	v_pk_mul_f32 v[56:57], v[56:57], v[164:165]
	v_pk_mul_f32 v[52:53], v[52:53], v[168:169]
	v_pk_mul_f32 v[50:51], v[50:51], v[166:167]
	v_pk_mul_f32 v[78:79], v[78:79], v[138:139]
	v_pk_mul_f32 v[74:75], v[74:75], v[142:143]
	v_pk_mul_f32 v[70:71], v[70:71], v[162:163]
	v_pk_mul_f32 v[80:81], v[80:81], v[140:141]
	v_pk_mul_f32 v[76:77], v[76:77], v[144:145]
	v_pk_mul_f32 v[72:73], v[72:73], v[164:165]
	v_pk_mul_f32 v[68:69], v[68:69], v[168:169]
	v_pk_mul_f32 v[66:67], v[66:67], v[166:167]
	v_pk_mul_f32 v[18:19], v[18:19], v[244:245]
	v_pk_mul_f32 v[20:21], v[20:21], v[246:247]
.LBB0_1222:
	v_cvt_pk_fp8_f32 v130, v98, v99
	v_cvt_pk_fp8_f32 v131, v102, v103
	ds_read_b128 v[138:141], v205 offset:0
	ds_read_b128 v[142:145], v206 offset:0
	ds_read_b128 v[170:173], v205 offset:0x800
	ds_read_b128 v[174:177], v206 offset:0x800
	v_cvt_pk_fp8_f32 v130, v100, v101 op_sel:[0,0,1]
	v_cvt_pk_fp8_f32 v131, v104, v105 op_sel:[0,0,1]
	s_waitcnt lgkmcnt(2)
	v_cvt_pk_fp8_f32 v132, v106, v107
	v_cvt_pk_fp8_f32 v133, v110, v111
	ds_read_b128 v[210:213], v203 offset:0
	ds_read_b128 v[214:217], v204 offset:0
	v_cvt_pk_fp8_f32 v132, v108, v109 op_sel:[0,0,1]
	v_cvt_pk_fp8_f32 v133, v112, v113 op_sel:[0,0,1]
	v_mfma_f32_32x32x64_f8f6f4 v[98:113], v[138:145], v[154:161], v[82:97]
	s_waitcnt lgkmcnt(2)
	v_cvt_pk_fp8_f32 v134, v114, v115
	v_cvt_pk_fp8_f32 v135, v118, v119
	v_cvt_pk_fp8_f32 v136, v122, v123
	v_cvt_pk_fp8_f32 v137, v126, v127
	v_cvt_pk_fp8_f32 v134, v116, v117 op_sel:[0,0,1]
	v_cvt_pk_fp8_f32 v135, v120, v121 op_sel:[0,0,1]
	v_cvt_pk_fp8_f32 v136, v124, v125 op_sel:[0,0,1]
	v_cvt_pk_fp8_f32 v137, v128, v129 op_sel:[0,0,1]
	v_mfma_f32_32x32x64_f8f6f4 v[114:129], v[170:177], v[154:161], v[82:97]
	ds_read_b128 v[162:165], v203 offset:0x800
	ds_read_b128 v[166:169], v204 offset:0x800
	s_nop 0
	v_mfma_f32_16x16x128_f8f6f4 v[18:21], v[130:137], v[146:153], v[18:21]
	s_waitcnt vmcnt(0) lgkmcnt(0)
	s_barrier
	s_waitcnt lgkmcnt(2)
	v_mfma_f32_32x32x64_f8f6f4 v[2:17], v[130:137], v[210:217], v[2:17]
	ds_read_b128 v[138:141], v203 offset:0x1000
	ds_read_b128 v[142:145], v204 offset:0x1000
	v_max3_f32 v170, v98, v99, v100
	v_max3_f32 v170, v170, v101, v102
	v_max3_f32 v170, v170, v103, v104
	v_max3_f32 v170, v170, v105, v106
	v_max3_f32 v170, v170, v107, v108
	v_max3_f32 v170, v170, v109, v110
	v_max3_f32 v170, v170, v111, v112
	v_max_f32 v170, v170, v113
	s_nop 0
	v_max3_f32 v170, v170, v114, v115
	v_max3_f32 v170, v170, v116, v117
	v_max3_f32 v170, v170, v118, v119
	v_max3_f32 v170, v170, v120, v121
	v_max3_f32 v170, v170, v122, v123
	v_max3_f32 v170, v170, v124, v125
	v_max3_f32 v170, v170, v126, v127
	v_max3_f32 v170, v170, v128, v129
	v_mov_b32 v171, v170
	s_nop 1
	v_permlane32_swap_b32 v170, v171
	v_max_f32 v170, v170, v171
	s_nop 0
	v_cmp_ge_f32_e32 vcc, s54, v170
	s_cmp_lg_u64 vcc, exec
	s_cselect_b64 s[38:39], -1, 0
	s_cmp_eq_u64 vcc, exec
	s_cbranch_scc1 .LBB0_1224
	s_nop 4
	v_add_f32_e32 v82, 0xc0c00000, v170
	v_max_f32_e32 v82, 0, v82
	v_exp_f32_e64 v170, -v82
	v_add_f32_e32 v198, v198, v82
	v_sub_f32_e32 v98, v98, v82
	v_sub_f32_e32 v114, v114, v82
	v_sub_f32_e32 v99, v99, v82
	v_sub_f32_e32 v115, v115, v82
	v_sub_f32_e32 v100, v100, v82
	v_sub_f32_e32 v116, v116, v82
	v_sub_f32_e32 v101, v101, v82
	v_sub_f32_e32 v117, v117, v82
	v_sub_f32_e32 v102, v102, v82
	v_sub_f32_e32 v118, v118, v82
	v_sub_f32_e32 v103, v103, v82
	v_sub_f32_e32 v119, v119, v82
	v_sub_f32_e32 v104, v104, v82
	v_sub_f32_e32 v120, v120, v82
	v_sub_f32_e32 v105, v105, v82
	v_sub_f32_e32 v121, v121, v82
	v_sub_f32_e32 v106, v106, v82
	v_sub_f32_e32 v122, v122, v82
	v_sub_f32_e32 v107, v107, v82
	v_sub_f32_e32 v123, v123, v82
	v_sub_f32_e32 v108, v108, v82
	v_sub_f32_e32 v124, v124, v82
	v_sub_f32_e32 v109, v109, v82
	v_sub_f32_e32 v125, v125, v82
	v_sub_f32_e32 v110, v110, v82
	v_sub_f32_e32 v126, v126, v82
	v_sub_f32_e32 v111, v111, v82
	v_sub_f32_e32 v127, v127, v82
	v_sub_f32_e32 v112, v112, v82
	v_sub_f32_e32 v128, v128, v82
	v_sub_f32_e32 v113, v113, v82
	v_sub_f32_e32 v129, v129, v82
	v_xor_b32_e32 v82, 0x80000000, v198
	v_mov_b32_e32 v83, v82
	v_mov_b32_e32 v84, v82
	v_mov_b32_e32 v85, v82
	v_mov_b32_e32 v86, v82
	v_mov_b32_e32 v87, v82
	v_mov_b32_e32 v88, v82
	v_mov_b32_e32 v89, v82
	v_mov_b32_e32 v90, v82
	v_mov_b32_e32 v91, v82
	v_mov_b32_e32 v92, v82
	v_mov_b32_e32 v93, v82
	v_mov_b32_e32 v94, v82
	v_mov_b32_e32 v95, v82
	v_mov_b32_e32 v96, v82
	v_mov_b32_e32 v97, v82
	s_branch .LBB0_1225

.LBB0_1225:
	s_waitcnt lgkmcnt(2)
	v_mfma_f32_32x32x64_f8f6f4 v[34:49], v[130:137], v[162:169], v[34:49]
	ds_read_b128 v[162:165], v203 offset:0x1800
	ds_read_b128 v[166:169], v204 offset:0x1800
	v_exp_f32_e32 v98, v98
	v_exp_f32_e32 v99, v99
	v_exp_f32_e32 v100, v100
	v_exp_f32_e32 v101, v101
	v_exp_f32_e32 v102, v102
	v_exp_f32_e32 v103, v103
	v_exp_f32_e32 v104, v104
	v_exp_f32_e32 v105, v105
	v_exp_f32_e32 v106, v106
	v_exp_f32_e32 v107, v107
	v_exp_f32_e32 v108, v108
	s_waitcnt lgkmcnt(2)
	v_mfma_f32_32x32x64_f8f6f4 v[50:65], v[130:137], v[138:145], v[50:65]
	v_exp_f32_e32 v109, v109
	v_exp_f32_e32 v110, v110
	v_exp_f32_e32 v111, v111
	v_exp_f32_e32 v112, v112
	v_exp_f32_e32 v113, v113
	v_exp_f32_e32 v114, v114
	v_exp_f32_e32 v115, v115
	v_exp_f32_e32 v116, v116
	v_exp_f32_e32 v117, v117
	v_exp_f32_e32 v118, v118
	v_exp_f32_e32 v119, v119
	s_waitcnt lgkmcnt(0)
	v_mfma_f32_32x32x64_f8f6f4 v[66:81], v[130:137], v[162:169], v[66:81]
	v_exp_f32_e32 v120, v120
	v_exp_f32_e32 v121, v121
	v_exp_f32_e32 v122, v122
	v_exp_f32_e32 v123, v123
	v_exp_f32_e32 v124, v124
	v_exp_f32_e32 v125, v125
	v_exp_f32_e32 v126, v126
	v_exp_f32_e32 v127, v127
	v_exp_f32_e32 v128, v128
	v_exp_f32_e32 v129, v129
	s_andn2_b64 vcc, exec, s[38:39]
	s_cbranch_vccnz .LBB0_1229
	s_and_saveexec_b64 s[38:39], s[6:7]
	ds_write_b32 v187, v170 offset:49152
	s_or_b64 exec, exec, s[38:39]
	s_waitcnt lgkmcnt(0)
	v_add_u32_e32 v166, s78, v186
	ds_read_b128 v[138:141], v166 offset:49248
	ds_read_b128 v[142:145], v166 offset:49216
	ds_read_b128 v[162:165], v166 offset:49184
	ds_read_b128 v[166:169], v166 offset:49152
	ds_read_b128 v[244:247], v250 offset:49152
	s_waitcnt lgkmcnt(0)
	v_pk_mul_f32 v[14:15], v[14:15], v[138:139]
	v_pk_mul_f32 v[10:11], v[10:11], v[142:143]
	v_pk_mul_f32 v[6:7], v[6:7], v[162:163]
	v_pk_mul_f32 v[16:17], v[16:17], v[140:141]
	v_pk_mul_f32 v[12:13], v[12:13], v[144:145]
	v_pk_mul_f32 v[8:9], v[8:9], v[164:165]
	v_pk_mul_f32 v[4:5], v[4:5], v[168:169]
	v_pk_mul_f32 v[2:3], v[2:3], v[166:167]
	v_pk_mul_f32 v[46:47], v[46:47], v[138:139]
	v_pk_mul_f32 v[42:43], v[42:43], v[142:143]
	v_pk_mul_f32 v[38:39], v[38:39], v[162:163]
	v_pk_mul_f32 v[48:49], v[48:49], v[140:141]
	v_pk_mul_f32 v[44:45], v[44:45], v[144:145]
	v_pk_mul_f32 v[40:41], v[40:41], v[164:165]
	v_pk_mul_f32 v[36:37], v[36:37], v[168:169]
	v_pk_mul_f32 v[34:35], v[34:35], v[166:167]
	v_pk_mul_f32 v[62:63], v[62:63], v[138:139]
	v_pk_mul_f32 v[58:59], v[58:59], v[142:143]
	v_pk_mul_f32 v[54:55], v[54:55], v[162:163]
	v_pk_mul_f32 v[64:65], v[64:65], v[140:141]
	v_pk_mul_f32 v[60:61], v[60:61], v[144:145]
	v_pk_mul_f32 v[56:57], v[56:57], v[164:165]
	v_pk_mul_f32 v[52:53], v[52:53], v[168:169]
	v_pk_mul_f32 v[50:51], v[50:51], v[166:167]
	v_pk_mul_f32 v[78:79], v[78:79], v[138:139]
	v_pk_mul_f32 v[74:75], v[74:75], v[142:143]
	v_pk_mul_f32 v[70:71], v[70:71], v[162:163]
	v_pk_mul_f32 v[80:81], v[80:81], v[140:141]
	v_pk_mul_f32 v[76:77], v[76:77], v[144:145]
	v_pk_mul_f32 v[72:73], v[72:73], v[164:165]
	v_pk_mul_f32 v[68:69], v[68:69], v[168:169]
	v_pk_mul_f32 v[66:67], v[66:67], v[166:167]
	v_pk_mul_f32 v[18:19], v[18:19], v[244:245]
	v_pk_mul_f32 v[20:21], v[20:21], v[246:247]
.LBB0_1229:
	v_cvt_pk_fp8_f32 v130, v98, v99
	v_cvt_pk_fp8_f32 v131, v102, v103
	ds_read_b128 v[138:141], v201 offset:0
	ds_read_b128 v[142:145], v202 offset:0
	ds_read_b128 v[170:173], v201 offset:0x800
	ds_read_b128 v[174:177], v202 offset:0x800
	v_cvt_pk_fp8_f32 v130, v100, v101 op_sel:[0,0,1]
	v_cvt_pk_fp8_f32 v131, v104, v105 op_sel:[0,0,1]
	s_waitcnt lgkmcnt(2)
	v_cvt_pk_fp8_f32 v132, v106, v107
	v_cvt_pk_fp8_f32 v133, v110, v111
	ds_read_b128 v[210:213], v199 offset:0
	ds_read_b128 v[214:217], v200 offset:0
	v_cvt_pk_fp8_f32 v132, v108, v109 op_sel:[0,0,1]
	v_cvt_pk_fp8_f32 v133, v112, v113 op_sel:[0,0,1]
	v_mfma_f32_32x32x64_f8f6f4 v[98:113], v[138:145], v[154:161], v[82:97]
	s_waitcnt lgkmcnt(2)
	v_cvt_pk_fp8_f32 v134, v114, v115
	v_cvt_pk_fp8_f32 v135, v118, v119
	v_cvt_pk_fp8_f32 v136, v122, v123
	v_cvt_pk_fp8_f32 v137, v126, v127
	v_cvt_pk_fp8_f32 v134, v116, v117 op_sel:[0,0,1]
	v_cvt_pk_fp8_f32 v135, v120, v121 op_sel:[0,0,1]
	v_cvt_pk_fp8_f32 v136, v124, v125 op_sel:[0,0,1]
	v_cvt_pk_fp8_f32 v137, v128, v129 op_sel:[0,0,1]
	v_mfma_f32_32x32x64_f8f6f4 v[114:129], v[170:177], v[154:161], v[82:97]
	ds_read_b128 v[162:165], v199 offset:0x800
	ds_read_b128 v[166:169], v200 offset:0x800
	s_nop 0
	v_mfma_f32_16x16x128_f8f6f4 v[18:21], v[130:137], v[146:153], v[18:21]
	s_waitcnt vmcnt(0) lgkmcnt(0)
	s_barrier
	s_waitcnt lgkmcnt(2)
	v_mfma_f32_32x32x64_f8f6f4 v[2:17], v[130:137], v[210:217], v[2:17]
	ds_read_b128 v[138:141], v199 offset:0x1000
	ds_read_b128 v[142:145], v200 offset:0x1000
	v_max3_f32 v170, v98, v99, v100
	v_max3_f32 v170, v170, v101, v102
	v_max3_f32 v170, v170, v103, v104
	v_max3_f32 v170, v170, v105, v106
	v_max3_f32 v170, v170, v107, v108
	v_max3_f32 v170, v170, v109, v110
	v_max3_f32 v170, v170, v111, v112
	v_max_f32 v170, v170, v113
	s_nop 0
	v_max3_f32 v170, v170, v114, v115
	v_max3_f32 v170, v170, v116, v117
	v_max3_f32 v170, v170, v118, v119
	v_max3_f32 v170, v170, v120, v121
	v_max3_f32 v170, v170, v122, v123
	v_max3_f32 v170, v170, v124, v125
	v_max3_f32 v170, v170, v126, v127
	v_max3_f32 v170, v170, v128, v129
	v_mov_b32 v171, v170
	s_nop 1
	v_permlane32_swap_b32 v170, v171
	v_max_f32 v170, v170, v171
	s_nop 0
	v_cmp_ge_f32_e32 vcc, s54, v170
	s_cmp_lg_u64 vcc, exec
	s_cselect_b64 s[38:39], -1, 0
	s_cmp_eq_u64 vcc, exec
	s_cbranch_scc1 .LBB0_1231
	s_nop 4
	v_add_f32_e32 v82, 0xc0c00000, v170
	v_max_f32_e32 v82, 0, v82
	v_exp_f32_e64 v170, -v82
	v_add_f32_e32 v198, v198, v82
	v_sub_f32_e32 v98, v98, v82
	v_sub_f32_e32 v114, v114, v82
	v_sub_f32_e32 v99, v99, v82
	v_sub_f32_e32 v115, v115, v82
	v_sub_f32_e32 v100, v100, v82
	v_sub_f32_e32 v116, v116, v82
	v_sub_f32_e32 v101, v101, v82
	v_sub_f32_e32 v117, v117, v82
	v_sub_f32_e32 v102, v102, v82
	v_sub_f32_e32 v118, v118, v82
	v_sub_f32_e32 v103, v103, v82
	v_sub_f32_e32 v119, v119, v82
	v_sub_f32_e32 v104, v104, v82
	v_sub_f32_e32 v120, v120, v82
	v_sub_f32_e32 v105, v105, v82
	v_sub_f32_e32 v121, v121, v82
	v_sub_f32_e32 v106, v106, v82
	v_sub_f32_e32 v122, v122, v82
	v_sub_f32_e32 v107, v107, v82
	v_sub_f32_e32 v123, v123, v82
	v_sub_f32_e32 v108, v108, v82
	v_sub_f32_e32 v124, v124, v82
	v_sub_f32_e32 v109, v109, v82
	v_sub_f32_e32 v125, v125, v82
	v_sub_f32_e32 v110, v110, v82
	v_sub_f32_e32 v126, v126, v82
	v_sub_f32_e32 v111, v111, v82
	v_sub_f32_e32 v127, v127, v82
	v_sub_f32_e32 v112, v112, v82
	v_sub_f32_e32 v128, v128, v82
	v_sub_f32_e32 v113, v113, v82
	v_sub_f32_e32 v129, v129, v82
	v_xor_b32_e32 v82, 0x80000000, v198
	v_mov_b32_e32 v83, v82
	v_mov_b32_e32 v84, v82
	v_mov_b32_e32 v85, v82
	v_mov_b32_e32 v86, v82
	v_mov_b32_e32 v87, v82
	v_mov_b32_e32 v88, v82
	v_mov_b32_e32 v89, v82
	v_mov_b32_e32 v90, v82
	v_mov_b32_e32 v91, v82
	v_mov_b32_e32 v92, v82
	v_mov_b32_e32 v93, v82
	v_mov_b32_e32 v94, v82
	v_mov_b32_e32 v95, v82
	v_mov_b32_e32 v96, v82
	v_mov_b32_e32 v97, v82
	s_branch .LBB0_1232

.LBB0_1232:
	s_waitcnt lgkmcnt(2)
	v_mfma_f32_32x32x64_f8f6f4 v[34:49], v[130:137], v[162:169], v[34:49]
	ds_read_b128 v[162:165], v199 offset:0x1800
	ds_read_b128 v[166:169], v200 offset:0x1800
	v_exp_f32_e32 v98, v98
	v_exp_f32_e32 v99, v99
	v_exp_f32_e32 v100, v100
	v_exp_f32_e32 v101, v101
	v_exp_f32_e32 v102, v102
	v_exp_f32_e32 v103, v103
	v_exp_f32_e32 v104, v104
	v_exp_f32_e32 v105, v105
	v_exp_f32_e32 v106, v106
	v_exp_f32_e32 v107, v107
	v_exp_f32_e32 v108, v108
	s_waitcnt lgkmcnt(2)
	v_mfma_f32_32x32x64_f8f6f4 v[50:65], v[130:137], v[138:145], v[50:65]
	v_exp_f32_e32 v109, v109
	v_exp_f32_e32 v110, v110
	v_exp_f32_e32 v111, v111
	v_exp_f32_e32 v112, v112
	v_exp_f32_e32 v113, v113
	v_exp_f32_e32 v114, v114
	v_exp_f32_e32 v115, v115
	v_exp_f32_e32 v116, v116
	v_exp_f32_e32 v117, v117
	v_exp_f32_e32 v118, v118
	v_exp_f32_e32 v119, v119
	s_waitcnt lgkmcnt(0)
	v_mfma_f32_32x32x64_f8f6f4 v[66:81], v[130:137], v[162:169], v[66:81]
	v_exp_f32_e32 v120, v120
	v_exp_f32_e32 v121, v121
	v_exp_f32_e32 v122, v122
	v_exp_f32_e32 v123, v123
	v_exp_f32_e32 v124, v124
	v_exp_f32_e32 v125, v125
	v_exp_f32_e32 v126, v126
	v_exp_f32_e32 v127, v127
	v_exp_f32_e32 v128, v128
	v_exp_f32_e32 v129, v129
	s_andn2_b64 vcc, exec, s[38:39]
	s_cbranch_vccnz .LBB0_1236
	s_and_saveexec_b64 s[38:39], s[6:7]
	ds_write_b32 v187, v170 offset:49152
	s_or_b64 exec, exec, s[38:39]
	s_waitcnt lgkmcnt(0)
	v_add_u32_e32 v166, s78, v186
	ds_read_b128 v[138:141], v166 offset:49248
	ds_read_b128 v[142:145], v166 offset:49216
	ds_read_b128 v[162:165], v166 offset:49184
	ds_read_b128 v[166:169], v166 offset:49152
	ds_read_b128 v[244:247], v250 offset:49152
	s_waitcnt lgkmcnt(0)
	v_pk_mul_f32 v[14:15], v[14:15], v[138:139]
	v_pk_mul_f32 v[10:11], v[10:11], v[142:143]
	v_pk_mul_f32 v[6:7], v[6:7], v[162:163]
	v_pk_mul_f32 v[16:17], v[16:17], v[140:141]
	v_pk_mul_f32 v[12:13], v[12:13], v[144:145]
	v_pk_mul_f32 v[8:9], v[8:9], v[164:165]
	v_pk_mul_f32 v[4:5], v[4:5], v[168:169]
	v_pk_mul_f32 v[2:3], v[2:3], v[166:167]
	v_pk_mul_f32 v[46:47], v[46:47], v[138:139]
	v_pk_mul_f32 v[42:43], v[42:43], v[142:143]
	v_pk_mul_f32 v[38:39], v[38:39], v[162:163]
	v_pk_mul_f32 v[48:49], v[48:49], v[140:141]
	v_pk_mul_f32 v[44:45], v[44:45], v[144:145]
	v_pk_mul_f32 v[40:41], v[40:41], v[164:165]
	v_pk_mul_f32 v[36:37], v[36:37], v[168:169]
	v_pk_mul_f32 v[34:35], v[34:35], v[166:167]
	v_pk_mul_f32 v[62:63], v[62:63], v[138:139]
	v_pk_mul_f32 v[58:59], v[58:59], v[142:143]
	v_pk_mul_f32 v[54:55], v[54:55], v[162:163]
	v_pk_mul_f32 v[64:65], v[64:65], v[140:141]
	v_pk_mul_f32 v[60:61], v[60:61], v[144:145]
	v_pk_mul_f32 v[56:57], v[56:57], v[164:165]
	v_pk_mul_f32 v[52:53], v[52:53], v[168:169]
	v_pk_mul_f32 v[50:51], v[50:51], v[166:167]
	v_pk_mul_f32 v[78:79], v[78:79], v[138:139]
	v_pk_mul_f32 v[74:75], v[74:75], v[142:143]
	v_pk_mul_f32 v[70:71], v[70:71], v[162:163]
	v_pk_mul_f32 v[80:81], v[80:81], v[140:141]
	v_pk_mul_f32 v[76:77], v[76:77], v[144:145]
	v_pk_mul_f32 v[72:73], v[72:73], v[164:165]
	v_pk_mul_f32 v[68:69], v[68:69], v[168:169]
	v_pk_mul_f32 v[66:67], v[66:67], v[166:167]
	v_pk_mul_f32 v[18:19], v[18:19], v[244:245]
	v_pk_mul_f32 v[20:21], v[20:21], v[246:247]
.LBB0_1236:
	v_cvt_pk_fp8_f32 v130, v98, v99
	v_cvt_pk_fp8_f32 v131, v102, v103
	ds_read_b128 v[138:141], v183 offset:0
	ds_read_b128 v[142:145], v190 offset:0
	ds_read_b128 v[170:173], v183 offset:0x800
	ds_read_b128 v[174:177], v190 offset:0x800
	v_cvt_pk_fp8_f32 v130, v100, v101 op_sel:[0,0,1]
	v_cvt_pk_fp8_f32 v131, v104, v105 op_sel:[0,0,1]
	s_waitcnt lgkmcnt(2)
	v_cvt_pk_fp8_f32 v132, v106, v107
	v_cvt_pk_fp8_f32 v133, v110, v111
	ds_read_b128 v[210:213], v196 offset:0
	ds_read_b128 v[214:217], v197 offset:0
	v_cvt_pk_fp8_f32 v132, v108, v109 op_sel:[0,0,1]
	v_cvt_pk_fp8_f32 v133, v112, v113 op_sel:[0,0,1]
	v_mfma_f32_32x32x64_f8f6f4 v[98:113], v[138:145], v[154:161], v[82:97]
	s_waitcnt lgkmcnt(2)
	v_cvt_pk_fp8_f32 v134, v114, v115
	v_cvt_pk_fp8_f32 v135, v118, v119
	v_cvt_pk_fp8_f32 v136, v122, v123
	v_cvt_pk_fp8_f32 v137, v126, v127
	v_cvt_pk_fp8_f32 v134, v116, v117 op_sel:[0,0,1]
	v_cvt_pk_fp8_f32 v135, v120, v121 op_sel:[0,0,1]
	v_cvt_pk_fp8_f32 v136, v124, v125 op_sel:[0,0,1]
	v_cvt_pk_fp8_f32 v137, v128, v129 op_sel:[0,0,1]
	v_mfma_f32_32x32x64_f8f6f4 v[114:129], v[170:177], v[154:161], v[82:97]
	ds_read_b128 v[162:165], v196 offset:0x800
	ds_read_b128 v[166:169], v197 offset:0x800
	s_nop 0
	v_mfma_f32_16x16x128_f8f6f4 v[18:21], v[130:137], v[146:153], v[18:21]
	s_waitcnt vmcnt(0) lgkmcnt(0)
	s_barrier
	s_waitcnt lgkmcnt(2)
	v_mfma_f32_32x32x64_f8f6f4 v[2:17], v[130:137], v[210:217], v[2:17]
	ds_read_b128 v[138:141], v196 offset:0x1000
	ds_read_b128 v[142:145], v197 offset:0x1000
	v_max3_f32 v170, v98, v99, v100
	v_max3_f32 v170, v170, v101, v102
	v_max3_f32 v170, v170, v103, v104
	v_max3_f32 v170, v170, v105, v106
	v_max3_f32 v170, v170, v107, v108
	v_max3_f32 v170, v170, v109, v110
	v_max3_f32 v170, v170, v111, v112
	v_max_f32 v170, v170, v113
	s_nop 0
	v_max3_f32 v170, v170, v114, v115
	v_max3_f32 v170, v170, v116, v117
	v_max3_f32 v170, v170, v118, v119
	v_max3_f32 v170, v170, v120, v121
	v_max3_f32 v170, v170, v122, v123
	v_max3_f32 v170, v170, v124, v125
	v_max3_f32 v170, v170, v126, v127
	v_max3_f32 v170, v170, v128, v129
	v_mov_b32 v171, v170
	s_nop 1
	v_permlane32_swap_b32 v170, v171
	v_max_f32 v170, v170, v171
	s_nop 0
	v_cmp_ge_f32_e32 vcc, s54, v170
	s_cmp_lg_u64 vcc, exec
	s_cselect_b64 s[38:39], -1, 0
	s_cmp_eq_u64 vcc, exec
	s_cbranch_scc1 .LBB0_1238
	s_nop 4
	v_add_f32_e32 v82, 0xc0c00000, v170
	v_max_f32_e32 v82, 0, v82
	v_exp_f32_e64 v170, -v82
	v_add_f32_e32 v198, v198, v82
	v_sub_f32_e32 v98, v98, v82
	v_sub_f32_e32 v114, v114, v82
	v_sub_f32_e32 v99, v99, v82
	v_sub_f32_e32 v115, v115, v82
	v_sub_f32_e32 v100, v100, v82
	v_sub_f32_e32 v116, v116, v82
	v_sub_f32_e32 v101, v101, v82
	v_sub_f32_e32 v117, v117, v82
	v_sub_f32_e32 v102, v102, v82
	v_sub_f32_e32 v118, v118, v82
	v_sub_f32_e32 v103, v103, v82
	v_sub_f32_e32 v119, v119, v82
	v_sub_f32_e32 v104, v104, v82
	v_sub_f32_e32 v120, v120, v82
	v_sub_f32_e32 v105, v105, v82
	v_sub_f32_e32 v121, v121, v82
	v_sub_f32_e32 v106, v106, v82
	v_sub_f32_e32 v122, v122, v82
	v_sub_f32_e32 v107, v107, v82
	v_sub_f32_e32 v123, v123, v82
	v_sub_f32_e32 v108, v108, v82
	v_sub_f32_e32 v124, v124, v82
	v_sub_f32_e32 v109, v109, v82
	v_sub_f32_e32 v125, v125, v82
	v_sub_f32_e32 v110, v110, v82
	v_sub_f32_e32 v126, v126, v82
	v_sub_f32_e32 v111, v111, v82
	v_sub_f32_e32 v127, v127, v82
	v_sub_f32_e32 v112, v112, v82
	v_sub_f32_e32 v128, v128, v82
	v_sub_f32_e32 v113, v113, v82
	v_sub_f32_e32 v129, v129, v82
	v_xor_b32_e32 v82, 0x80000000, v198
	v_mov_b32_e32 v83, v82
	v_mov_b32_e32 v84, v82
	v_mov_b32_e32 v85, v82
	v_mov_b32_e32 v86, v82
	v_mov_b32_e32 v87, v82
	v_mov_b32_e32 v88, v82
	v_mov_b32_e32 v89, v82
	v_mov_b32_e32 v90, v82
	v_mov_b32_e32 v91, v82
	v_mov_b32_e32 v92, v82
	v_mov_b32_e32 v93, v82
	v_mov_b32_e32 v94, v82
	v_mov_b32_e32 v95, v82
	v_mov_b32_e32 v96, v82
	v_mov_b32_e32 v97, v82
	s_branch .LBB0_1239

.LBB0_1256:
	v_cvt_pk_fp8_f32 v130, v98, v99
	v_cvt_pk_fp8_f32 v131, v102, v103
	ds_read_b128 v[138:141], v201 offset:0
	ds_read_b128 v[142:145], v202 offset:0
	ds_read_b128 v[170:173], v201 offset:0x800
	ds_read_b128 v[174:177], v202 offset:0x800
	v_cvt_pk_fp8_f32 v130, v100, v101 op_sel:[0,0,1]
	v_cvt_pk_fp8_f32 v131, v104, v105 op_sel:[0,0,1]
	s_waitcnt lgkmcnt(2)
	v_cvt_pk_fp8_f32 v132, v106, v107
	v_cvt_pk_fp8_f32 v133, v110, v111
	ds_read_b128 v[210:213], v199 offset:0
	ds_read_b128 v[214:217], v200 offset:0
	v_cvt_pk_fp8_f32 v132, v108, v109 op_sel:[0,0,1]
	v_cvt_pk_fp8_f32 v133, v112, v113 op_sel:[0,0,1]
	v_mfma_f32_32x32x64_f8f6f4 v[98:113], v[138:145], v[154:161], v[82:97]
	s_waitcnt lgkmcnt(2)
	v_mfma_f32_32x32x64_f8f6f4 v[82:97], v[170:177], v[154:161], v[82:97]
	v_cvt_pk_fp8_f32 v134, v114, v115
	v_cvt_pk_fp8_f32 v135, v118, v119
	v_cvt_pk_fp8_f32 v136, v122, v123
	v_cvt_pk_fp8_f32 v137, v126, v127
	v_cvt_pk_fp8_f32 v134, v116, v117 op_sel:[0,0,1]
	v_cvt_pk_fp8_f32 v135, v120, v121 op_sel:[0,0,1]
	v_cvt_pk_fp8_f32 v136, v124, v125 op_sel:[0,0,1]
	v_cvt_pk_fp8_f32 v137, v128, v129 op_sel:[0,0,1]
	s_nop 0
	ds_read_b128 v[162:165], v199 offset:0x800
	ds_read_b128 v[166:169], v200 offset:0x800
	s_nop 0
	v_mfma_f32_16x16x128_f8f6f4 v[18:21], v[130:137], v[146:153], v[18:21]
	s_waitcnt vmcnt(0) lgkmcnt(0)
	s_barrier
	s_waitcnt lgkmcnt(2)
	v_mfma_f32_32x32x64_f8f6f4 v[2:17], v[130:137], v[210:217], v[2:17]
	ds_read_b128 v[138:141], v199 offset:0x1000
	ds_read_b128 v[142:145], v200 offset:0x1000
	v_max3_f32 v114, v98, v99, v100
	v_max3_f32 v114, v114, v101, v102
	v_max3_f32 v114, v114, v103, v104
	v_max3_f32 v114, v114, v105, v106
	v_max3_f32 v114, v114, v107, v108
	v_max3_f32 v114, v114, v109, v110
	v_max3_f32 v114, v114, v111, v112
	v_max_f32 v114, v114, v113
	s_nop 0
	v_max3_f32 v114, v114, v82, v83
	v_max3_f32 v114, v114, v84, v85
	v_max3_f32 v114, v114, v86, v87
	v_max3_f32 v114, v114, v88, v89
	v_max3_f32 v114, v114, v90, v91
	v_max3_f32 v114, v114, v92, v93
	v_max3_f32 v114, v114, v94, v95
	v_max3_f32 v114, v114, v96, v97
	v_mov_b32 v115, v114
	s_nop 1
	v_permlane32_swap_b32 v114, v115
	v_max_f32 v114, v114, v115
	s_nop 0
	v_cmp_ge_f32_e32 vcc, s54, v114
	s_cmp_lg_u64 vcc, exec
	s_cselect_b64 s[38:39], -1, 0
	s_cmp_eq_u64 vcc, exec
	s_cbranch_scc1 .LBB0_1258
	v_add_f32_e32 v114, 0xc0c00000, v114
	v_max_f32_e32 v114, 0, v114
	v_exp_f32_e64 v170, -v114
	v_sub_f32_e32 v98, v98, v114
	v_sub_f32_e32 v82, v82, v114
	v_sub_f32_e32 v99, v99, v114
	v_sub_f32_e32 v83, v83, v114
	v_sub_f32_e32 v100, v100, v114
	v_sub_f32_e32 v84, v84, v114
	v_sub_f32_e32 v101, v101, v114
	v_sub_f32_e32 v85, v85, v114
	v_sub_f32_e32 v102, v102, v114
	v_sub_f32_e32 v86, v86, v114
	v_sub_f32_e32 v103, v103, v114
	v_sub_f32_e32 v87, v87, v114
	v_sub_f32_e32 v104, v104, v114
	v_sub_f32_e32 v88, v88, v114
	v_sub_f32_e32 v105, v105, v114
	v_sub_f32_e32 v89, v89, v114
	v_sub_f32_e32 v106, v106, v114
	v_sub_f32_e32 v90, v90, v114
	v_sub_f32_e32 v107, v107, v114
	v_sub_f32_e32 v91, v91, v114
	v_sub_f32_e32 v108, v108, v114
	v_sub_f32_e32 v92, v92, v114
	v_sub_f32_e32 v109, v109, v114
	v_sub_f32_e32 v93, v93, v114
	v_sub_f32_e32 v110, v110, v114
	v_sub_f32_e32 v94, v94, v114
	v_sub_f32_e32 v111, v111, v114
	v_sub_f32_e32 v95, v95, v114
	v_sub_f32_e32 v112, v112, v114
	v_sub_f32_e32 v96, v96, v114
	v_sub_f32_e32 v113, v113, v114
	v_sub_f32_e32 v97, v97, v114
	v_add_f32_e32 v114, v198, v114
	v_xor_b32_e32 v114, 0x80000000, v114
	v_mov_b32_e32 v115, v114
	v_mov_b32_e32 v116, v114
	v_mov_b32_e32 v117, v114
	v_mov_b32_e32 v118, v114
	v_mov_b32_e32 v119, v114
	v_mov_b32_e32 v120, v114
	v_mov_b32_e32 v121, v114
	v_mov_b32_e32 v122, v114
	v_mov_b32_e32 v123, v114
	v_mov_b32_e32 v124, v114
	v_mov_b32_e32 v125, v114
	v_mov_b32_e32 v126, v114
	v_mov_b32_e32 v127, v114
	v_mov_b32_e32 v128, v114
	v_mov_b32_e32 v129, v114
	s_branch .LBB0_1259

.LBB0_1259:
	s_waitcnt lgkmcnt(2)
	v_mfma_f32_32x32x64_f8f6f4 v[34:49], v[130:137], v[162:169], v[34:49]
	ds_read_b128 v[114:117], v199 offset:0x1800
	ds_read_b128 v[118:121], v200 offset:0x1800
	v_exp_f32_e32 v98, v98
	v_exp_f32_e32 v99, v99
	v_exp_f32_e32 v100, v100
	v_exp_f32_e32 v101, v101
	v_exp_f32_e32 v102, v102
	v_exp_f32_e32 v103, v103
	v_exp_f32_e32 v104, v104
	v_exp_f32_e32 v105, v105
	v_exp_f32_e32 v106, v106
	v_exp_f32_e32 v107, v107
	v_exp_f32_e32 v108, v108
	s_waitcnt lgkmcnt(2)
	v_mfma_f32_32x32x64_f8f6f4 v[50:65], v[130:137], v[138:145], v[50:65]
	v_exp_f32_e32 v109, v109
	v_exp_f32_e32 v110, v110
	v_exp_f32_e32 v111, v111
	v_exp_f32_e32 v112, v112
	v_exp_f32_e32 v113, v113
	v_exp_f32_e32 v82, v82
	v_exp_f32_e32 v83, v83
	v_exp_f32_e32 v84, v84
	v_exp_f32_e32 v85, v85
	v_exp_f32_e32 v86, v86
	v_exp_f32_e32 v87, v87
	s_waitcnt lgkmcnt(0)
	v_mfma_f32_32x32x64_f8f6f4 v[66:81], v[130:137], v[114:121], v[66:81]
	v_exp_f32_e32 v88, v88
	v_exp_f32_e32 v89, v89
	v_exp_f32_e32 v90, v90
	v_exp_f32_e32 v91, v91
	v_exp_f32_e32 v92, v92
	v_exp_f32_e32 v93, v93
	v_exp_f32_e32 v94, v94
	v_exp_f32_e32 v95, v95
	v_exp_f32_e32 v96, v96
	v_exp_f32_e32 v97, v97
	s_andn2_b64 vcc, exec, s[38:39]
	s_cbranch_vccnz .LBB0_1263
	s_and_saveexec_b64 s[38:39], s[6:7]
	ds_write_b32 v187, v170 offset:49152
	s_or_b64 exec, exec, s[38:39]
	s_waitcnt lgkmcnt(0)
	v_add_u32_e32 v126, s78, v186
	ds_read_b128 v[114:117], v126 offset:49248
	ds_read_b128 v[118:121], v126 offset:49216
	ds_read_b128 v[122:125], v126 offset:49184
	ds_read_b128 v[126:129], v126 offset:49152
	ds_read_b128 v[244:247], v250 offset:49152
	s_waitcnt lgkmcnt(0)
	v_pk_mul_f32 v[14:15], v[14:15], v[114:115]
	v_pk_mul_f32 v[10:11], v[10:11], v[118:119]
	v_pk_mul_f32 v[6:7], v[6:7], v[122:123]
	v_pk_mul_f32 v[16:17], v[16:17], v[116:117]
	v_pk_mul_f32 v[12:13], v[12:13], v[120:121]
	v_pk_mul_f32 v[8:9], v[8:9], v[124:125]
	v_pk_mul_f32 v[4:5], v[4:5], v[128:129]
	v_pk_mul_f32 v[2:3], v[2:3], v[126:127]
	v_pk_mul_f32 v[46:47], v[46:47], v[114:115]
	v_pk_mul_f32 v[42:43], v[42:43], v[118:119]
	v_pk_mul_f32 v[38:39], v[38:39], v[122:123]
	v_pk_mul_f32 v[48:49], v[48:49], v[116:117]
	v_pk_mul_f32 v[44:45], v[44:45], v[120:121]
	v_pk_mul_f32 v[40:41], v[40:41], v[124:125]
	v_pk_mul_f32 v[36:37], v[36:37], v[128:129]
	v_pk_mul_f32 v[34:35], v[34:35], v[126:127]
	v_pk_mul_f32 v[62:63], v[62:63], v[114:115]
	v_pk_mul_f32 v[58:59], v[58:59], v[118:119]
	v_pk_mul_f32 v[54:55], v[54:55], v[122:123]
	v_pk_mul_f32 v[64:65], v[64:65], v[116:117]
	v_pk_mul_f32 v[60:61], v[60:61], v[120:121]
	v_pk_mul_f32 v[56:57], v[56:57], v[124:125]
	v_pk_mul_f32 v[52:53], v[52:53], v[128:129]
	v_pk_mul_f32 v[50:51], v[50:51], v[126:127]
	v_pk_mul_f32 v[78:79], v[78:79], v[114:115]
	v_pk_mul_f32 v[74:75], v[74:75], v[118:119]
	v_pk_mul_f32 v[70:71], v[70:71], v[122:123]
	v_pk_mul_f32 v[80:81], v[80:81], v[116:117]
	v_pk_mul_f32 v[76:77], v[76:77], v[120:121]
	v_pk_mul_f32 v[72:73], v[72:73], v[124:125]
	v_pk_mul_f32 v[68:69], v[68:69], v[128:129]
	v_pk_mul_f32 v[66:67], v[66:67], v[126:127]
	v_pk_mul_f32 v[18:19], v[18:19], v[244:245]
	v_pk_mul_f32 v[20:21], v[20:21], v[246:247]
.LBB0_1263:
	v_cvt_pk_fp8_f32 v130, v98, v99
	v_cvt_pk_fp8_f32 v131, v102, v103
	v_cvt_pk_fp8_f32 v132, v106, v107
	v_cvt_pk_fp8_f32 v133, v110, v111
	v_cvt_pk_fp8_f32 v134, v82, v83
	v_cvt_pk_fp8_f32 v135, v86, v87
	v_cvt_pk_fp8_f32 v136, v90, v91
	v_cvt_pk_fp8_f32 v137, v94, v95
	v_cvt_pk_fp8_f32 v130, v100, v101 op_sel:[0,0,1]
	v_cvt_pk_fp8_f32 v131, v104, v105 op_sel:[0,0,1]
	v_cvt_pk_fp8_f32 v132, v108, v109 op_sel:[0,0,1]
	v_cvt_pk_fp8_f32 v133, v112, v113 op_sel:[0,0,1]
	v_cvt_pk_fp8_f32 v134, v84, v85 op_sel:[0,0,1]
	v_cvt_pk_fp8_f32 v135, v88, v89 op_sel:[0,0,1]
	v_cvt_pk_fp8_f32 v136, v92, v93 op_sel:[0,0,1]
	v_cvt_pk_fp8_f32 v137, v96, v97 op_sel:[0,0,1]
	ds_read_b128 v[82:85], v196 offset:0
	ds_read_b128 v[86:89], v197 offset:0
	ds_read_b128 v[90:93], v196 offset:0x800
	ds_read_b128 v[94:97], v197 offset:0x800
	ds_read_b128 v[98:101], v196 offset:0x1000
	s_nop 1
	v_mfma_f32_16x16x128_f8f6f4 v[18:21], v[130:137], v[146:153], v[18:21]
	ds_read_b128 v[102:105], v197 offset:0x1000
	s_waitcnt lgkmcnt(4)
	v_mfma_f32_32x32x64_f8f6f4 v[2:17], v[130:137], v[82:89], v[2:17]
	s_waitcnt lgkmcnt(2)
	v_mfma_f32_32x32x64_f8f6f4 v[34:49], v[130:137], v[90:97], v[34:49]
	s_nop 7
	s_nop 7
	ds_read_b128 v[82:85], v196 offset:0x1800
	ds_read_b128 v[86:89], v197 offset:0x1800
	s_waitcnt lgkmcnt(2)
	v_mfma_f32_32x32x64_f8f6f4 v[50:65], v[130:137], v[98:105], v[50:65]
	s_waitcnt lgkmcnt(0)
	v_mfma_f32_32x32x64_f8f6f4 v[66:81], v[130:137], v[82:89], v[66:81]
	s_mov_b64 s[38:39], 0
.LBB0_1264:
	s_lshl_b32 s94, s77, 8
	s_add_i32 s77, s94, 0x8000
	s_and_b64 vcc, exec, s[38:39]
	s_cbranch_vccz .LBB0_1317
	ds_read_b128 v[18:21], v183 offset:0
	ds_read_b128 v[22:25], v190 offset:0
	ds_read_b128 v[34:37], v183 offset:0x800
	ds_read_b128 v[38:41], v190 offset:0x800
	s_waitcnt lgkmcnt(0)
	s_waitcnt vmcnt(0)
	s_nop 9
	v_mfma_f32_32x32x64_f8f6f4 v[18:33], v[18:25], v[154:161], 0
	s_mov_b32 s37, s36
	s_mov_b32 s38, s36
	s_mov_b32 s39, s36
	s_mov_b32 s40, s36
	s_mov_b32 s41, s36
	s_mov_b32 s42, s36
	s_mov_b32 s43, s36
	s_mov_b32 s44, s36
	s_mov_b32 s45, s36
	s_mov_b32 s46, s36
	s_mov_b32 s47, s36
	s_mov_b32 s48, s36
	s_mov_b32 s49, s36
	s_mov_b32 s50, s36
	s_mov_b32 s51, s36
	v_mov_b64_e32 v[2:3], s[36:37]
	v_mov_b64_e32 v[4:5], s[38:39]
	v_mov_b64_e32 v[6:7], s[40:41]
	v_mov_b64_e32 v[8:9], s[42:43]
	v_mov_b64_e32 v[10:11], s[44:45]
	v_mov_b64_e32 v[12:13], s[46:47]
	v_mov_b64_e32 v[14:15], s[48:49]
	v_mov_b64_e32 v[16:17], s[50:51]
	v_max_f32_e32 v42, v19, v19
	v_max_f32_e32 v43, v18, v18
	v_max_f32_e32 v42, v43, v42
	v_max3_f32 v42, v42, v20, v21
	v_max3_f32 v42, v42, v22, v23
	v_max3_f32 v42, v42, v24, v25
	v_max3_f32 v42, v42, v26, v27
	v_max3_f32 v42, v42, v28, v29
	v_max3_f32 v50, v42, v30, v31
	v_mfma_f32_32x32x64_f8f6f4 v[34:49], v[34:41], v[154:161], 0
	v_max3_f32 v50, v50, v32, v33
	s_lshl_b32 s45, s81, 10
	s_lshl_b32 s46, s80, 10
	s_cmp_lg_u32 0, -1
	s_cselect_b32 s38, 0, 0
	s_add_i32 s37, s38, 0x2000
	s_add_i32 s39, s38, 0x3000
	s_add_i32 s6, s38, 0x1000
	v_add_u32_e32 v203, s37, v194
	s_add_i32 s37, s38, 0x6000
	v_add_u32_e32 v199, s39, v194
	s_add_i32 s39, s38, 0x8000
	s_add_i32 s38, s38, 0xa000
	v_add_u32_e32 v205, s6, v194
	v_add_u32_e32 v201, s37, v194
	s_nop 4
	v_max3_f32 v50, v50, v34, v35
	v_max3_f32 v50, v50, v36, v37
	v_max3_f32 v50, v50, v38, v39
	v_max3_f32 v50, v50, v40, v41
	v_max3_f32 v50, v50, v42, v43
	v_max3_f32 v50, v50, v44, v45
	v_max3_f32 v50, v50, v46, v47
	v_max3_f32 v50, v50, v48, v49
	v_mov_b32_e32 v51, v50
	s_nop 1
	v_permlane32_swap_b32_e32 v50, v51
	v_max_f32_e32 v51, v51, v51
	v_max_f32_e32 v50, v50, v50
	v_max_f32_e32 v50, v50, v51
	v_add_f32_e32 v198, 0xc0600000, v50
	v_add_u32_e32 v196, s39, v194
	v_add_u32_e32 v194, s38, v194
	s_lshl_b32 s38, s95, 4
	v_sub_f32_e32 v18, v18, v198
	s_and_b32 s38, s38, 0xfffffc00
	s_ashr_i32 s89, s88, 31
	v_exp_f32_e32 v114, v18
	s_or_b32 s40, s88, 0x100
	s_add_i32 s41, s94, 0x4100
	s_or_b32 s42, s88, 0x140
	s_add_i32 s43, s94, 0x4140
	v_lshl_or_b32 v18, v193, 4, s38
	s_lshl_b64 s[38:39], s[88:89], 10
	s_add_u32 s38, s38, s87
	v_xor_b32_e32 v82, 0x80000000, v198
	v_sub_f32_e32 v34, v34, v198
	v_sub_f32_e32 v19, v19, v198
	v_sub_f32_e32 v35, v35, v198
	v_sub_f32_e32 v20, v20, v198
	v_sub_f32_e32 v36, v36, v198
	v_sub_f32_e32 v21, v21, v198
	v_sub_f32_e32 v37, v37, v198
	v_sub_f32_e32 v22, v22, v198
	v_sub_f32_e32 v38, v38, v198
	v_sub_f32_e32 v23, v23, v198
	v_sub_f32_e32 v39, v39, v198
	v_sub_f32_e32 v24, v24, v198
	v_sub_f32_e32 v40, v40, v198
	v_sub_f32_e32 v25, v25, v198
	v_sub_f32_e32 v41, v41, v198
	v_sub_f32_e32 v26, v26, v198
	v_sub_f32_e32 v42, v42, v198
	v_sub_f32_e32 v27, v27, v198
	v_sub_f32_e32 v43, v43, v198
	v_sub_f32_e32 v28, v28, v198
	v_sub_f32_e32 v44, v44, v198
	v_sub_f32_e32 v29, v29, v198
	v_sub_f32_e32 v45, v45, v198
	v_sub_f32_e32 v30, v30, v198
	v_sub_f32_e32 v46, v46, v198
	v_sub_f32_e32 v31, v31, v198
	v_sub_f32_e32 v47, v47, v198
	v_sub_f32_e32 v32, v32, v198
	v_sub_f32_e32 v48, v48, v198
	v_sub_f32_e32 v33, v33, v198
	v_sub_f32_e32 v49, v49, v198
	s_addc_u32 s39, s39, s76
	v_mov_b32_e32 v83, v82
	v_mov_b32_e32 v84, v82
	v_mov_b32_e32 v85, v82
	v_mov_b32_e32 v86, v82
	v_mov_b32_e32 v87, v82
	v_mov_b32_e32 v88, v82
	v_mov_b32_e32 v89, v82
	v_mov_b32_e32 v90, v82
	v_mov_b32_e32 v91, v82
	v_mov_b32_e32 v92, v82
	v_mov_b32_e32 v93, v82
	v_mov_b32_e32 v94, v82
	v_mov_b32_e32 v95, v82
	v_mov_b32_e32 v96, v82
	v_mov_b32_e32 v97, v82
	v_exp_f32_e32 v98, v34
	v_exp_f32_e32 v115, v19
	v_exp_f32_e32 v99, v35
	v_exp_f32_e32 v116, v20
	v_exp_f32_e32 v100, v36
	v_exp_f32_e32 v117, v21
	v_exp_f32_e32 v101, v37
	v_exp_f32_e32 v118, v22
	v_exp_f32_e32 v102, v38
	v_exp_f32_e32 v119, v23
	v_exp_f32_e32 v103, v39
	v_exp_f32_e32 v120, v24
	v_exp_f32_e32 v104, v40
	v_exp_f32_e32 v121, v25
	v_exp_f32_e32 v105, v41
	v_exp_f32_e32 v122, v26
	v_exp_f32_e32 v106, v42
	v_exp_f32_e32 v123, v27
	v_exp_f32_e32 v107, v43
	v_exp_f32_e32 v124, v28
	v_exp_f32_e32 v108, v44
	v_exp_f32_e32 v125, v29
	v_exp_f32_e32 v109, v45
	v_exp_f32_e32 v126, v30
	v_exp_f32_e32 v110, v46
	v_exp_f32_e32 v127, v31
	v_exp_f32_e32 v111, v47
	v_exp_f32_e32 v128, v32
	v_exp_f32_e32 v112, v48
	v_exp_f32_e32 v129, v33
	v_exp_f32_e32 v113, v49
	v_mov_b32_e32 v19, v181
	s_add_u32 s38, s38, 0x29c30000
	s_waitcnt vmcnt(3) lgkmcnt(0)
	s_barrier
	v_lshl_add_u64 v[172:173], s[92:93], 0, v[18:19]
	s_addc_u32 s39, s39, 0
	v_add3_u32 v18, s79, v191, v192
	v_lshl_add_u64 v[174:175], s[38:39], 0, v[18:19]
	v_mov_b32_e32 v162, 0
	v_mov_b64_e32 v[48:49], v[16:17]
	v_mov_b64_e32 v[64:65], v[16:17]
	v_mov_b64_e32 v[80:81], v[16:17]
	v_mov_b64_e32 v[32:33], v[16:17]
	v_lshl_add_u64 v[170:171], s[28:29], 0, v[180:181]
	v_add_u32_e32 v206, v205, v195
	v_cmp_gt_u32_e64 s[6:7], 32, v193
	v_add_u32_e32 v204, v203, v195
	v_add_u32_e32 v202, v201, v195
	s_movk_i32 s37, 0x100
	v_add_u32_e32 v200, v199, v195
	v_add_u32_e32 v197, v196, v195
	v_add_u32_e32 v195, v194, v195
	s_mov_b32 s44, -3
	s_add_i32 s45, s45, 0
	s_add_i32 s46, s46, 0
	v_mov_b64_e32 v[46:47], v[14:15]
	v_mov_b64_e32 v[44:45], v[12:13]
	v_mov_b64_e32 v[42:43], v[10:11]
	v_mov_b64_e32 v[40:41], v[8:9]
	v_mov_b64_e32 v[38:39], v[6:7]
	v_mov_b64_e32 v[36:37], v[4:5]
	v_mov_b64_e32 v[34:35], v[2:3]
	v_mov_b64_e32 v[62:63], v[14:15]
	v_mov_b64_e32 v[60:61], v[12:13]
	v_mov_b64_e32 v[58:59], v[10:11]
	v_mov_b64_e32 v[56:57], v[8:9]
	v_mov_b64_e32 v[54:55], v[6:7]
	v_mov_b64_e32 v[52:53], v[4:5]
	v_mov_b64_e32 v[50:51], v[2:3]
	v_mov_b64_e32 v[78:79], v[14:15]
	v_mov_b64_e32 v[76:77], v[12:13]
	v_mov_b64_e32 v[74:75], v[10:11]
	v_mov_b64_e32 v[72:73], v[8:9]
	v_mov_b64_e32 v[70:71], v[6:7]
	v_mov_b64_e32 v[68:69], v[4:5]
	v_mov_b64_e32 v[66:67], v[2:3]
	v_mov_b64_e32 v[30:31], v[14:15]
	v_mov_b64_e32 v[28:29], v[12:13]
	v_mov_b64_e32 v[26:27], v[10:11]
	v_mov_b64_e32 v[24:25], v[8:9]
	v_mov_b64_e32 v[22:23], v[6:7]
	v_mov_b64_e32 v[20:21], v[4:5]
	v_mov_b64_e32 v[18:19], v[2:3]
	v_mov_b32_e32 v163, v162
	v_mov_b32_e32 v164, v162
	v_mov_b32_e32 v165, v162
	v_mov_b32_e32 v166, v162
	v_mov_b32_e32 v167, v162
	v_mov_b32_e32 v168, v162
	v_mov_b32_e32 v169, v162
	s_branch .LBB0_1268
.LBB0_1266:
	s_or_b64 exec, exec, s[38:39]
	s_waitcnt lgkmcnt(0)
	v_add_u32_e32 v142, s78, v186
	ds_read_b128 v[130:133], v142 offset:49248
	ds_read_b128 v[134:137], v142 offset:49216
	ds_read_b128 v[138:141], v142 offset:49184
	ds_read_b128 v[142:145], v142 offset:49152
	ds_read_b128 v[244:247], v250 offset:49152
	s_waitcnt lgkmcnt(0)
	v_pk_mul_f32 v[14:15], v[14:15], v[130:131]
	v_pk_mul_f32 v[10:11], v[10:11], v[134:135]
	v_pk_mul_f32 v[6:7], v[6:7], v[138:139]
	v_pk_mul_f32 v[16:17], v[16:17], v[132:133]
	v_pk_mul_f32 v[12:13], v[12:13], v[136:137]
	v_pk_mul_f32 v[8:9], v[8:9], v[140:141]
	v_pk_mul_f32 v[4:5], v[4:5], v[144:145]
	v_pk_mul_f32 v[2:3], v[2:3], v[142:143]
	v_pk_mul_f32 v[46:47], v[46:47], v[130:131]
	v_pk_mul_f32 v[42:43], v[42:43], v[134:135]
	v_pk_mul_f32 v[38:39], v[38:39], v[138:139]
	v_pk_mul_f32 v[48:49], v[48:49], v[132:133]
	v_pk_mul_f32 v[44:45], v[44:45], v[136:137]
	v_pk_mul_f32 v[40:41], v[40:41], v[140:141]
	v_pk_mul_f32 v[36:37], v[36:37], v[144:145]
	v_pk_mul_f32 v[34:35], v[34:35], v[142:143]
	v_pk_mul_f32 v[62:63], v[62:63], v[130:131]
	v_pk_mul_f32 v[58:59], v[58:59], v[134:135]
	v_pk_mul_f32 v[54:55], v[54:55], v[138:139]
	v_pk_mul_f32 v[64:65], v[64:65], v[132:133]
	v_pk_mul_f32 v[60:61], v[60:61], v[136:137]
	v_pk_mul_f32 v[56:57], v[56:57], v[140:141]
	v_pk_mul_f32 v[52:53], v[52:53], v[144:145]
	v_pk_mul_f32 v[50:51], v[50:51], v[142:143]
	v_pk_mul_f32 v[78:79], v[78:79], v[130:131]
	v_pk_mul_f32 v[74:75], v[74:75], v[134:135]
	v_pk_mul_f32 v[70:71], v[70:71], v[138:139]
	v_pk_mul_f32 v[80:81], v[80:81], v[132:133]
	v_pk_mul_f32 v[76:77], v[76:77], v[136:137]
	v_pk_mul_f32 v[72:73], v[72:73], v[140:141]
	v_pk_mul_f32 v[68:69], v[68:69], v[144:145]
	v_pk_mul_f32 v[66:67], v[66:67], v[142:143]
	v_pk_mul_f32 v[18:19], v[18:19], v[244:245]
	v_pk_mul_f32 v[20:21], v[20:21], v[246:247]

.LBB0_1268:
	s_add_i32 s49, s45, 0x3000
	v_lshl_add_u64 v[130:131], s[14:15], 0, v[174:175]
	s_mov_b32 m0, s49
	v_lshl_add_u64 v[176:177], s[14:15], 0, v[172:173]
	s_add_i32 s47, s46, 0x8000
	global_load_lds_dwordx4 v[130:131], off
	v_lshl_add_u64 v[130:131], v[176:177], 0, s[56:57]
	s_mov_b32 m0, s47
	s_add_i32 s48, s46, 0x9000
	global_load_lds_dwordx4 v[130:131], off
	v_lshl_add_u64 v[130:131], v[176:177], 0, s[58:59]
	s_mov_b32 m0, s48
	v_cvt_pk_fp8_f32 v162, v114, v115
	global_load_lds_dwordx4 v[130:131], off
	v_cvt_pk_fp8_f32 v163, v118, v119
	ds_read_b128 v[130:133], v205 offset:0
	ds_read_b128 v[134:137], v206 offset:0
	ds_read_b128 v[210:213], v205 offset:0x800
	ds_read_b128 v[214:217], v206 offset:0x800
	v_cvt_pk_fp8_f32 v162, v116, v117 op_sel:[0,0,1]
	v_cvt_pk_fp8_f32 v163, v120, v121 op_sel:[0,0,1]
	s_waitcnt lgkmcnt(2)
	v_cvt_pk_fp8_f32 v164, v122, v123
	v_cvt_pk_fp8_f32 v165, v126, v127
	ds_read_b128 v[218:221], v188 offset:0
	ds_read_b128 v[222:225], v189 offset:0
	v_cvt_pk_fp8_f32 v164, v124, v125 op_sel:[0,0,1]
	v_cvt_pk_fp8_f32 v165, v128, v129 op_sel:[0,0,1]
	v_mfma_f32_32x32x64_f8f6f4 v[114:129], v[130:137], v[154:161], v[82:97]
	s_waitcnt lgkmcnt(2)
	v_mfma_f32_32x32x64_f8f6f4 v[130:145], v[210:217], v[154:161], v[82:97]
	v_cvt_pk_fp8_f32 v166, v98, v99
	v_cvt_pk_fp8_f32 v167, v102, v103
	v_cvt_pk_fp8_f32 v168, v106, v107
	v_cvt_pk_fp8_f32 v169, v110, v111
	v_cvt_pk_fp8_f32 v166, v100, v101 op_sel:[0,0,1]
	v_cvt_pk_fp8_f32 v167, v104, v105 op_sel:[0,0,1]
	v_cvt_pk_fp8_f32 v168, v108, v109 op_sel:[0,0,1]
	v_cvt_pk_fp8_f32 v169, v112, v113 op_sel:[0,0,1]
	s_nop 0
	ds_read_b128 v[106:109], v188 offset:0x800
	ds_read_b128 v[110:113], v189 offset:0x800
	s_nop 0
	v_mfma_f32_16x16x128_f8f6f4 v[18:21], v[162:169], v[146:153], v[18:21]
	s_waitcnt lgkmcnt(2)
	v_mfma_f32_32x32x64_f8f6f4 v[2:17], v[162:169], v[218:225], v[2:17]
	ds_read_b128 v[98:101], v188 offset:0x1000
	ds_read_b128 v[102:105], v189 offset:0x1000
	v_max3_f32 v191, v114, v115, v116
	v_max3_f32 v191, v191, v117, v118
	v_max3_f32 v191, v191, v119, v120
	v_max3_f32 v191, v191, v121, v122
	v_max3_f32 v191, v191, v123, v124
	v_max3_f32 v191, v191, v125, v126
	v_max3_f32 v191, v191, v127, v128
	v_max_f32 v191, v191, v129
	s_nop 0
	v_max3_f32 v191, v191, v130, v131
	v_max3_f32 v191, v191, v132, v133
	v_max3_f32 v191, v191, v134, v135
	v_max3_f32 v191, v191, v136, v137
	v_max3_f32 v191, v191, v138, v139
	v_max3_f32 v191, v191, v140, v141
	v_max3_f32 v191, v191, v142, v143
	v_max3_f32 v191, v191, v144, v145
	v_mov_b32 v192, v191
	s_nop 1
	v_permlane32_swap_b32 v191, v192
	v_max_f32 v191, v191, v192
	s_nop 0
	v_cmp_ge_f32_e32 vcc, s54, v191
	s_cmp_lg_u64 vcc, exec
	s_cselect_b64 s[38:39], -1, 0
	s_cmp_eq_u64 vcc, exec
	s_cbranch_scc1 .LBB0_1270
	v_add_f32_e32 v82, 0xc0c00000, v191
	v_max_f32_e32 v82, 0, v82
	v_exp_f32_e64 v191, -v82
	v_add_f32_e32 v198, v198, v82
	v_sub_f32_e32 v114, v114, v82
	v_sub_f32_e32 v130, v130, v82
	v_sub_f32_e32 v115, v115, v82
	v_sub_f32_e32 v131, v131, v82
	v_sub_f32_e32 v116, v116, v82
	v_sub_f32_e32 v132, v132, v82
	v_sub_f32_e32 v117, v117, v82
	v_sub_f32_e32 v133, v133, v82
	v_sub_f32_e32 v118, v118, v82
	v_sub_f32_e32 v134, v134, v82
	v_sub_f32_e32 v119, v119, v82
	v_sub_f32_e32 v135, v135, v82
	v_sub_f32_e32 v120, v120, v82
	v_sub_f32_e32 v136, v136, v82
	v_sub_f32_e32 v121, v121, v82
	v_sub_f32_e32 v137, v137, v82
	v_sub_f32_e32 v122, v122, v82
	v_sub_f32_e32 v138, v138, v82
	v_sub_f32_e32 v123, v123, v82
	v_sub_f32_e32 v139, v139, v82
	v_sub_f32_e32 v124, v124, v82
	v_sub_f32_e32 v140, v140, v82
	v_sub_f32_e32 v125, v125, v82
	v_sub_f32_e32 v141, v141, v82
	v_sub_f32_e32 v126, v126, v82
	v_sub_f32_e32 v142, v142, v82
	v_sub_f32_e32 v127, v127, v82
	v_sub_f32_e32 v143, v143, v82
	v_sub_f32_e32 v128, v128, v82
	v_sub_f32_e32 v144, v144, v82
	v_sub_f32_e32 v129, v129, v82
	v_sub_f32_e32 v145, v145, v82
	v_xor_b32_e32 v82, 0x80000000, v198
	v_mov_b32_e32 v83, v82
	v_mov_b32_e32 v84, v82
	v_mov_b32_e32 v85, v82
	v_mov_b32_e32 v86, v82
	v_mov_b32_e32 v87, v82
	v_mov_b32_e32 v88, v82
	v_mov_b32_e32 v89, v82
	v_mov_b32_e32 v90, v82
	v_mov_b32_e32 v91, v82
	v_mov_b32_e32 v92, v82
	v_mov_b32_e32 v93, v82
	v_mov_b32_e32 v94, v82
	v_mov_b32_e32 v95, v82
	v_mov_b32_e32 v96, v82
	v_mov_b32_e32 v97, v82
	s_branch .LBB0_1271

.LBB0_1271:
	s_waitcnt lgkmcnt(2)
	v_mfma_f32_32x32x64_f8f6f4 v[34:49], v[162:169], v[106:113], v[34:49]
	ds_read_b128 v[106:109], v188 offset:0x1800
	ds_read_b128 v[110:113], v189 offset:0x1800
	v_exp_f32_e32 v114, v114
	v_exp_f32_e32 v115, v115
	v_exp_f32_e32 v116, v116
	v_exp_f32_e32 v117, v117
	v_exp_f32_e32 v118, v118
	v_exp_f32_e32 v119, v119
	v_exp_f32_e32 v120, v120
	v_exp_f32_e32 v121, v121
	v_exp_f32_e32 v122, v122
	v_exp_f32_e32 v123, v123
	v_exp_f32_e32 v124, v124
	s_waitcnt lgkmcnt(2)
	v_mfma_f32_32x32x64_f8f6f4 v[50:65], v[162:169], v[98:105], v[50:65]
	v_exp_f32_e32 v125, v125
	v_exp_f32_e32 v126, v126
	v_exp_f32_e32 v127, v127
	v_exp_f32_e32 v128, v128
	v_exp_f32_e32 v129, v129
	v_exp_f32_e32 v130, v130
	v_exp_f32_e32 v131, v131
	v_exp_f32_e32 v132, v132
	v_exp_f32_e32 v133, v133
	v_exp_f32_e32 v134, v134
	v_exp_f32_e32 v135, v135
	s_waitcnt lgkmcnt(0)
	v_mfma_f32_32x32x64_f8f6f4 v[66:81], v[162:169], v[106:113], v[66:81]
	v_exp_f32_e32 v136, v136
	v_exp_f32_e32 v137, v137
	v_exp_f32_e32 v138, v138
	v_exp_f32_e32 v139, v139
	v_exp_f32_e32 v140, v140
	v_exp_f32_e32 v141, v141
	v_exp_f32_e32 v142, v142
	v_exp_f32_e32 v143, v143
	v_exp_f32_e32 v144, v144
	v_exp_f32_e32 v145, v145
	s_andn2_b64 vcc, exec, s[38:39]
	s_cbranch_vccnz .LBB0_1275
	s_and_saveexec_b64 s[38:39], s[6:7]
	ds_write_b32 v187, v191 offset:49152
	s_or_b64 exec, exec, s[38:39]
	s_waitcnt lgkmcnt(0)
	v_add_u32_e32 v110, s78, v186
	ds_read_b128 v[98:101], v110 offset:49248
	ds_read_b128 v[102:105], v110 offset:49216
	ds_read_b128 v[106:109], v110 offset:49184
	ds_read_b128 v[110:113], v110 offset:49152
	ds_read_b128 v[244:247], v250 offset:49152
	s_waitcnt lgkmcnt(0)
	v_pk_mul_f32 v[14:15], v[14:15], v[98:99]
	v_pk_mul_f32 v[10:11], v[10:11], v[102:103]
	v_pk_mul_f32 v[6:7], v[6:7], v[106:107]
	v_pk_mul_f32 v[16:17], v[16:17], v[100:101]
	v_pk_mul_f32 v[12:13], v[12:13], v[104:105]
	v_pk_mul_f32 v[8:9], v[8:9], v[108:109]
	v_pk_mul_f32 v[4:5], v[4:5], v[112:113]
	v_pk_mul_f32 v[2:3], v[2:3], v[110:111]
	v_pk_mul_f32 v[46:47], v[46:47], v[98:99]
	v_pk_mul_f32 v[42:43], v[42:43], v[102:103]
	v_pk_mul_f32 v[38:39], v[38:39], v[106:107]
	v_pk_mul_f32 v[48:49], v[48:49], v[100:101]
	v_pk_mul_f32 v[44:45], v[44:45], v[104:105]
	v_pk_mul_f32 v[40:41], v[40:41], v[108:109]
	v_pk_mul_f32 v[36:37], v[36:37], v[112:113]
	v_pk_mul_f32 v[34:35], v[34:35], v[110:111]
	v_pk_mul_f32 v[62:63], v[62:63], v[98:99]
	v_pk_mul_f32 v[58:59], v[58:59], v[102:103]
	v_pk_mul_f32 v[54:55], v[54:55], v[106:107]
	v_pk_mul_f32 v[64:65], v[64:65], v[100:101]
	v_pk_mul_f32 v[60:61], v[60:61], v[104:105]
	v_pk_mul_f32 v[56:57], v[56:57], v[108:109]
	v_pk_mul_f32 v[52:53], v[52:53], v[112:113]
	v_pk_mul_f32 v[50:51], v[50:51], v[110:111]
	v_pk_mul_f32 v[78:79], v[78:79], v[98:99]
	v_pk_mul_f32 v[74:75], v[74:75], v[102:103]
	v_pk_mul_f32 v[70:71], v[70:71], v[106:107]
	v_pk_mul_f32 v[80:81], v[80:81], v[100:101]
	v_pk_mul_f32 v[76:77], v[76:77], v[104:105]
	v_pk_mul_f32 v[72:73], v[72:73], v[108:109]
	v_pk_mul_f32 v[68:69], v[68:69], v[112:113]
	v_pk_mul_f32 v[66:67], v[66:67], v[110:111]
	v_pk_mul_f32 v[18:19], v[18:19], v[244:245]
	v_pk_mul_f32 v[20:21], v[20:21], v[246:247]
.LBB0_1275:
	s_add_i32 s38, s88, s37
	s_cmpk_eq_i32 s44, 0xf9
	s_cselect_b32 s38, s77, s38
	s_ashr_i32 s39, s38, 31
	s_lshl_b64 s[38:39], s[38:39], 10
	s_mov_b32 m0, s45
	s_waitcnt vmcnt(3) lgkmcnt(0)
	s_barrier
	v_lshl_add_u64 v[98:99], v[170:171], 0, s[38:39]
	s_add_i32 s51, s46, 0xa000
	global_load_lds_dwordx4 v[98:99], off
	v_lshl_add_u64 v[98:99], v[176:177], 0, s[60:61]
	s_mov_b32 m0, s51
	s_add_i32 s50, s46, 0xb000
	global_load_lds_dwordx4 v[98:99], off
	v_lshl_add_u64 v[98:99], v[176:177], 0, s[62:63]
	s_mov_b32 m0, s50
	v_cvt_pk_fp8_f32 v162, v114, v115
	global_load_lds_dwordx4 v[98:99], off
	v_cvt_pk_fp8_f32 v163, v118, v119
	ds_read_b128 v[210:213], v203 offset:0
	ds_read_b128 v[214:217], v204 offset:0
	ds_read_b128 v[218:221], v203 offset:0x800
	ds_read_b128 v[222:225], v204 offset:0x800
	v_cvt_pk_fp8_f32 v162, v116, v117 op_sel:[0,0,1]
	v_cvt_pk_fp8_f32 v163, v120, v121 op_sel:[0,0,1]
	s_waitcnt lgkmcnt(2)
	v_mfma_f32_32x32x64_f8f6f4 v[98:113], v[210:217], v[154:161], v[82:97]
	v_cvt_pk_fp8_f32 v164, v122, v123
	v_cvt_pk_fp8_f32 v165, v126, v127
	ds_read_b128 v[226:229], v201 offset:0
	ds_read_b128 v[230:233], v202 offset:0
	v_cvt_pk_fp8_f32 v164, v124, v125 op_sel:[0,0,1]
	v_cvt_pk_fp8_f32 v165, v128, v129 op_sel:[0,0,1]
	s_waitcnt lgkmcnt(2)
	v_mfma_f32_32x32x64_f8f6f4 v[114:129], v[218:225], v[154:161], v[82:97]
	v_cvt_pk_fp8_f32 v166, v130, v131
	v_cvt_pk_fp8_f32 v167, v134, v135
	v_cvt_pk_fp8_f32 v168, v138, v139
	v_cvt_pk_fp8_f32 v169, v142, v143
	v_cvt_pk_fp8_f32 v166, v132, v133 op_sel:[0,0,1]
	v_cvt_pk_fp8_f32 v167, v136, v137 op_sel:[0,0,1]
	v_cvt_pk_fp8_f32 v168, v140, v141 op_sel:[0,0,1]
	v_cvt_pk_fp8_f32 v169, v144, v145 op_sel:[0,0,1]
	s_nop 0
	ds_read_b128 v[138:141], v201 offset:0x800
	ds_read_b128 v[142:145], v202 offset:0x800
	s_nop 0
	v_mfma_f32_16x16x128_f8f6f4 v[18:21], v[162:169], v[146:153], v[18:21]
	s_waitcnt lgkmcnt(2)
	v_mfma_f32_32x32x64_f8f6f4 v[2:17], v[162:169], v[226:233], v[2:17]
	ds_read_b128 v[130:133], v201 offset:0x1000
	ds_read_b128 v[134:137], v202 offset:0x1000
	v_max3_f32 v191, v98, v99, v100
	v_max3_f32 v191, v191, v101, v102
	v_max3_f32 v191, v191, v103, v104
	v_max3_f32 v191, v191, v105, v106
	v_max3_f32 v191, v191, v107, v108
	v_max3_f32 v191, v191, v109, v110
	v_max3_f32 v191, v191, v111, v112
	v_max_f32 v191, v191, v113
	s_nop 0
	v_max3_f32 v191, v191, v114, v115
	v_max3_f32 v191, v191, v116, v117
	v_max3_f32 v191, v191, v118, v119
	v_max3_f32 v191, v191, v120, v121
	v_max3_f32 v191, v191, v122, v123
	v_max3_f32 v191, v191, v124, v125
	v_max3_f32 v191, v191, v126, v127
	v_max3_f32 v191, v191, v128, v129
	v_mov_b32 v192, v191
	s_nop 1
	v_permlane32_swap_b32 v191, v192
	v_max_f32 v191, v191, v192
	s_nop 0
	v_cmp_ge_f32_e32 vcc, s54, v191
	s_cmp_lg_u64 vcc, exec
	s_cselect_b64 s[38:39], -1, 0
	s_cmp_eq_u64 vcc, exec
	s_cbranch_scc1 .LBB0_1277
	v_add_f32_e32 v82, 0xc0c00000, v191
	v_max_f32_e32 v82, 0, v82
	v_exp_f32_e64 v191, -v82
	v_add_f32_e32 v198, v198, v82
	v_sub_f32_e32 v98, v98, v82
	v_sub_f32_e32 v114, v114, v82
	v_sub_f32_e32 v99, v99, v82
	v_sub_f32_e32 v115, v115, v82
	v_sub_f32_e32 v100, v100, v82
	v_sub_f32_e32 v116, v116, v82
	v_sub_f32_e32 v101, v101, v82
	v_sub_f32_e32 v117, v117, v82
	v_sub_f32_e32 v102, v102, v82
	v_sub_f32_e32 v118, v118, v82
	v_sub_f32_e32 v103, v103, v82
	v_sub_f32_e32 v119, v119, v82
	v_sub_f32_e32 v104, v104, v82
	v_sub_f32_e32 v120, v120, v82
	v_sub_f32_e32 v105, v105, v82
	v_sub_f32_e32 v121, v121, v82
	v_sub_f32_e32 v106, v106, v82
	v_sub_f32_e32 v122, v122, v82
	v_sub_f32_e32 v107, v107, v82
	v_sub_f32_e32 v123, v123, v82
	v_sub_f32_e32 v108, v108, v82
	v_sub_f32_e32 v124, v124, v82
	v_sub_f32_e32 v109, v109, v82
	v_sub_f32_e32 v125, v125, v82
	v_sub_f32_e32 v110, v110, v82
	v_sub_f32_e32 v126, v126, v82
	v_sub_f32_e32 v111, v111, v82
	v_sub_f32_e32 v127, v127, v82
	v_sub_f32_e32 v112, v112, v82
	v_sub_f32_e32 v128, v128, v82
	v_sub_f32_e32 v113, v113, v82
	v_sub_f32_e32 v129, v129, v82
	v_xor_b32_e32 v82, 0x80000000, v198
	v_mov_b32_e32 v83, v82
	v_mov_b32_e32 v84, v82
	v_mov_b32_e32 v85, v82
	v_mov_b32_e32 v86, v82
	v_mov_b32_e32 v87, v82
	v_mov_b32_e32 v88, v82
	v_mov_b32_e32 v89, v82
	v_mov_b32_e32 v90, v82
	v_mov_b32_e32 v91, v82
	v_mov_b32_e32 v92, v82
	v_mov_b32_e32 v93, v82
	v_mov_b32_e32 v94, v82
	v_mov_b32_e32 v95, v82
	v_mov_b32_e32 v96, v82
	v_mov_b32_e32 v97, v82
	s_branch .LBB0_1278

.LBB0_1278:
	s_waitcnt lgkmcnt(2)
	v_mfma_f32_32x32x64_f8f6f4 v[34:49], v[162:169], v[138:145], v[34:49]
	ds_read_b128 v[138:141], v201 offset:0x1800
	ds_read_b128 v[142:145], v202 offset:0x1800
	v_exp_f32_e32 v98, v98
	v_exp_f32_e32 v99, v99
	v_exp_f32_e32 v100, v100
	v_exp_f32_e32 v101, v101
	v_exp_f32_e32 v102, v102
	v_exp_f32_e32 v103, v103
	v_exp_f32_e32 v104, v104
	v_exp_f32_e32 v105, v105
	v_exp_f32_e32 v106, v106
	v_exp_f32_e32 v107, v107
	v_exp_f32_e32 v108, v108
	s_waitcnt lgkmcnt(2)
	v_mfma_f32_32x32x64_f8f6f4 v[50:65], v[162:169], v[130:137], v[50:65]
	v_exp_f32_e32 v109, v109
	v_exp_f32_e32 v110, v110
	v_exp_f32_e32 v111, v111
	v_exp_f32_e32 v112, v112
	v_exp_f32_e32 v113, v113
	v_exp_f32_e32 v114, v114
	v_exp_f32_e32 v115, v115
	v_exp_f32_e32 v116, v116
	v_exp_f32_e32 v117, v117
	v_exp_f32_e32 v118, v118
	v_exp_f32_e32 v119, v119
	s_waitcnt lgkmcnt(0)
	v_mfma_f32_32x32x64_f8f6f4 v[66:81], v[162:169], v[138:145], v[66:81]
	v_exp_f32_e32 v120, v120
	v_exp_f32_e32 v121, v121
	v_exp_f32_e32 v122, v122
	v_exp_f32_e32 v123, v123
	v_exp_f32_e32 v124, v124
	v_exp_f32_e32 v125, v125
	v_exp_f32_e32 v126, v126
	v_exp_f32_e32 v127, v127
	v_exp_f32_e32 v128, v128
	v_exp_f32_e32 v129, v129
	s_andn2_b64 vcc, exec, s[38:39]
	s_cbranch_vccnz .LBB0_1282
	s_and_saveexec_b64 s[38:39], s[6:7]
	ds_write_b32 v187, v191 offset:49152
	s_or_b64 exec, exec, s[38:39]
	s_waitcnt lgkmcnt(0)
	v_add_u32_e32 v142, s78, v186
	ds_read_b128 v[130:133], v142 offset:49248
	ds_read_b128 v[134:137], v142 offset:49216
	ds_read_b128 v[138:141], v142 offset:49184
	ds_read_b128 v[142:145], v142 offset:49152
	ds_read_b128 v[244:247], v250 offset:49152
	s_waitcnt lgkmcnt(0)
	v_pk_mul_f32 v[14:15], v[14:15], v[130:131]
	v_pk_mul_f32 v[10:11], v[10:11], v[134:135]
	v_pk_mul_f32 v[6:7], v[6:7], v[138:139]
	v_pk_mul_f32 v[16:17], v[16:17], v[132:133]
	v_pk_mul_f32 v[12:13], v[12:13], v[136:137]
	v_pk_mul_f32 v[8:9], v[8:9], v[140:141]
	v_pk_mul_f32 v[4:5], v[4:5], v[144:145]
	v_pk_mul_f32 v[2:3], v[2:3], v[142:143]
	v_pk_mul_f32 v[46:47], v[46:47], v[130:131]
	v_pk_mul_f32 v[42:43], v[42:43], v[134:135]
	v_pk_mul_f32 v[38:39], v[38:39], v[138:139]
	v_pk_mul_f32 v[48:49], v[48:49], v[132:133]
	v_pk_mul_f32 v[44:45], v[44:45], v[136:137]
	v_pk_mul_f32 v[40:41], v[40:41], v[140:141]
	v_pk_mul_f32 v[36:37], v[36:37], v[144:145]
	v_pk_mul_f32 v[34:35], v[34:35], v[142:143]
	v_pk_mul_f32 v[62:63], v[62:63], v[130:131]
	v_pk_mul_f32 v[58:59], v[58:59], v[134:135]
	v_pk_mul_f32 v[54:55], v[54:55], v[138:139]
	v_pk_mul_f32 v[64:65], v[64:65], v[132:133]
	v_pk_mul_f32 v[60:61], v[60:61], v[136:137]
	v_pk_mul_f32 v[56:57], v[56:57], v[140:141]
	v_pk_mul_f32 v[52:53], v[52:53], v[144:145]
	v_pk_mul_f32 v[50:51], v[50:51], v[142:143]
	v_pk_mul_f32 v[78:79], v[78:79], v[130:131]
	v_pk_mul_f32 v[74:75], v[74:75], v[134:135]
	v_pk_mul_f32 v[70:71], v[70:71], v[138:139]
	v_pk_mul_f32 v[80:81], v[80:81], v[132:133]
	v_pk_mul_f32 v[76:77], v[76:77], v[136:137]
	v_pk_mul_f32 v[72:73], v[72:73], v[140:141]
	v_pk_mul_f32 v[68:69], v[68:69], v[144:145]
	v_pk_mul_f32 v[66:67], v[66:67], v[142:143]
	v_pk_mul_f32 v[18:19], v[18:19], v[244:245]
	v_pk_mul_f32 v[20:21], v[20:21], v[246:247]
.LBB0_1282:
	s_add_i32 s44, s44, 4
	s_cmpk_lt_u32 s44, 0xfc
	s_cselect_b32 s38, s40, s41
	s_add_i32 s38, s38, s37
	s_addk_i32 s38, 0xff40
	s_ashr_i32 s39, s38, 31
	s_lshl_b64 s[38:39], s[38:39], 10
	s_waitcnt vmcnt(3) lgkmcnt(0)
	s_barrier
	v_lshl_add_u64 v[130:131], v[170:171], 0, s[38:39]
	s_add_i32 m0, s45, 0x1000
	v_cvt_pk_fp8_f32 v162, v98, v99
	global_load_lds_dwordx4 v[130:131], off
	v_lshl_add_u64 v[130:131], v[176:177], 0, s[64:65]
	s_add_i32 m0, s46, 0x4000
	v_cvt_pk_fp8_f32 v163, v102, v103
	global_load_lds_dwordx4 v[130:131], off
	v_lshl_add_u64 v[130:131], v[176:177], 0, s[66:67]
	s_add_i32 m0, s46, 0x5000
	v_cvt_pk_fp8_f32 v162, v100, v101 op_sel:[0,0,1]
	global_load_lds_dwordx4 v[130:131], off
	ds_read_b128 v[130:133], v199 offset:0
	ds_read_b128 v[134:137], v200 offset:0
	ds_read_b128 v[210:213], v199 offset:0x800
	ds_read_b128 v[214:217], v200 offset:0x800
	v_cvt_pk_fp8_f32 v163, v104, v105 op_sel:[0,0,1]
	s_waitcnt lgkmcnt(2)
	v_cvt_pk_fp8_f32 v164, v106, v107
	v_cvt_pk_fp8_f32 v165, v110, v111
	ds_read_b128 v[218:221], v196 offset:0
	ds_read_b128 v[222:225], v197 offset:0
	v_cvt_pk_fp8_f32 v164, v108, v109 op_sel:[0,0,1]
	v_cvt_pk_fp8_f32 v165, v112, v113 op_sel:[0,0,1]
	v_mfma_f32_32x32x64_f8f6f4 v[98:113], v[130:137], v[154:161], v[82:97]
	s_waitcnt lgkmcnt(2)
	v_mfma_f32_32x32x64_f8f6f4 v[130:145], v[210:217], v[154:161], v[82:97]
	v_cvt_pk_fp8_f32 v166, v114, v115
	v_cvt_pk_fp8_f32 v167, v118, v119
	v_cvt_pk_fp8_f32 v168, v122, v123
	v_cvt_pk_fp8_f32 v169, v126, v127
	v_cvt_pk_fp8_f32 v166, v116, v117 op_sel:[0,0,1]
	v_cvt_pk_fp8_f32 v167, v120, v121 op_sel:[0,0,1]
	v_cvt_pk_fp8_f32 v168, v124, v125 op_sel:[0,0,1]
	v_cvt_pk_fp8_f32 v169, v128, v129 op_sel:[0,0,1]
	s_nop 0
	ds_read_b128 v[122:125], v196 offset:0x800
	ds_read_b128 v[126:129], v197 offset:0x800
	s_nop 0
	v_mfma_f32_16x16x128_f8f6f4 v[18:21], v[162:169], v[146:153], v[18:21]
	s_waitcnt lgkmcnt(2)
	v_mfma_f32_32x32x64_f8f6f4 v[2:17], v[162:169], v[218:225], v[2:17]
	ds_read_b128 v[114:117], v196 offset:0x1000
	ds_read_b128 v[118:121], v197 offset:0x1000
	v_max3_f32 v191, v98, v99, v100
	v_max3_f32 v191, v191, v101, v102
	v_max3_f32 v191, v191, v103, v104
	v_max3_f32 v191, v191, v105, v106
	v_max3_f32 v191, v191, v107, v108
	v_max3_f32 v191, v191, v109, v110
	v_max3_f32 v191, v191, v111, v112
	v_max_f32 v191, v191, v113
	s_nop 0
	v_max3_f32 v191, v191, v130, v131
	v_max3_f32 v191, v191, v132, v133
	v_max3_f32 v191, v191, v134, v135
	v_max3_f32 v191, v191, v136, v137
	v_max3_f32 v191, v191, v138, v139
	v_max3_f32 v191, v191, v140, v141
	v_max3_f32 v191, v191, v142, v143
	v_max3_f32 v191, v191, v144, v145
	v_mov_b32 v192, v191
	s_nop 1
	v_permlane32_swap_b32 v191, v192
	v_max_f32 v191, v191, v192
	s_nop 0
	v_cmp_ge_f32_e32 vcc, s54, v191
	s_cmp_lg_u64 vcc, exec
	s_cselect_b64 s[38:39], -1, 0
	s_cmp_eq_u64 vcc, exec
	s_cbranch_scc1 .LBB0_1284
	v_add_f32_e32 v82, 0xc0c00000, v191
	v_max_f32_e32 v82, 0, v82
	v_exp_f32_e64 v191, -v82
	v_add_f32_e32 v198, v198, v82
	v_sub_f32_e32 v98, v98, v82
	v_sub_f32_e32 v130, v130, v82
	v_sub_f32_e32 v99, v99, v82
	v_sub_f32_e32 v131, v131, v82
	v_sub_f32_e32 v100, v100, v82
	v_sub_f32_e32 v132, v132, v82
	v_sub_f32_e32 v101, v101, v82
	v_sub_f32_e32 v133, v133, v82
	v_sub_f32_e32 v102, v102, v82
	v_sub_f32_e32 v134, v134, v82
	v_sub_f32_e32 v103, v103, v82
	v_sub_f32_e32 v135, v135, v82
	v_sub_f32_e32 v104, v104, v82
	v_sub_f32_e32 v136, v136, v82
	v_sub_f32_e32 v105, v105, v82
	v_sub_f32_e32 v137, v137, v82
	v_sub_f32_e32 v106, v106, v82
	v_sub_f32_e32 v138, v138, v82
	v_sub_f32_e32 v107, v107, v82
	v_sub_f32_e32 v139, v139, v82
	v_sub_f32_e32 v108, v108, v82
	v_sub_f32_e32 v140, v140, v82
	v_sub_f32_e32 v109, v109, v82
	v_sub_f32_e32 v141, v141, v82
	v_sub_f32_e32 v110, v110, v82
	v_sub_f32_e32 v142, v142, v82
	v_sub_f32_e32 v111, v111, v82
	v_sub_f32_e32 v143, v143, v82
	v_sub_f32_e32 v112, v112, v82
	v_sub_f32_e32 v144, v144, v82
	v_sub_f32_e32 v113, v113, v82
	v_sub_f32_e32 v145, v145, v82
	v_xor_b32_e32 v82, 0x80000000, v198
	v_mov_b32_e32 v83, v82
	v_mov_b32_e32 v84, v82
	v_mov_b32_e32 v85, v82
	v_mov_b32_e32 v86, v82
	v_mov_b32_e32 v87, v82
	v_mov_b32_e32 v88, v82
	v_mov_b32_e32 v89, v82
	v_mov_b32_e32 v90, v82
	v_mov_b32_e32 v91, v82
	v_mov_b32_e32 v92, v82
	v_mov_b32_e32 v93, v82
	v_mov_b32_e32 v94, v82
	v_mov_b32_e32 v95, v82
	v_mov_b32_e32 v96, v82
	v_mov_b32_e32 v97, v82
	s_branch .LBB0_1285

.LBB0_1285:
	s_waitcnt lgkmcnt(2)
	v_mfma_f32_32x32x64_f8f6f4 v[34:49], v[162:169], v[122:129], v[34:49]
	ds_read_b128 v[122:125], v196 offset:0x1800
	ds_read_b128 v[126:129], v197 offset:0x1800
	v_exp_f32_e32 v98, v98
	v_exp_f32_e32 v99, v99
	v_exp_f32_e32 v100, v100
	v_exp_f32_e32 v101, v101
	v_exp_f32_e32 v102, v102
	v_exp_f32_e32 v103, v103
	v_exp_f32_e32 v104, v104
	v_exp_f32_e32 v105, v105
	v_exp_f32_e32 v106, v106
	v_exp_f32_e32 v107, v107
	v_exp_f32_e32 v108, v108
	s_waitcnt lgkmcnt(2)
	v_mfma_f32_32x32x64_f8f6f4 v[50:65], v[162:169], v[114:121], v[50:65]
	v_exp_f32_e32 v109, v109
	v_exp_f32_e32 v110, v110
	v_exp_f32_e32 v111, v111
	v_exp_f32_e32 v112, v112
	v_exp_f32_e32 v113, v113
	v_exp_f32_e32 v130, v130
	v_exp_f32_e32 v131, v131
	v_exp_f32_e32 v132, v132
	v_exp_f32_e32 v133, v133
	v_exp_f32_e32 v134, v134
	v_exp_f32_e32 v135, v135
	s_waitcnt lgkmcnt(0)
	v_mfma_f32_32x32x64_f8f6f4 v[66:81], v[162:169], v[122:129], v[66:81]
	v_exp_f32_e32 v136, v136
	v_exp_f32_e32 v137, v137
	v_exp_f32_e32 v138, v138
	v_exp_f32_e32 v139, v139
	v_exp_f32_e32 v140, v140
	v_exp_f32_e32 v141, v141
	v_exp_f32_e32 v142, v142
	v_exp_f32_e32 v143, v143
	v_exp_f32_e32 v144, v144
	v_exp_f32_e32 v145, v145
	s_andn2_b64 vcc, exec, s[38:39]
	s_cbranch_vccnz .LBB0_1289
	s_and_saveexec_b64 s[38:39], s[6:7]
	ds_write_b32 v187, v191 offset:49152
	s_or_b64 exec, exec, s[38:39]
	s_waitcnt lgkmcnt(0)
	v_add_u32_e32 v126, s78, v186
	ds_read_b128 v[114:117], v126 offset:49248
	ds_read_b128 v[118:121], v126 offset:49216
	ds_read_b128 v[122:125], v126 offset:49184
	ds_read_b128 v[126:129], v126 offset:49152
	ds_read_b128 v[244:247], v250 offset:49152
	s_waitcnt lgkmcnt(0)
	v_pk_mul_f32 v[14:15], v[14:15], v[114:115]
	v_pk_mul_f32 v[10:11], v[10:11], v[118:119]
	v_pk_mul_f32 v[6:7], v[6:7], v[122:123]
	v_pk_mul_f32 v[16:17], v[16:17], v[116:117]
	v_pk_mul_f32 v[12:13], v[12:13], v[120:121]
	v_pk_mul_f32 v[8:9], v[8:9], v[124:125]
	v_pk_mul_f32 v[4:5], v[4:5], v[128:129]
	v_pk_mul_f32 v[2:3], v[2:3], v[126:127]
	v_pk_mul_f32 v[46:47], v[46:47], v[114:115]
	v_pk_mul_f32 v[42:43], v[42:43], v[118:119]
	v_pk_mul_f32 v[38:39], v[38:39], v[122:123]
	v_pk_mul_f32 v[48:49], v[48:49], v[116:117]
	v_pk_mul_f32 v[44:45], v[44:45], v[120:121]
	v_pk_mul_f32 v[40:41], v[40:41], v[124:125]
	v_pk_mul_f32 v[36:37], v[36:37], v[128:129]
	v_pk_mul_f32 v[34:35], v[34:35], v[126:127]
	v_pk_mul_f32 v[62:63], v[62:63], v[114:115]
	v_pk_mul_f32 v[58:59], v[58:59], v[118:119]
	v_pk_mul_f32 v[54:55], v[54:55], v[122:123]
	v_pk_mul_f32 v[64:65], v[64:65], v[116:117]
	v_pk_mul_f32 v[60:61], v[60:61], v[120:121]
	v_pk_mul_f32 v[56:57], v[56:57], v[124:125]
	v_pk_mul_f32 v[52:53], v[52:53], v[128:129]
	v_pk_mul_f32 v[50:51], v[50:51], v[126:127]
	v_pk_mul_f32 v[78:79], v[78:79], v[114:115]
	v_pk_mul_f32 v[74:75], v[74:75], v[118:119]
	v_pk_mul_f32 v[70:71], v[70:71], v[122:123]
	v_pk_mul_f32 v[80:81], v[80:81], v[116:117]
	v_pk_mul_f32 v[76:77], v[76:77], v[120:121]
	v_pk_mul_f32 v[72:73], v[72:73], v[124:125]
	v_pk_mul_f32 v[68:69], v[68:69], v[128:129]
	v_pk_mul_f32 v[66:67], v[66:67], v[126:127]
	v_pk_mul_f32 v[18:19], v[18:19], v[244:245]
	v_pk_mul_f32 v[20:21], v[20:21], v[246:247]
.LBB0_1289:
	s_cmpk_lt_u32 s44, 0xfb
	s_cselect_b32 s38, s42, s43
	s_add_i32 s38, s38, s37
	s_addk_i32 s38, 0xff40
	s_ashr_i32 s39, s38, 31
	s_lshl_b64 s[38:39], s[38:39], 10
	s_waitcnt vmcnt(3) lgkmcnt(0)
	s_barrier
	v_lshl_add_u64 v[114:115], v[170:171], 0, s[38:39]
	s_add_i32 m0, s45, 0x2000
	v_cvt_pk_fp8_f32 v162, v98, v99
	global_load_lds_dwordx4 v[114:115], off
	v_lshl_add_u64 v[114:115], v[176:177], 0, s[68:69]
	s_add_i32 m0, s46, 0x6000
	v_cvt_pk_fp8_f32 v163, v102, v103
	global_load_lds_dwordx4 v[114:115], off
	v_lshl_add_u64 v[114:115], v[176:177], 0, s[70:71]
	s_add_i32 m0, s46, 0x7000
	v_cvt_pk_fp8_f32 v162, v100, v101 op_sel:[0,0,1]
	global_load_lds_dwordx4 v[114:115], off
	ds_read_b128 v[210:213], v183 offset:0
	ds_read_b128 v[214:217], v190 offset:0
	ds_read_b128 v[218:221], v183 offset:0x800
	ds_read_b128 v[222:225], v190 offset:0x800
	v_cvt_pk_fp8_f32 v163, v104, v105 op_sel:[0,0,1]
	s_waitcnt lgkmcnt(2)
	v_mfma_f32_32x32x64_f8f6f4 v[114:129], v[210:217], v[154:161], v[82:97]
	v_cvt_pk_fp8_f32 v164, v106, v107
	v_cvt_pk_fp8_f32 v165, v110, v111
	ds_read_b128 v[226:229], v194 offset:0
	ds_read_b128 v[230:233], v195 offset:0
	v_cvt_pk_fp8_f32 v164, v108, v109 op_sel:[0,0,1]
	v_cvt_pk_fp8_f32 v165, v112, v113 op_sel:[0,0,1]
	s_waitcnt lgkmcnt(2)
	v_mfma_f32_32x32x64_f8f6f4 v[98:113], v[218:225], v[154:161], v[82:97]
	v_cvt_pk_fp8_f32 v166, v130, v131
	v_cvt_pk_fp8_f32 v167, v134, v135
	v_cvt_pk_fp8_f32 v168, v138, v139
	v_cvt_pk_fp8_f32 v169, v142, v143
	v_cvt_pk_fp8_f32 v166, v132, v133 op_sel:[0,0,1]
	v_cvt_pk_fp8_f32 v167, v136, v137 op_sel:[0,0,1]
	v_cvt_pk_fp8_f32 v168, v140, v141 op_sel:[0,0,1]
	v_cvt_pk_fp8_f32 v169, v144, v145 op_sel:[0,0,1]
	s_nop 0
	ds_read_b128 v[138:141], v194 offset:0x800
	ds_read_b128 v[142:145], v195 offset:0x800
	s_nop 0
	v_mfma_f32_16x16x128_f8f6f4 v[18:21], v[162:169], v[146:153], v[18:21]
	s_waitcnt lgkmcnt(2)
	v_mfma_f32_32x32x64_f8f6f4 v[2:17], v[162:169], v[226:233], v[2:17]
	ds_read_b128 v[130:133], v194 offset:0x1000
	ds_read_b128 v[134:137], v195 offset:0x1000
	v_max3_f32 v176, v114, v115, v116
	v_max3_f32 v176, v176, v117, v118
	v_max3_f32 v176, v176, v119, v120
	v_max3_f32 v176, v176, v121, v122
	v_max3_f32 v176, v176, v123, v124
	v_max3_f32 v176, v176, v125, v126
	v_max3_f32 v176, v176, v127, v128
	v_max_f32 v176, v176, v129
	s_nop 0
	v_max3_f32 v176, v176, v98, v99
	v_max3_f32 v176, v176, v100, v101
	v_max3_f32 v176, v176, v102, v103
	v_max3_f32 v176, v176, v104, v105
	v_max3_f32 v176, v176, v106, v107
	v_max3_f32 v176, v176, v108, v109
	v_max3_f32 v176, v176, v110, v111
	v_max3_f32 v176, v176, v112, v113
	v_mov_b32 v177, v176
	s_nop 1
	v_permlane32_swap_b32 v176, v177
	v_max_f32 v176, v176, v177
	s_nop 0
	v_cmp_ge_f32_e32 vcc, s54, v176
	s_cmp_lg_u64 vcc, exec
	s_cselect_b64 s[38:39], -1, 0
	s_cmp_eq_u64 vcc, exec
	s_cbranch_scc1 .LBB0_1291
	v_add_f32_e32 v82, 0xc0c00000, v176
	v_max_f32_e32 v82, 0, v82
	v_exp_f32_e64 v176, -v82
	v_add_f32_e32 v198, v198, v82
	v_sub_f32_e32 v114, v114, v82
	v_sub_f32_e32 v98, v98, v82
	v_sub_f32_e32 v115, v115, v82
	v_sub_f32_e32 v99, v99, v82
	v_sub_f32_e32 v116, v116, v82
	v_sub_f32_e32 v100, v100, v82
	v_sub_f32_e32 v117, v117, v82
	v_sub_f32_e32 v101, v101, v82
	v_sub_f32_e32 v118, v118, v82
	v_sub_f32_e32 v102, v102, v82
	v_sub_f32_e32 v119, v119, v82
	v_sub_f32_e32 v103, v103, v82
	v_sub_f32_e32 v120, v120, v82
	v_sub_f32_e32 v104, v104, v82
	v_sub_f32_e32 v121, v121, v82
	v_sub_f32_e32 v105, v105, v82
	v_sub_f32_e32 v122, v122, v82
	v_sub_f32_e32 v106, v106, v82
	v_sub_f32_e32 v123, v123, v82
	v_sub_f32_e32 v107, v107, v82
	v_sub_f32_e32 v124, v124, v82
	v_sub_f32_e32 v108, v108, v82
	v_sub_f32_e32 v125, v125, v82
	v_sub_f32_e32 v109, v109, v82
	v_sub_f32_e32 v126, v126, v82
	v_sub_f32_e32 v110, v110, v82
	v_sub_f32_e32 v127, v127, v82
	v_sub_f32_e32 v111, v111, v82
	v_sub_f32_e32 v128, v128, v82
	v_sub_f32_e32 v112, v112, v82
	v_sub_f32_e32 v129, v129, v82
	v_sub_f32_e32 v113, v113, v82
	v_xor_b32_e32 v82, 0x80000000, v198
	v_mov_b32_e32 v83, v82
	v_mov_b32_e32 v84, v82
	v_mov_b32_e32 v85, v82
	v_mov_b32_e32 v86, v82
	v_mov_b32_e32 v87, v82
	v_mov_b32_e32 v88, v82
	v_mov_b32_e32 v89, v82
	v_mov_b32_e32 v90, v82
	v_mov_b32_e32 v91, v82
	v_mov_b32_e32 v92, v82
	v_mov_b32_e32 v93, v82
	v_mov_b32_e32 v94, v82
	v_mov_b32_e32 v95, v82
	v_mov_b32_e32 v96, v82
	v_mov_b32_e32 v97, v82
	s_branch .LBB0_1292

.LBB0_1295:
	s_ashr_i32 s95, s94, 31
	s_lshl_b64 s[38:39], s[94:95], 10
	s_add_u32 s28, s28, s38
	s_addc_u32 s29, s29, s39
	v_mov_b32_e32 v183, v181
	v_lshl_add_u64 v[130:131], s[28:29], 0, v[180:181]
	s_mov_b64 s[28:29], 0x2030000
	s_mov_b32 m0, s49
	v_lshl_add_u64 v[130:131], v[130:131], 0, s[28:29]
	v_lshl_add_u64 v[170:171], s[90:91], 0, v[182:183]
	s_mov_b64 s[28:29], 0x204000
	global_load_lds_dwordx4 v[130:131], off
	v_lshl_add_u64 v[130:131], v[170:171], 0, s[28:29]
	s_mov_b32 m0, s47
	s_mov_b64 s[28:29], 0x205000
	global_load_lds_dwordx4 v[130:131], off
	v_lshl_add_u64 v[130:131], v[170:171], 0, s[28:29]
	s_mov_b32 m0, s48
	v_cvt_pk_fp8_f32 v162, v114, v115
	global_load_lds_dwordx4 v[130:131], off
	v_cvt_pk_fp8_f32 v163, v118, v119
	ds_read_b128 v[130:133], v205 offset:0
	ds_read_b128 v[134:137], v206 offset:0
	ds_read_b128 v[210:213], v205 offset:0x800
	ds_read_b128 v[214:217], v206 offset:0x800
	v_cvt_pk_fp8_f32 v162, v116, v117 op_sel:[0,0,1]
	v_cvt_pk_fp8_f32 v163, v120, v121 op_sel:[0,0,1]
	s_waitcnt lgkmcnt(2)
	v_cvt_pk_fp8_f32 v164, v122, v123
	v_cvt_pk_fp8_f32 v165, v126, v127
	ds_read_b128 v[218:221], v188 offset:0
	ds_read_b128 v[222:225], v189 offset:0
	v_cvt_pk_fp8_f32 v164, v124, v125 op_sel:[0,0,1]
	v_cvt_pk_fp8_f32 v165, v128, v129 op_sel:[0,0,1]
	v_mfma_f32_32x32x64_f8f6f4 v[114:129], v[130:137], v[154:161], v[82:97]
	s_waitcnt lgkmcnt(2)
	v_mfma_f32_32x32x64_f8f6f4 v[130:145], v[210:217], v[154:161], v[82:97]
	v_cvt_pk_fp8_f32 v166, v98, v99
	v_cvt_pk_fp8_f32 v167, v102, v103
	v_cvt_pk_fp8_f32 v168, v106, v107
	v_cvt_pk_fp8_f32 v169, v110, v111
	v_cvt_pk_fp8_f32 v166, v100, v101 op_sel:[0,0,1]
	v_cvt_pk_fp8_f32 v167, v104, v105 op_sel:[0,0,1]
	v_cvt_pk_fp8_f32 v168, v108, v109 op_sel:[0,0,1]
	v_cvt_pk_fp8_f32 v169, v112, v113 op_sel:[0,0,1]
	s_nop 0
	ds_read_b128 v[106:109], v188 offset:0x800
	ds_read_b128 v[110:113], v189 offset:0x800
	s_nop 0
	v_mfma_f32_16x16x128_f8f6f4 v[18:21], v[162:169], v[146:153], v[18:21]
	s_waitcnt lgkmcnt(2)
	v_mfma_f32_32x32x64_f8f6f4 v[2:17], v[162:169], v[218:225], v[2:17]
	ds_read_b128 v[98:101], v188 offset:0x1000
	ds_read_b128 v[102:105], v189 offset:0x1000
	v_max3_f32 v172, v114, v115, v116
	v_max3_f32 v172, v172, v117, v118
	v_max3_f32 v172, v172, v119, v120
	v_max3_f32 v172, v172, v121, v122
	v_max3_f32 v172, v172, v123, v124
	v_max3_f32 v172, v172, v125, v126
	v_max3_f32 v172, v172, v127, v128
	v_max_f32 v172, v172, v129
	s_nop 0
	v_max3_f32 v172, v172, v130, v131
	v_max3_f32 v172, v172, v132, v133
	v_max3_f32 v172, v172, v134, v135
	v_max3_f32 v172, v172, v136, v137
	v_max3_f32 v172, v172, v138, v139
	v_max3_f32 v172, v172, v140, v141
	v_max3_f32 v172, v172, v142, v143
	v_max3_f32 v172, v172, v144, v145
	v_mov_b32 v173, v172
	s_nop 1
	v_permlane32_swap_b32 v172, v173
	v_max_f32 v172, v172, v173
	s_nop 0
	v_cmp_ge_f32_e32 vcc, s54, v172
	s_cmp_lg_u64 vcc, exec
	s_cselect_b64 s[28:29], -1, 0
	s_cmp_eq_u64 vcc, exec
	s_cbranch_scc1 .LBB0_1297
	v_add_f32_e32 v82, 0xc0c00000, v172
	v_max_f32_e32 v82, 0, v82
	v_exp_f32_e64 v172, -v82
	v_add_f32_e32 v198, v198, v82
	v_sub_f32_e32 v114, v114, v82
	v_sub_f32_e32 v130, v130, v82
	v_sub_f32_e32 v115, v115, v82
	v_sub_f32_e32 v131, v131, v82
	v_sub_f32_e32 v116, v116, v82
	v_sub_f32_e32 v132, v132, v82
	v_sub_f32_e32 v117, v117, v82
	v_sub_f32_e32 v133, v133, v82
	v_sub_f32_e32 v118, v118, v82
	v_sub_f32_e32 v134, v134, v82
	v_sub_f32_e32 v119, v119, v82
	v_sub_f32_e32 v135, v135, v82
	v_sub_f32_e32 v120, v120, v82
	v_sub_f32_e32 v136, v136, v82
	v_sub_f32_e32 v121, v121, v82
	v_sub_f32_e32 v137, v137, v82
	v_sub_f32_e32 v122, v122, v82
	v_sub_f32_e32 v138, v138, v82
	v_sub_f32_e32 v123, v123, v82
	v_sub_f32_e32 v139, v139, v82
	v_sub_f32_e32 v124, v124, v82
	v_sub_f32_e32 v140, v140, v82
	v_sub_f32_e32 v125, v125, v82
	v_sub_f32_e32 v141, v141, v82
	v_sub_f32_e32 v126, v126, v82
	v_sub_f32_e32 v142, v142, v82
	v_sub_f32_e32 v127, v127, v82
	v_sub_f32_e32 v143, v143, v82
	v_sub_f32_e32 v128, v128, v82
	v_sub_f32_e32 v144, v144, v82
	v_sub_f32_e32 v129, v129, v82
	v_sub_f32_e32 v145, v145, v82
	v_xor_b32_e32 v82, 0x80000000, v198
	v_mov_b32_e32 v83, v82
	v_mov_b32_e32 v84, v82
	v_mov_b32_e32 v85, v82
	v_mov_b32_e32 v86, v82
	v_mov_b32_e32 v87, v82
	v_mov_b32_e32 v88, v82
	v_mov_b32_e32 v89, v82
	v_mov_b32_e32 v90, v82
	v_mov_b32_e32 v91, v82
	v_mov_b32_e32 v92, v82
	v_mov_b32_e32 v93, v82
	v_mov_b32_e32 v94, v82
	v_mov_b32_e32 v95, v82
	v_mov_b32_e32 v96, v82
	v_mov_b32_e32 v97, v82
	s_branch .LBB0_1298

.LBB0_1298:
	s_waitcnt lgkmcnt(2)
	v_mfma_f32_32x32x64_f8f6f4 v[34:49], v[162:169], v[106:113], v[34:49]
	ds_read_b128 v[210:213], v188 offset:0x1800
	ds_read_b128 v[214:217], v189 offset:0x1800
	v_exp_f32_e32 v114, v114
	v_exp_f32_e32 v115, v115
	v_exp_f32_e32 v116, v116
	v_exp_f32_e32 v117, v117
	v_exp_f32_e32 v118, v118
	v_exp_f32_e32 v119, v119
	v_exp_f32_e32 v120, v120
	v_exp_f32_e32 v121, v121
	v_exp_f32_e32 v122, v122
	v_exp_f32_e32 v123, v123
	v_exp_f32_e32 v124, v124
	s_waitcnt lgkmcnt(2)
	v_mfma_f32_32x32x64_f8f6f4 v[50:65], v[162:169], v[98:105], v[50:65]
	v_exp_f32_e32 v125, v125
	v_exp_f32_e32 v126, v126
	v_exp_f32_e32 v127, v127
	v_exp_f32_e32 v128, v128
	v_exp_f32_e32 v129, v129
	v_exp_f32_e32 v130, v130
	v_exp_f32_e32 v131, v131
	v_exp_f32_e32 v132, v132
	v_exp_f32_e32 v133, v133
	v_exp_f32_e32 v134, v134
	v_exp_f32_e32 v135, v135
	s_waitcnt lgkmcnt(0)
	v_mfma_f32_32x32x64_f8f6f4 v[66:81], v[162:169], v[210:217], v[66:81]
	v_exp_f32_e32 v136, v136
	v_exp_f32_e32 v137, v137
	v_exp_f32_e32 v138, v138
	v_exp_f32_e32 v139, v139
	v_exp_f32_e32 v140, v140
	v_exp_f32_e32 v141, v141
	v_exp_f32_e32 v142, v142
	v_exp_f32_e32 v143, v143
	v_exp_f32_e32 v144, v144
	v_exp_f32_e32 v145, v145
	s_andn2_b64 vcc, exec, s[28:29]
	s_cbranch_vccnz .LBB0_1302
	s_and_saveexec_b64 s[28:29], s[6:7]
	ds_write_b32 v187, v172 offset:49152
	s_or_b64 exec, exec, s[28:29]
	s_waitcnt lgkmcnt(0)
	v_add_u32_e32 v110, s78, v186
	ds_read_b128 v[98:101], v110 offset:49248
	ds_read_b128 v[102:105], v110 offset:49216
	ds_read_b128 v[106:109], v110 offset:49184
	ds_read_b128 v[110:113], v110 offset:49152
	ds_read_b128 v[244:247], v250 offset:49152
	s_waitcnt lgkmcnt(0)
	v_pk_mul_f32 v[14:15], v[14:15], v[98:99]
	v_pk_mul_f32 v[10:11], v[10:11], v[102:103]
	v_pk_mul_f32 v[6:7], v[6:7], v[106:107]
	v_pk_mul_f32 v[16:17], v[16:17], v[100:101]
	v_pk_mul_f32 v[12:13], v[12:13], v[104:105]
	v_pk_mul_f32 v[8:9], v[8:9], v[108:109]
	v_pk_mul_f32 v[4:5], v[4:5], v[112:113]
	v_pk_mul_f32 v[2:3], v[2:3], v[110:111]
	v_pk_mul_f32 v[46:47], v[46:47], v[98:99]
	v_pk_mul_f32 v[42:43], v[42:43], v[102:103]
	v_pk_mul_f32 v[38:39], v[38:39], v[106:107]
	v_pk_mul_f32 v[48:49], v[48:49], v[100:101]
	v_pk_mul_f32 v[44:45], v[44:45], v[104:105]
	v_pk_mul_f32 v[40:41], v[40:41], v[108:109]
	v_pk_mul_f32 v[36:37], v[36:37], v[112:113]
	v_pk_mul_f32 v[34:35], v[34:35], v[110:111]
	v_pk_mul_f32 v[62:63], v[62:63], v[98:99]
	v_pk_mul_f32 v[58:59], v[58:59], v[102:103]
	v_pk_mul_f32 v[54:55], v[54:55], v[106:107]
	v_pk_mul_f32 v[64:65], v[64:65], v[100:101]
	v_pk_mul_f32 v[60:61], v[60:61], v[104:105]
	v_pk_mul_f32 v[56:57], v[56:57], v[108:109]
	v_pk_mul_f32 v[52:53], v[52:53], v[112:113]
	v_pk_mul_f32 v[50:51], v[50:51], v[110:111]
	v_pk_mul_f32 v[78:79], v[78:79], v[98:99]
	v_pk_mul_f32 v[74:75], v[74:75], v[102:103]
	v_pk_mul_f32 v[70:71], v[70:71], v[106:107]
	v_pk_mul_f32 v[80:81], v[80:81], v[100:101]
	v_pk_mul_f32 v[76:77], v[76:77], v[104:105]
	v_pk_mul_f32 v[72:73], v[72:73], v[108:109]
	v_pk_mul_f32 v[68:69], v[68:69], v[112:113]
	v_pk_mul_f32 v[66:67], v[66:67], v[110:111]
	v_pk_mul_f32 v[18:19], v[18:19], v[244:245]
	v_pk_mul_f32 v[20:21], v[20:21], v[246:247]
.LBB0_1302:
	s_mov_b32 m0, s51
	s_waitcnt vmcnt(3) lgkmcnt(0)
	s_barrier
	v_lshl_add_u64 v[98:99], v[170:171], 0, s[82:83]
	global_load_lds_dwordx4 v[98:99], off
	v_lshl_add_u64 v[98:99], v[170:171], 0, s[84:85]
	s_mov_b32 m0, s50
	v_cvt_pk_fp8_f32 v162, v114, v115
	global_load_lds_dwordx4 v[98:99], off
	v_cvt_pk_fp8_f32 v163, v118, v119
	ds_read_b128 v[170:173], v203 offset:0
	ds_read_b128 v[174:177], v204 offset:0
	ds_read_b128 v[210:213], v203 offset:0x800
	ds_read_b128 v[214:217], v204 offset:0x800
	v_cvt_pk_fp8_f32 v162, v116, v117 op_sel:[0,0,1]
	v_cvt_pk_fp8_f32 v163, v120, v121 op_sel:[0,0,1]
	s_waitcnt lgkmcnt(2)
	v_mfma_f32_32x32x64_f8f6f4 v[98:113], v[170:177], v[154:161], v[82:97]
	v_cvt_pk_fp8_f32 v164, v122, v123
	v_cvt_pk_fp8_f32 v165, v126, v127
	ds_read_b128 v[218:221], v201 offset:0
	ds_read_b128 v[222:225], v202 offset:0
	v_cvt_pk_fp8_f32 v164, v124, v125 op_sel:[0,0,1]
	v_cvt_pk_fp8_f32 v165, v128, v129 op_sel:[0,0,1]
	s_waitcnt lgkmcnt(2)
	v_mfma_f32_32x32x64_f8f6f4 v[114:129], v[210:217], v[154:161], v[82:97]
	v_cvt_pk_fp8_f32 v166, v130, v131
	v_cvt_pk_fp8_f32 v167, v134, v135
	v_cvt_pk_fp8_f32 v168, v138, v139
	v_cvt_pk_fp8_f32 v169, v142, v143
	v_cvt_pk_fp8_f32 v166, v132, v133 op_sel:[0,0,1]
	v_cvt_pk_fp8_f32 v167, v136, v137 op_sel:[0,0,1]
	v_cvt_pk_fp8_f32 v168, v140, v141 op_sel:[0,0,1]
	v_cvt_pk_fp8_f32 v169, v144, v145 op_sel:[0,0,1]
	s_nop 0
	ds_read_b128 v[138:141], v201 offset:0x800
	ds_read_b128 v[142:145], v202 offset:0x800
	s_nop 0
	v_mfma_f32_16x16x128_f8f6f4 v[18:21], v[162:169], v[146:153], v[18:21]
	s_waitcnt lgkmcnt(2)
	v_mfma_f32_32x32x64_f8f6f4 v[2:17], v[162:169], v[218:225], v[2:17]
	ds_read_b128 v[130:133], v201 offset:0x1000
	ds_read_b128 v[134:137], v202 offset:0x1000
	v_max3_f32 v170, v98, v99, v100
	v_max3_f32 v170, v170, v101, v102
	v_max3_f32 v170, v170, v103, v104
	v_max3_f32 v170, v170, v105, v106
	v_max3_f32 v170, v170, v107, v108
	v_max3_f32 v170, v170, v109, v110
	v_max3_f32 v170, v170, v111, v112
	v_max_f32 v170, v170, v113
	s_nop 0
	v_max3_f32 v170, v170, v114, v115
	v_max3_f32 v170, v170, v116, v117
	v_max3_f32 v170, v170, v118, v119
	v_max3_f32 v170, v170, v120, v121
	v_max3_f32 v170, v170, v122, v123
	v_max3_f32 v170, v170, v124, v125
	v_max3_f32 v170, v170, v126, v127
	v_max3_f32 v170, v170, v128, v129
	v_mov_b32 v171, v170
	s_nop 1
	v_permlane32_swap_b32 v170, v171
	v_max_f32 v170, v170, v171
	s_nop 0
	v_cmp_ge_f32_e32 vcc, s54, v170
	s_cmp_lg_u64 vcc, exec
	s_cselect_b64 s[28:29], -1, 0
	s_cmp_eq_u64 vcc, exec
	s_cbranch_scc1 .LBB0_1304
	v_add_f32_e32 v82, 0xc0c00000, v170
	v_max_f32_e32 v82, 0, v82
	v_exp_f32_e64 v170, -v82
	v_add_f32_e32 v198, v198, v82
	v_sub_f32_e32 v98, v98, v82
	v_sub_f32_e32 v114, v114, v82
	v_sub_f32_e32 v99, v99, v82
	v_sub_f32_e32 v115, v115, v82
	v_sub_f32_e32 v100, v100, v82
	v_sub_f32_e32 v116, v116, v82
	v_sub_f32_e32 v101, v101, v82
	v_sub_f32_e32 v117, v117, v82
	v_sub_f32_e32 v102, v102, v82
	v_sub_f32_e32 v118, v118, v82
	v_sub_f32_e32 v103, v103, v82
	v_sub_f32_e32 v119, v119, v82
	v_sub_f32_e32 v104, v104, v82
	v_sub_f32_e32 v120, v120, v82
	v_sub_f32_e32 v105, v105, v82
	v_sub_f32_e32 v121, v121, v82
	v_sub_f32_e32 v106, v106, v82
	v_sub_f32_e32 v122, v122, v82
	v_sub_f32_e32 v107, v107, v82
	v_sub_f32_e32 v123, v123, v82
	v_sub_f32_e32 v108, v108, v82
	v_sub_f32_e32 v124, v124, v82
	v_sub_f32_e32 v109, v109, v82
	v_sub_f32_e32 v125, v125, v82
	v_sub_f32_e32 v110, v110, v82
	v_sub_f32_e32 v126, v126, v82
	v_sub_f32_e32 v111, v111, v82
	v_sub_f32_e32 v127, v127, v82
	v_sub_f32_e32 v112, v112, v82
	v_sub_f32_e32 v128, v128, v82
	v_sub_f32_e32 v113, v113, v82
	v_sub_f32_e32 v129, v129, v82
	v_xor_b32_e32 v82, 0x80000000, v198
	v_mov_b32_e32 v83, v82
	v_mov_b32_e32 v84, v82
	v_mov_b32_e32 v85, v82
	v_mov_b32_e32 v86, v82
	v_mov_b32_e32 v87, v82
	v_mov_b32_e32 v88, v82
	v_mov_b32_e32 v89, v82
	v_mov_b32_e32 v90, v82
	v_mov_b32_e32 v91, v82
	v_mov_b32_e32 v92, v82
	v_mov_b32_e32 v93, v82
	v_mov_b32_e32 v94, v82
	v_mov_b32_e32 v95, v82
	v_mov_b32_e32 v96, v82
	v_mov_b32_e32 v97, v82
	s_branch .LBB0_1305

.LBB0_1305:
	s_waitcnt lgkmcnt(2)
	v_mfma_f32_32x32x64_f8f6f4 v[34:49], v[162:169], v[138:145], v[34:49]
	ds_read_b128 v[210:213], v201 offset:0x1800
	ds_read_b128 v[214:217], v202 offset:0x1800
	v_exp_f32_e32 v98, v98
	v_exp_f32_e32 v99, v99
	v_exp_f32_e32 v100, v100
	v_exp_f32_e32 v101, v101
	v_exp_f32_e32 v102, v102
	v_exp_f32_e32 v103, v103
	v_exp_f32_e32 v104, v104
	v_exp_f32_e32 v105, v105
	v_exp_f32_e32 v106, v106
	v_exp_f32_e32 v107, v107
	v_exp_f32_e32 v108, v108
	s_waitcnt lgkmcnt(2)
	v_mfma_f32_32x32x64_f8f6f4 v[50:65], v[162:169], v[130:137], v[50:65]
	v_exp_f32_e32 v109, v109
	v_exp_f32_e32 v110, v110
	v_exp_f32_e32 v111, v111
	v_exp_f32_e32 v112, v112
	v_exp_f32_e32 v113, v113
	v_exp_f32_e32 v114, v114
	v_exp_f32_e32 v115, v115
	v_exp_f32_e32 v116, v116
	v_exp_f32_e32 v117, v117
	v_exp_f32_e32 v118, v118
	v_exp_f32_e32 v119, v119
	s_waitcnt lgkmcnt(0)
	v_mfma_f32_32x32x64_f8f6f4 v[66:81], v[162:169], v[210:217], v[66:81]
	v_exp_f32_e32 v120, v120
	v_exp_f32_e32 v121, v121
	v_exp_f32_e32 v122, v122
	v_exp_f32_e32 v123, v123
	v_exp_f32_e32 v124, v124
	v_exp_f32_e32 v125, v125
	v_exp_f32_e32 v126, v126
	v_exp_f32_e32 v127, v127
	v_exp_f32_e32 v128, v128
	v_exp_f32_e32 v129, v129
	s_andn2_b64 vcc, exec, s[28:29]
	s_cbranch_vccnz .LBB0_1309
	s_and_saveexec_b64 s[28:29], s[6:7]
	ds_write_b32 v187, v170 offset:49152
	s_or_b64 exec, exec, s[28:29]
	s_waitcnt lgkmcnt(0)
	v_add_u32_e32 v142, s78, v186
	ds_read_b128 v[130:133], v142 offset:49248
	ds_read_b128 v[134:137], v142 offset:49216
	ds_read_b128 v[138:141], v142 offset:49184
	ds_read_b128 v[142:145], v142 offset:49152
	ds_read_b128 v[244:247], v250 offset:49152
	s_waitcnt lgkmcnt(0)
	v_pk_mul_f32 v[14:15], v[14:15], v[130:131]
	v_pk_mul_f32 v[10:11], v[10:11], v[134:135]
	v_pk_mul_f32 v[6:7], v[6:7], v[138:139]
	v_pk_mul_f32 v[16:17], v[16:17], v[132:133]
	v_pk_mul_f32 v[12:13], v[12:13], v[136:137]
	v_pk_mul_f32 v[8:9], v[8:9], v[140:141]
	v_pk_mul_f32 v[4:5], v[4:5], v[144:145]
	v_pk_mul_f32 v[2:3], v[2:3], v[142:143]
	v_pk_mul_f32 v[46:47], v[46:47], v[130:131]
	v_pk_mul_f32 v[42:43], v[42:43], v[134:135]
	v_pk_mul_f32 v[38:39], v[38:39], v[138:139]
	v_pk_mul_f32 v[48:49], v[48:49], v[132:133]
	v_pk_mul_f32 v[44:45], v[44:45], v[136:137]
	v_pk_mul_f32 v[40:41], v[40:41], v[140:141]
	v_pk_mul_f32 v[36:37], v[36:37], v[144:145]
	v_pk_mul_f32 v[34:35], v[34:35], v[142:143]
	v_pk_mul_f32 v[62:63], v[62:63], v[130:131]
	v_pk_mul_f32 v[58:59], v[58:59], v[134:135]
	v_pk_mul_f32 v[54:55], v[54:55], v[138:139]
	v_pk_mul_f32 v[64:65], v[64:65], v[132:133]
	v_pk_mul_f32 v[60:61], v[60:61], v[136:137]
	v_pk_mul_f32 v[56:57], v[56:57], v[140:141]
	v_pk_mul_f32 v[52:53], v[52:53], v[144:145]
	v_pk_mul_f32 v[50:51], v[50:51], v[142:143]
	v_pk_mul_f32 v[78:79], v[78:79], v[130:131]
	v_pk_mul_f32 v[74:75], v[74:75], v[134:135]
	v_pk_mul_f32 v[70:71], v[70:71], v[138:139]
	v_pk_mul_f32 v[80:81], v[80:81], v[132:133]
	v_pk_mul_f32 v[76:77], v[76:77], v[136:137]
	v_pk_mul_f32 v[72:73], v[72:73], v[140:141]
	v_pk_mul_f32 v[68:69], v[68:69], v[144:145]
	v_pk_mul_f32 v[66:67], v[66:67], v[142:143]
	v_pk_mul_f32 v[18:19], v[18:19], v[244:245]
	v_pk_mul_f32 v[20:21], v[20:21], v[246:247]
.LBB0_1309:
	s_waitcnt vmcnt(0) lgkmcnt(0)
	s_barrier
	v_cvt_pk_fp8_f32 v162, v98, v99
	v_cvt_pk_fp8_f32 v163, v102, v103
	ds_read_b128 v[130:133], v199 offset:0
	ds_read_b128 v[134:137], v200 offset:0
	ds_read_b128 v[170:173], v199 offset:0x800
	ds_read_b128 v[174:177], v200 offset:0x800
	v_cvt_pk_fp8_f32 v162, v100, v101 op_sel:[0,0,1]
	v_cvt_pk_fp8_f32 v163, v104, v105 op_sel:[0,0,1]
	s_waitcnt lgkmcnt(2)
	v_cvt_pk_fp8_f32 v164, v106, v107
	v_cvt_pk_fp8_f32 v165, v110, v111
	ds_read_b128 v[200:203], v196 offset:0
	ds_read_b128 v[204:207], v197 offset:0
	v_cvt_pk_fp8_f32 v164, v108, v109 op_sel:[0,0,1]
	v_cvt_pk_fp8_f32 v165, v112, v113 op_sel:[0,0,1]
	v_mfma_f32_32x32x64_f8f6f4 v[98:113], v[130:137], v[154:161], v[82:97]
	s_waitcnt lgkmcnt(2)
	v_mfma_f32_32x32x64_f8f6f4 v[82:97], v[170:177], v[154:161], v[82:97]
	v_cvt_pk_fp8_f32 v166, v114, v115
	v_cvt_pk_fp8_f32 v167, v118, v119
	v_cvt_pk_fp8_f32 v168, v122, v123
	v_cvt_pk_fp8_f32 v169, v126, v127
	v_cvt_pk_fp8_f32 v166, v116, v117 op_sel:[0,0,1]
	v_cvt_pk_fp8_f32 v167, v120, v121 op_sel:[0,0,1]
	v_cvt_pk_fp8_f32 v168, v124, v125 op_sel:[0,0,1]
	v_cvt_pk_fp8_f32 v169, v128, v129 op_sel:[0,0,1]
	s_nop 0
	ds_read_b128 v[138:141], v196 offset:0x800
	ds_read_b128 v[142:145], v197 offset:0x800
	s_nop 0
	v_mfma_f32_16x16x128_f8f6f4 v[18:21], v[162:169], v[146:153], v[18:21]
	s_waitcnt lgkmcnt(2)
	v_mfma_f32_32x32x64_f8f6f4 v[2:17], v[162:169], v[200:207], v[2:17]
	ds_read_b128 v[130:133], v196 offset:0x1000
	ds_read_b128 v[134:137], v197 offset:0x1000
	v_max3_f32 v114, v98, v99, v100
	v_max3_f32 v114, v114, v101, v102
	v_max3_f32 v114, v114, v103, v104
	v_max3_f32 v114, v114, v105, v106
	v_max3_f32 v114, v114, v107, v108
	v_max3_f32 v114, v114, v109, v110
	v_max3_f32 v114, v114, v111, v112
	v_max_f32 v114, v114, v113
	s_nop 0
	v_max3_f32 v114, v114, v82, v83
	v_max3_f32 v114, v114, v84, v85
	v_max3_f32 v114, v114, v86, v87
	v_max3_f32 v114, v114, v88, v89
	v_max3_f32 v114, v114, v90, v91
	v_max3_f32 v114, v114, v92, v93
	v_max3_f32 v114, v114, v94, v95
	v_max3_f32 v114, v114, v96, v97
	v_mov_b32 v115, v114
	s_nop 1
	v_permlane32_swap_b32 v114, v115
	v_max_f32 v114, v114, v115
	s_nop 0
	v_cmp_ge_f32_e32 vcc, s54, v114
	s_cmp_lg_u64 vcc, exec
	s_cselect_b64 s[28:29], -1, 0
	s_cmp_eq_u64 vcc, exec
	s_cbranch_scc1 .LBB0_1311
	v_add_f32_e32 v114, 0xc0c00000, v114
	v_max_f32_e32 v114, 0, v114
	v_exp_f32_e64 v154, -v114
	v_sub_f32_e32 v98, v98, v114
	v_sub_f32_e32 v82, v82, v114
	v_sub_f32_e32 v99, v99, v114
	v_sub_f32_e32 v83, v83, v114
	v_sub_f32_e32 v100, v100, v114
	v_sub_f32_e32 v84, v84, v114
	v_sub_f32_e32 v101, v101, v114
	v_sub_f32_e32 v85, v85, v114
	v_sub_f32_e32 v102, v102, v114
	v_sub_f32_e32 v86, v86, v114
	v_sub_f32_e32 v103, v103, v114
	v_sub_f32_e32 v87, v87, v114
	v_sub_f32_e32 v104, v104, v114
	v_sub_f32_e32 v88, v88, v114
	v_sub_f32_e32 v105, v105, v114
	v_sub_f32_e32 v89, v89, v114
	v_sub_f32_e32 v106, v106, v114
	v_sub_f32_e32 v90, v90, v114
	v_sub_f32_e32 v107, v107, v114
	v_sub_f32_e32 v91, v91, v114
	v_sub_f32_e32 v108, v108, v114
	v_sub_f32_e32 v92, v92, v114
	v_sub_f32_e32 v109, v109, v114
	v_sub_f32_e32 v93, v93, v114
	v_sub_f32_e32 v110, v110, v114
	v_sub_f32_e32 v94, v94, v114
	v_sub_f32_e32 v111, v111, v114
	v_sub_f32_e32 v95, v95, v114
	v_sub_f32_e32 v112, v112, v114
	v_sub_f32_e32 v96, v96, v114
	v_sub_f32_e32 v113, v113, v114
	v_sub_f32_e32 v97, v97, v114
	v_add_f32_e32 v114, v198, v114
	v_xor_b32_e32 v114, 0x80000000, v114
	v_mov_b32_e32 v115, v114
	v_mov_b32_e32 v116, v114
	v_mov_b32_e32 v117, v114
	v_mov_b32_e32 v118, v114
	v_mov_b32_e32 v119, v114
	v_mov_b32_e32 v120, v114
	v_mov_b32_e32 v121, v114
	v_mov_b32_e32 v122, v114
	v_mov_b32_e32 v123, v114
	v_mov_b32_e32 v124, v114
	v_mov_b32_e32 v125, v114
	v_mov_b32_e32 v126, v114
	v_mov_b32_e32 v127, v114
	v_mov_b32_e32 v128, v114
	v_mov_b32_e32 v129, v114
	s_branch .LBB0_1312

.LBB0_1312:
	s_waitcnt lgkmcnt(2)
	v_mfma_f32_32x32x64_f8f6f4 v[34:49], v[162:169], v[138:145], v[34:49]
	ds_read_b128 v[114:117], v196 offset:0x1800
	ds_read_b128 v[118:121], v197 offset:0x1800
	v_exp_f32_e32 v98, v98
	v_exp_f32_e32 v99, v99
	v_exp_f32_e32 v100, v100
	v_exp_f32_e32 v101, v101
	v_exp_f32_e32 v102, v102
	v_exp_f32_e32 v103, v103
	v_exp_f32_e32 v104, v104
	v_exp_f32_e32 v105, v105
	v_exp_f32_e32 v106, v106
	v_exp_f32_e32 v107, v107
	v_exp_f32_e32 v108, v108
	s_waitcnt lgkmcnt(2)
	v_mfma_f32_32x32x64_f8f6f4 v[50:65], v[162:169], v[130:137], v[50:65]
	v_exp_f32_e32 v109, v109
	v_exp_f32_e32 v110, v110
	v_exp_f32_e32 v111, v111
	v_exp_f32_e32 v112, v112
	v_exp_f32_e32 v113, v113
	v_exp_f32_e32 v82, v82
	v_exp_f32_e32 v83, v83
	v_exp_f32_e32 v84, v84
	v_exp_f32_e32 v85, v85
	v_exp_f32_e32 v86, v86
	v_exp_f32_e32 v87, v87
	s_waitcnt lgkmcnt(0)
	v_mfma_f32_32x32x64_f8f6f4 v[66:81], v[162:169], v[114:121], v[66:81]
	v_exp_f32_e32 v88, v88
	v_exp_f32_e32 v89, v89
	v_exp_f32_e32 v90, v90
	v_exp_f32_e32 v91, v91
	v_exp_f32_e32 v92, v92
	v_exp_f32_e32 v93, v93
	v_exp_f32_e32 v94, v94
	v_exp_f32_e32 v95, v95
	v_exp_f32_e32 v96, v96
	v_exp_f32_e32 v97, v97
	s_andn2_b64 vcc, exec, s[28:29]
	s_cbranch_vccnz .LBB0_1316
	s_and_saveexec_b64 s[28:29], s[6:7]
	ds_write_b32 v187, v154 offset:49152
	s_or_b64 exec, exec, s[28:29]
	s_waitcnt lgkmcnt(0)
	v_add_u32_e32 v126, s78, v186
	ds_read_b128 v[114:117], v126 offset:49248
	ds_read_b128 v[118:121], v126 offset:49216
	ds_read_b128 v[122:125], v126 offset:49184
	ds_read_b128 v[126:129], v126 offset:49152
	ds_read_b128 v[244:247], v250 offset:49152
	s_waitcnt lgkmcnt(0)
	v_pk_mul_f32 v[14:15], v[14:15], v[114:115]
	v_pk_mul_f32 v[10:11], v[10:11], v[118:119]
	v_pk_mul_f32 v[6:7], v[6:7], v[122:123]
	v_pk_mul_f32 v[16:17], v[16:17], v[116:117]
	v_pk_mul_f32 v[12:13], v[12:13], v[120:121]
	v_pk_mul_f32 v[8:9], v[8:9], v[124:125]
	v_pk_mul_f32 v[4:5], v[4:5], v[128:129]
	v_pk_mul_f32 v[2:3], v[2:3], v[126:127]
	v_pk_mul_f32 v[46:47], v[46:47], v[114:115]
	v_pk_mul_f32 v[42:43], v[42:43], v[118:119]
	v_pk_mul_f32 v[38:39], v[38:39], v[122:123]
	v_pk_mul_f32 v[48:49], v[48:49], v[116:117]
	v_pk_mul_f32 v[44:45], v[44:45], v[120:121]
	v_pk_mul_f32 v[40:41], v[40:41], v[124:125]
	v_pk_mul_f32 v[36:37], v[36:37], v[128:129]
	v_pk_mul_f32 v[34:35], v[34:35], v[126:127]
	v_pk_mul_f32 v[62:63], v[62:63], v[114:115]
	v_pk_mul_f32 v[58:59], v[58:59], v[118:119]
	v_pk_mul_f32 v[54:55], v[54:55], v[122:123]
	v_pk_mul_f32 v[64:65], v[64:65], v[116:117]
	v_pk_mul_f32 v[60:61], v[60:61], v[120:121]
	v_pk_mul_f32 v[56:57], v[56:57], v[124:125]
	v_pk_mul_f32 v[52:53], v[52:53], v[128:129]
	v_pk_mul_f32 v[50:51], v[50:51], v[126:127]
	v_pk_mul_f32 v[78:79], v[78:79], v[114:115]
	v_pk_mul_f32 v[74:75], v[74:75], v[118:119]
	v_pk_mul_f32 v[70:71], v[70:71], v[122:123]
	v_pk_mul_f32 v[80:81], v[80:81], v[116:117]
	v_pk_mul_f32 v[76:77], v[76:77], v[120:121]
	v_pk_mul_f32 v[72:73], v[72:73], v[124:125]
	v_pk_mul_f32 v[68:69], v[68:69], v[128:129]
	v_pk_mul_f32 v[66:67], v[66:67], v[126:127]
	v_pk_mul_f32 v[18:19], v[18:19], v[244:245]
	v_pk_mul_f32 v[20:21], v[20:21], v[246:247]

.LBB0_1317:
	s_mov_b32 s98, 0x30003
	s_mov_b32 s99, 0x30003
	s_nop 15
	s_mov_b64 s[100:101], exec
	s_mov_b64 exec, s[98:99]
	ds_write_b128 v250, v[18:21] offset:49152
	s_mov_b64 exec, s[100:101]
	v_add_u32_e32 v249, s78, v186
	s_waitcnt lgkmcnt(0)
	ds_read_b128 v[30:33], v249 offset:49248
	ds_read_b128 v[26:29], v249 offset:49216
	ds_read_b128 v[22:25], v249 offset:49184
	ds_read_b128 v[18:21], v249 offset:49152
	s_waitcnt lgkmcnt(0)
	v_rcp_f32_e32 v18, v18
	v_rcp_f32_e32 v19, v19
	v_rcp_f32_e32 v20, v20
	v_rcp_f32_e32 v21, v21
	v_rcp_f32_e32 v22, v22
	v_rcp_f32_e32 v23, v23
	v_mul_f32_e32 v2, v2, v18
	v_mul_f32_e32 v34, v34, v18
	v_mul_f32_e32 v50, v50, v18
	v_mul_f32_e32 v18, v66, v18
	v_rcp_f32_e32 v24, v24
	v_rcp_f32_e32 v25, v25
	v_mov_b32_e32 v66, v179
	v_mul_f32_e32 v3, v3, v19
	v_rcp_f32_e32 v26, v26
	v_rcp_f32_e32 v27, v27
	s_waitcnt vmcnt(0) lgkmcnt(0)
	s_barrier
	v_cvt_pk_bf16_f32 v2, v2, v3
	v_mul_f32_e32 v4, v4, v20
	v_mul_f32_e32 v5, v5, v21
	v_rcp_f32_e32 v28, v28
	v_rcp_f32_e32 v29, v29
	ds_write_b32 v66, v2
	v_cvt_pk_bf16_f32 v2, v4, v5
	v_mul_f32_e32 v6, v6, v22
	v_mul_f32_e32 v7, v7, v23
	v_rcp_f32_e32 v30, v30
	v_rcp_f32_e32 v31, v31
	ds_write_b32 v66, v2 offset:2048
	v_cvt_pk_bf16_f32 v2, v6, v7
	v_mul_f32_e32 v8, v8, v24
	v_mul_f32_e32 v9, v9, v25
	v_rcp_f32_e32 v32, v32
	v_rcp_f32_e32 v33, v33
	ds_write_b32 v66, v2 offset:4096
	v_cvt_pk_bf16_f32 v2, v8, v9
	v_mul_f32_e32 v10, v10, v26
	v_mul_f32_e32 v11, v11, v27
	ds_write_b32 v66, v2 offset:6144
	v_cvt_pk_bf16_f32 v2, v10, v11
	v_mul_f32_e32 v12, v12, v28
	v_mul_f32_e32 v13, v13, v29
	ds_write_b32 v66, v2 offset:8192
	v_cvt_pk_bf16_f32 v2, v12, v13
	v_mul_f32_e32 v14, v14, v30
	v_mul_f32_e32 v15, v15, v31
	ds_write_b32 v66, v2 offset:10240
	v_cvt_pk_bf16_f32 v2, v14, v15
	v_mul_f32_e32 v16, v16, v32
	v_mul_f32_e32 v17, v17, v33
	ds_write_b32 v66, v2 offset:12288
	v_cvt_pk_bf16_f32 v2, v16, v17
	v_mul_f32_e32 v35, v35, v19
	ds_write_b32 v66, v2 offset:14336
	v_cvt_pk_bf16_f32 v2, v34, v35
	v_mul_f32_e32 v36, v36, v20
	v_mul_f32_e32 v37, v37, v21
	ds_write_b32 v66, v2 offset:16384
	v_cvt_pk_bf16_f32 v2, v36, v37
	v_mul_f32_e32 v38, v38, v22
	v_mul_f32_e32 v39, v39, v23
	ds_write_b32 v66, v2 offset:18432
	v_cvt_pk_bf16_f32 v2, v38, v39
	v_mul_f32_e32 v40, v40, v24
	v_mul_f32_e32 v41, v41, v25
	ds_write_b32 v66, v2 offset:20480
	v_cvt_pk_bf16_f32 v2, v40, v41
	v_mul_f32_e32 v42, v42, v26
	v_mul_f32_e32 v43, v43, v27
	ds_write_b32 v66, v2 offset:22528
	v_cvt_pk_bf16_f32 v2, v42, v43
	v_mul_f32_e32 v44, v44, v28
	v_mul_f32_e32 v45, v45, v29
	ds_write_b32 v66, v2 offset:24576
	v_cvt_pk_bf16_f32 v2, v44, v45
	v_mul_f32_e32 v46, v46, v30
	v_mul_f32_e32 v47, v47, v31
	ds_write_b32 v66, v2 offset:26624
	v_cvt_pk_bf16_f32 v2, v46, v47
	v_mul_f32_e32 v48, v48, v32
	v_mul_f32_e32 v49, v49, v33
	ds_write_b32 v66, v2 offset:28672
	v_cvt_pk_bf16_f32 v2, v48, v49
	v_mul_f32_e32 v51, v51, v19
	ds_write_b32 v66, v2 offset:30720
	v_cvt_pk_bf16_f32 v2, v50, v51
	v_mul_f32_e32 v52, v52, v20
	v_mul_f32_e32 v53, v53, v21
	ds_write_b32 v66, v2 offset:32768
	v_cvt_pk_bf16_f32 v2, v52, v53
	v_mul_f32_e32 v54, v54, v22
	v_mul_f32_e32 v55, v55, v23
	ds_write_b32 v66, v2 offset:34816
	v_cvt_pk_bf16_f32 v2, v54, v55
	v_mul_f32_e32 v56, v56, v24
	v_mul_f32_e32 v57, v57, v25
	ds_write_b32 v66, v2 offset:36864
	v_cvt_pk_bf16_f32 v2, v56, v57
	v_mul_f32_e32 v58, v58, v26
	v_mul_f32_e32 v59, v59, v27
	ds_write_b32 v66, v2 offset:38912
	v_cvt_pk_bf16_f32 v2, v58, v59
	v_mul_f32_e32 v60, v60, v28
	v_mul_f32_e32 v61, v61, v29
	ds_write_b32 v66, v2 offset:40960
	v_cvt_pk_bf16_f32 v2, v60, v61
	v_mul_f32_e32 v62, v62, v30
	v_mul_f32_e32 v63, v63, v31
	ds_write_b32 v66, v2 offset:43008
	v_cvt_pk_bf16_f32 v2, v62, v63
	v_mul_f32_e32 v64, v64, v32
	v_mul_f32_e32 v65, v65, v33
	ds_write_b32 v66, v2 offset:45056
	v_cvt_pk_bf16_f32 v2, v64, v65
	v_mul_f32_e32 v19, v67, v19
	ds_write_b32 v66, v2 offset:47104
	v_cvt_pk_bf16_f32 v2, v18, v19
	v_mul_f32_e32 v20, v68, v20
	v_mul_f32_e32 v21, v69, v21
	ds_write_b32 v66, v2 offset:49152
	v_cvt_pk_bf16_f32 v2, v20, v21
	v_mul_f32_e32 v22, v70, v22
	v_mul_f32_e32 v23, v71, v23
	ds_write_b32 v66, v2 offset:51200
	v_cvt_pk_bf16_f32 v2, v22, v23
	v_mul_f32_e32 v24, v72, v24
	v_mul_f32_e32 v25, v73, v25
	ds_write_b32 v66, v2 offset:53248
	v_cvt_pk_bf16_f32 v2, v24, v25
	v_mul_f32_e32 v26, v74, v26
	v_mul_f32_e32 v27, v75, v27
	ds_write_b32 v66, v2 offset:55296
	v_cvt_pk_bf16_f32 v2, v26, v27
	v_mul_f32_e32 v28, v76, v28
	v_mul_f32_e32 v29, v77, v29
	ds_write_b32 v66, v2 offset:57344
	v_cvt_pk_bf16_f32 v2, v28, v29
	v_mul_f32_e32 v30, v78, v30
	v_mul_f32_e32 v31, v79, v31
	ds_write_b32 v66, v2 offset:59392
	v_cvt_pk_bf16_f32 v2, v30, v31
	v_mov_b32_e32 v5, v0
	v_mul_f32_e32 v32, v80, v32
	v_mul_f32_e32 v33, v81, v33
	ds_write_b32 v66, v2 offset:61440
	v_cvt_pk_bf16_f32 v2, v32, v33
	ds_write_b32 v66, v2 offset:63488
	v_mov_b32_e32 v3, v181
	v_and_b32_e32 v4, 31, v5
	v_lshlrev_b32_e32 v2, 10, v4
	v_lshl_add_u64 v[6:7], s[96:97], 0, v[2:3]
	v_and_b32_e32 v2, 32, v5
	v_lshl_add_u64 v[6:7], v[6:7], 0, v[2:3]
	global_load_dwordx4 v[158:161], v[6:7], off offset:80
	global_load_dwordx4 v[154:157], v[6:7], off offset:64
	s_or_b32 s28, s87, 64
	v_readfirstlane_b32 s80, v5
	s_ashr_i32 s29, s28, 31
	s_ashr_i32 s81, s80, 6
	v_lshlrev_b32_e32 v3, 8, v5
	s_cmp_gt_i32 s81, 3
	v_and_b32_e32 v191, 0x3c00, v3
	v_lshlrev_b32_e32 v3, 4, v5
	s_cselect_b64 s[6:7], -1, 0
	s_and_b32 s95, s81, 3
	v_bitop3_b32 v192, v3, 48, v5 bitop3:0x48
	v_mov_b32_e32 v3, s80
	s_lshl_b32 s79, s95, 14
	v_bfi_b32 v3, s21, v3, v5
	v_or3_b32 v180, s79, v191, v192
	v_lshlrev_b32_e32 v182, 4, v3
	s_and_b64 vcc, exec, s[6:7]
	s_cbranch_vccnz .LBB0_1319
	s_ashr_i32 s89, s88, 31
	s_lshl_b64 s[38:39], s[88:89], 10
	s_add_u32 s38, s16, s38
	s_addc_u32 s39, s17, s39
	s_lshl_b32 s37, s95, 10
	s_cmp_lg_u32 0, -1
	v_lshl_add_u64 v[6:7], s[38:39], 0, v[180:181]
	s_cselect_b32 s38, 0, 0
	s_add_i32 s37, s38, s37
	v_lshl_add_u64 v[6:7], v[6:7], 0, s[28:29]
	s_mov_b32 m0, s37
	v_mov_b32_e32 v183, v181
	s_lshl_b32 s39, s81, 10
	global_load_lds_dwordx4 v[6:7], off
	v_lshl_add_u64 v[6:7], s[90:91], 0, v[182:183]
	s_add_i32 s40, s38, s39
	s_mov_b64 s[38:39], 0x1000
	v_lshl_add_u64 v[8:9], v[6:7], 0, s[38:39]
	s_or_b32 s38, s88, 64
	s_add_i32 m0, s40, 0x4000
	s_ashr_i32 s39, s38, 31
	global_load_lds_dwordx4 v182, s[90:91]
	s_add_i32 m0, s40, 0x5000
	s_lshl_b64 s[38:39], s[38:39], 10
	s_add_u32 s38, s16, s38
	s_addc_u32 s39, s17, s39
	global_load_lds_dwordx4 v[8:9], off
	v_lshl_add_u64 v[8:9], s[38:39], 0, v[180:181]
	s_or_b32 s38, s88, 0x80
	s_ashr_i32 s39, s38, 31
	s_add_i32 m0, s37, 0x1000
	s_lshl_b64 s[38:39], s[38:39], 10
	s_add_u32 s38, s16, s38
	v_lshl_add_u64 v[8:9], v[8:9], 0, s[28:29]
	s_addc_u32 s39, s17, s39
	global_load_lds_dwordx4 v[8:9], off
	v_lshl_add_u64 v[8:9], s[38:39], 0, v[180:181]
	v_lshl_add_u64 v[8:9], v[8:9], 0, s[28:29]
	s_add_i32 m0, s37, 0x2000
	s_mov_b64 s[38:39], 0x2000
	global_load_lds_dwordx4 v[8:9], off
	v_lshl_add_u64 v[8:9], v[6:7], 0, s[38:39]
	s_add_i32 m0, s40, 0x6000
	s_mov_b64 s[38:39], 0x3000
	global_load_lds_dwordx4 v[8:9], off
	v_lshl_add_u64 v[6:7], v[6:7], 0, s[38:39]
	s_add_i32 m0, s40, 0x7000
	s_nop 0
	global_load_lds_dwordx4 v[6:7], off

.LBB0_1323:
	s_and_b32 s37, s80, 0xffffffc0
	v_lshlrev_b32_e32 v6, 2, v5
	v_lshlrev_b32_e32 v3, 6, v4
	v_and_b32_e32 v6, 48, v6
	s_cmp_lg_u32 0, -1
	v_bitop3_b32 v194, v6, v3, v2 bitop3:0xde
	s_cselect_b32 s38, 0, 0
	v_lshlrev_b32_e32 v2, 3, v5
	v_and_b32_e32 v193, 63, v5
	v_add_u32_e32 v183, s38, v194
	s_addk_i32 s38, 0x4000
	v_and_b32_e32 v2, 32, v2
	s_lshl_b32 s37, s37, 2
	v_add_u32_e32 v188, s38, v194
	v_sub_u32_e32 v195, 16, v2
	v_lshrrev_b32_e32 v2, 5, v193
	s_add_i32 s78, s37, 0
	v_add_u32_e32 v190, v183, v195
	s_mov_b64 s[38:39], -1
	s_and_b64 vcc, exec, s[6:7]
	v_add_u32_e32 v189, v188, v195
	v_cmp_gt_u32_e64 s[6:7], 32, v193
	v_lshlrev_b32_e32 v186, 4, v2
	v_lshl_add_u32 v187, v4, 2, s78
	v_and_b32_e32 v248, 31, v193
	v_mov_b32_e32 v249, 0x38383838
	v_cmp_eq_u32_e64 s[98:99], 0, v248
	v_cmp_eq_u32_e64 s[100:101], 17, v248
	v_and_b32_e32 v248, 15, v193
	v_lshrrev_b32_e32 v250, 4, v193
	s_or_b64 s[98:99], s[98:99], s[100:101]
	v_lshlrev_b32_e32 v248, 6, v248
	v_lshl_add_u32 v250, v250, 4, v248
	v_cndmask_b32_e64 v146, 0, v249, s[98:99]
	v_add_u32_e32 v250, s78, v250
	v_mov_b32_e32 v147, v146
	v_mov_b32_e32 v148, v146
	v_mov_b32_e32 v149, v146
	v_mov_b32_e32 v150, v146
	v_mov_b32_e32 v151, v146
	v_mov_b32_e32 v152, v146
	v_mov_b32_e32 v153, v146
	s_cbranch_vccz .LBB0_1376
	ds_read_b128 v[18:21], v183 offset:0
	ds_read_b128 v[22:25], v190 offset:0
	ds_read_b128 v[34:37], v183 offset:0x800
	ds_read_b128 v[38:41], v190 offset:0x800
	s_waitcnt lgkmcnt(0)
	s_waitcnt vmcnt(0)
	v_mfma_f32_32x32x64_f8f6f4 v[18:33], v[18:25], v[154:161], 0
	s_mov_b32 s37, s36
	s_mov_b32 s38, s36
	s_mov_b32 s39, s36
	s_mov_b32 s40, s36
	s_mov_b32 s41, s36
	s_mov_b32 s42, s36
	s_mov_b32 s43, s36
	s_mov_b32 s44, s36
	s_mov_b32 s45, s36
	s_mov_b32 s46, s36
	s_mov_b32 s47, s36
	s_mov_b32 s48, s36
	s_mov_b32 s49, s36
	s_mov_b32 s50, s36
	s_mov_b32 s51, s36
	v_mov_b64_e32 v[2:3], s[36:37]
	v_mov_b64_e32 v[4:5], s[38:39]
	v_mov_b64_e32 v[6:7], s[40:41]
	v_mov_b64_e32 v[8:9], s[42:43]
	v_mov_b64_e32 v[10:11], s[44:45]
	v_mov_b64_e32 v[12:13], s[46:47]
	v_mov_b64_e32 v[14:15], s[48:49]
	v_mov_b64_e32 v[16:17], s[50:51]
	v_max_f32_e32 v42, v19, v19
	v_max_f32_e32 v43, v18, v18
	v_max_f32_e32 v42, v43, v42
	v_max3_f32 v42, v42, v20, v21
	v_max3_f32 v42, v42, v22, v23
	v_max3_f32 v42, v42, v24, v25
	v_max3_f32 v42, v42, v26, v27
	v_max3_f32 v42, v42, v28, v29
	v_max3_f32 v50, v42, v30, v31
	v_mfma_f32_32x32x64_f8f6f4 v[34:49], v[34:41], v[154:161], 0
	v_max3_f32 v50, v50, v32, v33
	s_cmp_lg_u32 0, -1
	s_cselect_b32 s37, 0, 0
	v_mov_b32_e32 v130, v181
	v_mov_b32_e32 v131, v181
	s_add_i32 s38, s37, 0x1000
	s_waitcnt vmcnt(0) lgkmcnt(0)
	s_barrier
	v_add_u32_e32 v207, s38, v194
	v_add_u32_e32 v209, v207, v195
	s_nop 11
	v_max3_f32 v50, v50, v34, v35
	v_max3_f32 v50, v50, v36, v37
	v_max3_f32 v50, v50, v38, v39
	v_max3_f32 v50, v50, v40, v41
	v_max3_f32 v50, v50, v42, v43
	v_max3_f32 v50, v50, v44, v45
	v_max3_f32 v50, v50, v46, v47
	v_max3_f32 v50, v50, v48, v49
	v_mov_b32_e32 v51, v50
	s_nop 1
	v_permlane32_swap_b32_e32 v50, v51
	v_max_f32_e32 v51, v51, v51
	v_max_f32_e32 v50, v50, v50
	v_max_f32_e32 v50, v50, v51
	v_add_f32_e32 v198, 0xc0600000, v50
	v_sub_f32_e32 v18, v18, v198
	v_sub_f32_e32 v19, v19, v198
	v_sub_f32_e32 v22, v22, v198
	v_sub_f32_e32 v23, v23, v198
	v_exp_f32_e32 v50, v18
	v_exp_f32_e32 v51, v19
	v_exp_f32_e32 v54, v22
	v_exp_f32_e32 v55, v23
	v_xor_b32_e32 v82, 0x80000000, v198
	v_sub_f32_e32 v20, v20, v198
	v_sub_f32_e32 v21, v21, v198
	v_sub_f32_e32 v24, v24, v198
	v_sub_f32_e32 v25, v25, v198
	v_mov_b32_e32 v83, v82
	v_mov_b32_e32 v84, v82
	v_mov_b32_e32 v85, v82
	v_mov_b32_e32 v86, v82
	v_mov_b32_e32 v87, v82
	v_mov_b32_e32 v88, v82
	v_mov_b32_e32 v89, v82
	v_mov_b32_e32 v90, v82
	v_mov_b32_e32 v91, v82
	v_mov_b32_e32 v92, v82
	v_mov_b32_e32 v93, v82
	v_mov_b32_e32 v94, v82
	v_mov_b32_e32 v95, v82
	v_mov_b32_e32 v96, v82
	v_mov_b32_e32 v97, v82
	v_exp_f32_e32 v52, v20
	v_exp_f32_e32 v53, v21
	v_exp_f32_e32 v56, v24
	v_exp_f32_e32 v57, v25
	v_cvt_pk_fp8_f32 v130, v50, v51
	v_cvt_pk_fp8_f32 v131, v54, v55
	ds_read_b128 v[18:21], v207 offset:0
	v_sub_f32_e32 v26, v26, v198
	v_sub_f32_e32 v27, v27, v198
	v_sub_f32_e32 v28, v28, v198
	v_sub_f32_e32 v29, v29, v198
	ds_read_b128 v[22:25], v209 offset:0
	v_sub_f32_e32 v34, v34, v198
	v_sub_f32_e32 v35, v35, v198
	v_sub_f32_e32 v36, v36, v198
	v_sub_f32_e32 v37, v37, v198
	v_sub_f32_e32 v38, v38, v198
	v_sub_f32_e32 v39, v39, v198
	v_sub_f32_e32 v40, v40, v198
	v_sub_f32_e32 v41, v41, v198
	v_sub_f32_e32 v42, v42, v198
	v_sub_f32_e32 v43, v43, v198
	v_sub_f32_e32 v44, v44, v198
	v_sub_f32_e32 v45, v45, v198
	v_sub_f32_e32 v30, v30, v198
	v_sub_f32_e32 v46, v46, v198
	v_sub_f32_e32 v31, v31, v198
	v_sub_f32_e32 v47, v47, v198
	v_sub_f32_e32 v32, v32, v198
	v_sub_f32_e32 v48, v48, v198
	v_sub_f32_e32 v33, v33, v198
	v_sub_f32_e32 v49, v49, v198
	v_exp_f32_e32 v58, v26
	v_exp_f32_e32 v59, v27
	v_exp_f32_e32 v60, v28
	v_exp_f32_e32 v61, v29
	ds_read_b128 v[26:29], v207 offset:0x800
	v_exp_f32_e32 v34, v34
	v_exp_f32_e32 v35, v35
	v_exp_f32_e32 v36, v36
	v_exp_f32_e32 v37, v37
	v_exp_f32_e32 v38, v38
	v_exp_f32_e32 v39, v39
	v_exp_f32_e32 v40, v40
	v_exp_f32_e32 v41, v41
	v_exp_f32_e32 v42, v42
	v_exp_f32_e32 v43, v43
	v_exp_f32_e32 v44, v44
	v_exp_f32_e32 v45, v45
	v_exp_f32_e32 v62, v30
	v_exp_f32_e32 v46, v46
	v_exp_f32_e32 v63, v31
	v_exp_f32_e32 v47, v47
	v_exp_f32_e32 v64, v32
	v_exp_f32_e32 v48, v48
	v_exp_f32_e32 v65, v33
	v_exp_f32_e32 v49, v49
	ds_read_b128 v[30:33], v209 offset:0x800
	v_cvt_pk_fp8_f32 v130, v52, v53 op_sel:[0,0,1]
	v_cvt_pk_fp8_f32 v131, v56, v57 op_sel:[0,0,1]
	s_waitcnt lgkmcnt(2)
	v_mfma_f32_32x32x64_f8f6f4 v[98:113], v[18:25], v[154:161], v[82:97]
	v_mov_b32_e32 v132, v181
	v_mov_b32_e32 v133, v181
	v_cvt_pk_fp8_f32 v132, v58, v59
	v_cvt_pk_fp8_f32 v133, v62, v63
	ds_read_b128 v[170:173], v188 offset:0
	ds_read_b128 v[174:177], v189 offset:0
	v_cvt_pk_fp8_f32 v132, v60, v61 op_sel:[0,0,1]
	v_cvt_pk_fp8_f32 v133, v64, v65 op_sel:[0,0,1]
	s_waitcnt lgkmcnt(2)
	v_mov_b64_e32 v[128:129], v[96:97]
	v_mov_b64_e32 v[126:127], v[94:95]
	v_mov_b64_e32 v[124:125], v[92:93]
	v_mov_b64_e32 v[122:123], v[90:91]
	v_mov_b64_e32 v[120:121], v[88:89]
	v_mov_b64_e32 v[118:119], v[86:87]
	v_mov_b64_e32 v[116:117], v[84:85]
	v_mov_b64_e32 v[114:115], v[82:83]
	v_mov_b32_e32 v134, v181
	v_mov_b32_e32 v135, v181
	v_mfma_f32_32x32x64_f8f6f4 v[114:129], v[26:33], v[154:161], v[114:129]
	v_mov_b32_e32 v136, v181
	v_mov_b32_e32 v137, v181
	v_cvt_pk_fp8_f32 v134, v34, v35
	v_cvt_pk_fp8_f32 v135, v38, v39
	v_cvt_pk_fp8_f32 v136, v42, v43
	v_cvt_pk_fp8_f32 v137, v46, v47
	v_cvt_pk_fp8_f32 v134, v36, v37 op_sel:[0,0,1]
	v_cvt_pk_fp8_f32 v135, v40, v41 op_sel:[0,0,1]
	v_cvt_pk_fp8_f32 v136, v44, v45 op_sel:[0,0,1]
	v_cvt_pk_fp8_f32 v137, v48, v49 op_sel:[0,0,1]
	s_nop 0
	ds_read_b128 v[138:141], v188 offset:0x800
	ds_read_b128 v[142:145], v189 offset:0x800
	s_nop 0
	v_mfma_f32_16x16x128_f8f6f4 v[18:21], v[130:137], v[146:153], 0
	s_add_i32 s38, s37, 0x2000
	v_add_u32_e32 v205, s38, v194
	s_add_i32 s38, s37, 0x6000
	v_add_u32_e32 v203, s38, v194
	s_add_i32 s38, s37, 0x3000
	s_waitcnt vmcnt(0) lgkmcnt(0)
	s_barrier
	v_add_u32_e32 v201, s38, v194
	s_add_i32 s38, s37, 0x8000
	s_add_i32 s37, s37, 0xa000
	v_add_u32_e32 v199, s38, v194
	v_add_u32_e32 v196, s37, v194
	v_mov_b64_e32 v[48:49], v[16:17]
	v_mov_b64_e32 v[64:65], v[16:17]
	v_mov_b64_e32 v[80:81], v[16:17]
	v_add_u32_e32 v206, v205, v195
	v_add_u32_e32 v204, v203, v195
	v_add_u32_e32 v202, v201, v195
	v_add_u32_e32 v200, v199, v195
	v_add_u32_e32 v197, v196, v195
	s_mov_b32 s37, -2
	v_mov_b64_e32 v[46:47], v[14:15]
	v_mov_b64_e32 v[44:45], v[12:13]
	v_mov_b64_e32 v[42:43], v[10:11]
	v_mov_b64_e32 v[40:41], v[8:9]
	v_mov_b64_e32 v[38:39], v[6:7]
	v_mov_b64_e32 v[36:37], v[4:5]
	v_mov_b64_e32 v[34:35], v[2:3]
	v_mov_b64_e32 v[62:63], v[14:15]
	v_mov_b64_e32 v[60:61], v[12:13]
	v_mov_b64_e32 v[58:59], v[10:11]
	v_mov_b64_e32 v[56:57], v[8:9]
	v_mov_b64_e32 v[54:55], v[6:7]
	v_mov_b64_e32 v[52:53], v[4:5]
	v_mov_b64_e32 v[50:51], v[2:3]
	v_mov_b64_e32 v[78:79], v[14:15]
	v_mov_b64_e32 v[76:77], v[12:13]
	v_mov_b64_e32 v[74:75], v[10:11]
	v_mov_b64_e32 v[72:73], v[8:9]
	v_mov_b64_e32 v[70:71], v[6:7]
	v_mov_b64_e32 v[68:69], v[4:5]
	v_mov_b64_e32 v[66:67], v[2:3]
	s_branch .LBB0_1327

.LBB0_1357:
	s_waitcnt lgkmcnt(2)
	v_mfma_f32_32x32x64_f8f6f4 v[34:49], v[130:137], v[138:145], v[34:49]
	ds_read_b128 v[210:213], v188 offset:0x1800
	ds_read_b128 v[214:217], v189 offset:0x1800
	v_exp_f32_e32 v98, v98
	v_exp_f32_e32 v99, v99
	v_exp_f32_e32 v100, v100
	v_exp_f32_e32 v101, v101
	v_exp_f32_e32 v102, v102
	v_exp_f32_e32 v103, v103
	v_exp_f32_e32 v104, v104
	v_exp_f32_e32 v105, v105
	v_exp_f32_e32 v106, v106
	v_exp_f32_e32 v107, v107
	v_exp_f32_e32 v108, v108
	s_waitcnt lgkmcnt(2)
	v_mfma_f32_32x32x64_f8f6f4 v[50:65], v[130:137], v[162:169], v[50:65]
	v_exp_f32_e32 v109, v109
	v_exp_f32_e32 v110, v110
	v_exp_f32_e32 v111, v111
	v_exp_f32_e32 v112, v112
	v_exp_f32_e32 v113, v113
	v_exp_f32_e32 v114, v114
	v_exp_f32_e32 v115, v115
	v_exp_f32_e32 v116, v116
	v_exp_f32_e32 v117, v117
	v_exp_f32_e32 v118, v118
	v_exp_f32_e32 v119, v119
	s_waitcnt lgkmcnt(0)
	v_mfma_f32_32x32x64_f8f6f4 v[66:81], v[130:137], v[210:217], v[66:81]
	v_exp_f32_e32 v120, v120
	v_exp_f32_e32 v121, v121
	v_exp_f32_e32 v122, v122
	v_exp_f32_e32 v123, v123
	v_exp_f32_e32 v124, v124
	v_exp_f32_e32 v125, v125
	v_exp_f32_e32 v126, v126
	v_exp_f32_e32 v127, v127
	v_exp_f32_e32 v128, v128
	v_exp_f32_e32 v129, v129
	s_andn2_b64 vcc, exec, s[38:39]
	s_cbranch_vccnz .LBB0_1361
	s_and_saveexec_b64 s[38:39], s[6:7]
	ds_write_b32 v187, v170 offset:49152
	s_or_b64 exec, exec, s[38:39]
	s_waitcnt lgkmcnt(0)
	v_add_u32_e32 v166, s78, v186
	ds_read_b128 v[138:141], v166 offset:49248
	ds_read_b128 v[142:145], v166 offset:49216
	ds_read_b128 v[162:165], v166 offset:49184
	ds_read_b128 v[166:169], v166 offset:49152
	ds_read_b128 v[244:247], v250 offset:49152
	s_waitcnt lgkmcnt(0)
	v_pk_mul_f32 v[14:15], v[14:15], v[138:139]
	v_pk_mul_f32 v[10:11], v[10:11], v[142:143]
	v_pk_mul_f32 v[6:7], v[6:7], v[162:163]
	v_pk_mul_f32 v[16:17], v[16:17], v[140:141]
	v_pk_mul_f32 v[12:13], v[12:13], v[144:145]
	v_pk_mul_f32 v[8:9], v[8:9], v[164:165]
	v_pk_mul_f32 v[4:5], v[4:5], v[168:169]
	v_pk_mul_f32 v[2:3], v[2:3], v[166:167]
	v_pk_mul_f32 v[46:47], v[46:47], v[138:139]
	v_pk_mul_f32 v[42:43], v[42:43], v[142:143]
	v_pk_mul_f32 v[38:39], v[38:39], v[162:163]
	v_pk_mul_f32 v[48:49], v[48:49], v[140:141]
	v_pk_mul_f32 v[44:45], v[44:45], v[144:145]
	v_pk_mul_f32 v[40:41], v[40:41], v[164:165]
	v_pk_mul_f32 v[36:37], v[36:37], v[168:169]
	v_pk_mul_f32 v[34:35], v[34:35], v[166:167]
	v_pk_mul_f32 v[62:63], v[62:63], v[138:139]
	v_pk_mul_f32 v[58:59], v[58:59], v[142:143]
	v_pk_mul_f32 v[54:55], v[54:55], v[162:163]
	v_pk_mul_f32 v[64:65], v[64:65], v[140:141]
	v_pk_mul_f32 v[60:61], v[60:61], v[144:145]
	v_pk_mul_f32 v[56:57], v[56:57], v[164:165]
	v_pk_mul_f32 v[52:53], v[52:53], v[168:169]
	v_pk_mul_f32 v[50:51], v[50:51], v[166:167]
	v_pk_mul_f32 v[78:79], v[78:79], v[138:139]
	v_pk_mul_f32 v[74:75], v[74:75], v[142:143]
	v_pk_mul_f32 v[70:71], v[70:71], v[162:163]
	v_pk_mul_f32 v[80:81], v[80:81], v[140:141]
	v_pk_mul_f32 v[76:77], v[76:77], v[144:145]
	v_pk_mul_f32 v[72:73], v[72:73], v[164:165]
	v_pk_mul_f32 v[68:69], v[68:69], v[168:169]
	v_pk_mul_f32 v[66:67], v[66:67], v[166:167]
	v_pk_mul_f32 v[18:19], v[18:19], v[244:245]
	v_pk_mul_f32 v[20:21], v[20:21], v[246:247]

.LBB0_1364:
	s_waitcnt lgkmcnt(2)
	v_mfma_f32_32x32x64_f8f6f4 v[34:49], v[130:137], v[162:169], v[34:49]
	ds_read_b128 v[210:213], v203 offset:0x1800
	ds_read_b128 v[214:217], v204 offset:0x1800
	v_exp_f32_e32 v98, v98
	v_exp_f32_e32 v99, v99
	v_exp_f32_e32 v100, v100
	v_exp_f32_e32 v101, v101
	v_exp_f32_e32 v102, v102
	v_exp_f32_e32 v103, v103
	v_exp_f32_e32 v104, v104
	v_exp_f32_e32 v105, v105
	v_exp_f32_e32 v106, v106
	v_exp_f32_e32 v107, v107
	v_exp_f32_e32 v108, v108
	s_waitcnt lgkmcnt(2)
	v_mfma_f32_32x32x64_f8f6f4 v[50:65], v[130:137], v[138:145], v[50:65]
	v_exp_f32_e32 v109, v109
	v_exp_f32_e32 v110, v110
	v_exp_f32_e32 v111, v111
	v_exp_f32_e32 v112, v112
	v_exp_f32_e32 v113, v113
	v_exp_f32_e32 v114, v114
	v_exp_f32_e32 v115, v115
	v_exp_f32_e32 v116, v116
	v_exp_f32_e32 v117, v117
	v_exp_f32_e32 v118, v118
	v_exp_f32_e32 v119, v119
	s_waitcnt lgkmcnt(0)
	v_mfma_f32_32x32x64_f8f6f4 v[66:81], v[130:137], v[210:217], v[66:81]
	v_exp_f32_e32 v120, v120
	v_exp_f32_e32 v121, v121
	v_exp_f32_e32 v122, v122
	v_exp_f32_e32 v123, v123
	v_exp_f32_e32 v124, v124
	v_exp_f32_e32 v125, v125
	v_exp_f32_e32 v126, v126
	v_exp_f32_e32 v127, v127
	v_exp_f32_e32 v128, v128
	v_exp_f32_e32 v129, v129
	s_andn2_b64 vcc, exec, s[38:39]
	s_cbranch_vccnz .LBB0_1368
	s_and_saveexec_b64 s[38:39], s[6:7]
	ds_write_b32 v187, v170 offset:49152
	s_or_b64 exec, exec, s[38:39]
	s_waitcnt lgkmcnt(0)
	v_add_u32_e32 v166, s78, v186
	ds_read_b128 v[138:141], v166 offset:49248
	ds_read_b128 v[142:145], v166 offset:49216
	ds_read_b128 v[162:165], v166 offset:49184
	ds_read_b128 v[166:169], v166 offset:49152
	ds_read_b128 v[244:247], v250 offset:49152
	s_waitcnt lgkmcnt(0)
	v_pk_mul_f32 v[14:15], v[14:15], v[138:139]
	v_pk_mul_f32 v[10:11], v[10:11], v[142:143]
	v_pk_mul_f32 v[6:7], v[6:7], v[162:163]
	v_pk_mul_f32 v[16:17], v[16:17], v[140:141]
	v_pk_mul_f32 v[12:13], v[12:13], v[144:145]
	v_pk_mul_f32 v[8:9], v[8:9], v[164:165]
	v_pk_mul_f32 v[4:5], v[4:5], v[168:169]
	v_pk_mul_f32 v[2:3], v[2:3], v[166:167]
	v_pk_mul_f32 v[46:47], v[46:47], v[138:139]
	v_pk_mul_f32 v[42:43], v[42:43], v[142:143]
	v_pk_mul_f32 v[38:39], v[38:39], v[162:163]
	v_pk_mul_f32 v[48:49], v[48:49], v[140:141]
	v_pk_mul_f32 v[44:45], v[44:45], v[144:145]
	v_pk_mul_f32 v[40:41], v[40:41], v[164:165]
	v_pk_mul_f32 v[36:37], v[36:37], v[168:169]
	v_pk_mul_f32 v[34:35], v[34:35], v[166:167]
	v_pk_mul_f32 v[62:63], v[62:63], v[138:139]
	v_pk_mul_f32 v[58:59], v[58:59], v[142:143]
	v_pk_mul_f32 v[54:55], v[54:55], v[162:163]
	v_pk_mul_f32 v[64:65], v[64:65], v[140:141]
	v_pk_mul_f32 v[60:61], v[60:61], v[144:145]
	v_pk_mul_f32 v[56:57], v[56:57], v[164:165]
	v_pk_mul_f32 v[52:53], v[52:53], v[168:169]
	v_pk_mul_f32 v[50:51], v[50:51], v[166:167]
	v_pk_mul_f32 v[78:79], v[78:79], v[138:139]
	v_pk_mul_f32 v[74:75], v[74:75], v[142:143]
	v_pk_mul_f32 v[70:71], v[70:71], v[162:163]
	v_pk_mul_f32 v[80:81], v[80:81], v[140:141]
	v_pk_mul_f32 v[76:77], v[76:77], v[144:145]
	v_pk_mul_f32 v[72:73], v[72:73], v[164:165]
	v_pk_mul_f32 v[68:69], v[68:69], v[168:169]
	v_pk_mul_f32 v[66:67], v[66:67], v[166:167]
	v_pk_mul_f32 v[18:19], v[18:19], v[244:245]
	v_pk_mul_f32 v[20:21], v[20:21], v[246:247]

.LBB0_1376:
	s_and_b64 vcc, exec, s[38:39]
	s_cbranch_vccz .LBB0_1202
	ds_read_b128 v[18:21], v183 offset:0
	ds_read_b128 v[22:25], v190 offset:0
	ds_read_b128 v[34:37], v183 offset:0x800
	ds_read_b128 v[38:41], v190 offset:0x800
	s_waitcnt lgkmcnt(0)
	s_waitcnt vmcnt(0)
	s_nop 11
	v_mfma_f32_32x32x64_f8f6f4 v[18:33], v[18:25], v[154:161], 0
	s_mov_b32 s37, s36
	s_mov_b32 s38, s36
	s_mov_b32 s39, s36
	s_mov_b32 s40, s36
	s_mov_b32 s41, s36
	s_mov_b32 s42, s36
	s_mov_b32 s43, s36
	s_mov_b32 s44, s36
	s_mov_b32 s45, s36
	s_mov_b32 s46, s36
	s_mov_b32 s47, s36
	s_mov_b32 s48, s36
	s_mov_b32 s49, s36
	s_mov_b32 s50, s36
	s_mov_b32 s51, s36
	v_mov_b64_e32 v[2:3], s[36:37]
	v_mov_b64_e32 v[4:5], s[38:39]
	v_mov_b64_e32 v[6:7], s[40:41]
	v_mov_b64_e32 v[8:9], s[42:43]
	v_mov_b64_e32 v[10:11], s[44:45]
	v_mov_b64_e32 v[12:13], s[46:47]
	v_mov_b64_e32 v[14:15], s[48:49]
	v_mov_b64_e32 v[16:17], s[50:51]
	v_max_f32_e32 v42, v19, v19
	v_max_f32_e32 v43, v18, v18
	v_max_f32_e32 v42, v43, v42
	v_max3_f32 v42, v42, v20, v21
	v_max3_f32 v42, v42, v22, v23
	v_max3_f32 v42, v42, v24, v25
	v_max3_f32 v42, v42, v26, v27
	v_max3_f32 v42, v42, v28, v29
	v_max3_f32 v50, v42, v30, v31
	v_mfma_f32_32x32x64_f8f6f4 v[34:49], v[34:41], v[154:161], 0
	v_max3_f32 v50, v50, v32, v33
	s_lshl_b32 s45, s95, 10
	s_lshl_b32 s46, s81, 10
	s_cmp_lg_u32 0, -1
	s_cselect_b32 s38, 0, 0
	s_add_i32 s37, s38, 0x2000
	s_add_i32 s39, s38, 0x3000
	s_add_i32 s6, s38, 0x1000
	v_add_u32_e32 v203, s37, v194
	s_add_i32 s37, s38, 0x6000
	v_add_u32_e32 v199, s39, v194
	s_add_i32 s39, s38, 0x8000
	s_add_i32 s38, s38, 0xa000
	v_add_u32_e32 v205, s6, v194
	v_add_u32_e32 v201, s37, v194
	s_nop 4
	v_max3_f32 v50, v50, v34, v35
	v_max3_f32 v50, v50, v36, v37
	v_max3_f32 v50, v50, v38, v39
	v_max3_f32 v50, v50, v40, v41
	v_max3_f32 v50, v50, v42, v43
	v_max3_f32 v50, v50, v44, v45
	v_max3_f32 v50, v50, v46, v47
	v_max3_f32 v50, v50, v48, v49
	v_mov_b32_e32 v51, v50
	s_nop 1
	v_permlane32_swap_b32_e32 v50, v51
	v_max_f32_e32 v51, v51, v51
	v_max_f32_e32 v50, v50, v50
	v_max_f32_e32 v50, v50, v51
	v_add_f32_e32 v198, 0xc0600000, v50
	v_sub_f32_e32 v18, v18, v198
	v_sub_f32_e32 v19, v19, v198
	v_add_u32_e32 v196, s39, v194
	v_add_u32_e32 v194, s38, v194
	s_lshl_b32 s38, s80, 4
	v_exp_f32_e32 v114, v18
	v_exp_f32_e32 v115, v19
	v_lshl_add_u64 v[18:19], s[16:17], 0, v[180:181]
	s_and_b32 s38, s38, 0xfffffc00
	s_ashr_i32 s89, s88, 31
	s_or_b32 s40, s88, 0x100
	s_add_i32 s41, s94, 0x4100
	s_or_b32 s42, s88, 0x140
	s_add_i32 s43, s94, 0x4140
	v_lshl_add_u64 v[170:171], v[18:19], 0, s[28:29]
	v_lshl_or_b32 v18, v193, 4, s38
	s_lshl_b64 s[38:39], s[88:89], 10
	s_add_u32 s38, s38, s87
	v_xor_b32_e32 v82, 0x80000000, v198
	v_sub_f32_e32 v34, v34, v198
	v_sub_f32_e32 v35, v35, v198
	v_sub_f32_e32 v20, v20, v198
	v_sub_f32_e32 v36, v36, v198
	v_sub_f32_e32 v21, v21, v198
	v_sub_f32_e32 v37, v37, v198
	v_sub_f32_e32 v22, v22, v198
	v_sub_f32_e32 v38, v38, v198
	v_sub_f32_e32 v23, v23, v198
	v_sub_f32_e32 v39, v39, v198
	v_sub_f32_e32 v24, v24, v198
	v_sub_f32_e32 v40, v40, v198
	v_sub_f32_e32 v25, v25, v198
	v_sub_f32_e32 v41, v41, v198
	v_sub_f32_e32 v26, v26, v198
	v_sub_f32_e32 v42, v42, v198
	v_sub_f32_e32 v27, v27, v198
	v_sub_f32_e32 v43, v43, v198
	v_sub_f32_e32 v28, v28, v198
	v_sub_f32_e32 v44, v44, v198
	v_sub_f32_e32 v29, v29, v198
	v_sub_f32_e32 v45, v45, v198
	v_sub_f32_e32 v30, v30, v198
	v_sub_f32_e32 v46, v46, v198
	v_sub_f32_e32 v31, v31, v198
	v_sub_f32_e32 v47, v47, v198
	v_sub_f32_e32 v32, v32, v198
	v_sub_f32_e32 v48, v48, v198
	v_sub_f32_e32 v33, v33, v198
	v_sub_f32_e32 v49, v49, v198
	s_addc_u32 s39, s39, s76
	v_mov_b32_e32 v83, v82
	v_mov_b32_e32 v84, v82
	v_mov_b32_e32 v85, v82
	v_mov_b32_e32 v86, v82
	v_mov_b32_e32 v87, v82
	v_mov_b32_e32 v88, v82
	v_mov_b32_e32 v89, v82
	v_mov_b32_e32 v90, v82
	v_mov_b32_e32 v91, v82
	v_mov_b32_e32 v92, v82
	v_mov_b32_e32 v93, v82
	v_mov_b32_e32 v94, v82
	v_mov_b32_e32 v95, v82
	v_mov_b32_e32 v96, v82
	v_mov_b32_e32 v97, v82
	v_exp_f32_e32 v98, v34
	v_exp_f32_e32 v99, v35
	v_exp_f32_e32 v116, v20
	v_exp_f32_e32 v100, v36
	v_exp_f32_e32 v117, v21
	v_exp_f32_e32 v101, v37
	v_exp_f32_e32 v118, v22
	v_exp_f32_e32 v102, v38
	v_exp_f32_e32 v119, v23
	v_exp_f32_e32 v103, v39
	v_exp_f32_e32 v120, v24
	v_exp_f32_e32 v104, v40
	v_exp_f32_e32 v121, v25
	v_exp_f32_e32 v105, v41
	v_exp_f32_e32 v122, v26
	v_exp_f32_e32 v106, v42
	v_exp_f32_e32 v123, v27
	v_exp_f32_e32 v107, v43
	v_exp_f32_e32 v124, v28
	v_exp_f32_e32 v108, v44
	v_exp_f32_e32 v125, v29
	v_exp_f32_e32 v109, v45
	v_exp_f32_e32 v126, v30
	v_exp_f32_e32 v110, v46
	v_exp_f32_e32 v127, v31
	v_exp_f32_e32 v111, v47
	v_exp_f32_e32 v128, v32
	v_exp_f32_e32 v112, v48
	v_exp_f32_e32 v129, v33
	v_exp_f32_e32 v113, v49
	v_mov_b32_e32 v19, v181
	s_add_u32 s38, s38, 0x29c30040
	s_waitcnt vmcnt(3) lgkmcnt(0)
	s_barrier
	v_lshl_add_u64 v[172:173], s[92:93], 0, v[18:19]
	s_addc_u32 s39, s39, 0
	v_add3_u32 v18, s79, v191, v192
	v_lshl_add_u64 v[174:175], s[38:39], 0, v[18:19]
	v_mov_b32_e32 v162, 0
	v_mov_b64_e32 v[48:49], v[16:17]
	v_mov_b64_e32 v[64:65], v[16:17]
	v_mov_b64_e32 v[80:81], v[16:17]
	v_mov_b64_e32 v[32:33], v[16:17]
	v_add_u32_e32 v206, v205, v195
	v_cmp_gt_u32_e64 s[6:7], 32, v193
	v_add_u32_e32 v204, v203, v195
	v_add_u32_e32 v202, v201, v195
	s_movk_i32 s37, 0x100
	v_add_u32_e32 v200, v199, v195
	v_add_u32_e32 v197, v196, v195
	v_add_u32_e32 v195, v194, v195
	s_mov_b32 s44, -3
	s_add_i32 s45, s45, 0
	s_add_i32 s46, s46, 0
	v_mov_b64_e32 v[46:47], v[14:15]
	v_mov_b64_e32 v[44:45], v[12:13]
	v_mov_b64_e32 v[42:43], v[10:11]
	v_mov_b64_e32 v[40:41], v[8:9]
	v_mov_b64_e32 v[38:39], v[6:7]
	v_mov_b64_e32 v[36:37], v[4:5]
	v_mov_b64_e32 v[34:35], v[2:3]
	v_mov_b64_e32 v[62:63], v[14:15]
	v_mov_b64_e32 v[60:61], v[12:13]
	v_mov_b64_e32 v[58:59], v[10:11]
	v_mov_b64_e32 v[56:57], v[8:9]
	v_mov_b64_e32 v[54:55], v[6:7]
	v_mov_b64_e32 v[52:53], v[4:5]
	v_mov_b64_e32 v[50:51], v[2:3]
	v_mov_b64_e32 v[78:79], v[14:15]
	v_mov_b64_e32 v[76:77], v[12:13]
	v_mov_b64_e32 v[74:75], v[10:11]
	v_mov_b64_e32 v[72:73], v[8:9]
	v_mov_b64_e32 v[70:71], v[6:7]
	v_mov_b64_e32 v[68:69], v[4:5]
	v_mov_b64_e32 v[66:67], v[2:3]
	v_mov_b64_e32 v[30:31], v[14:15]
	v_mov_b64_e32 v[28:29], v[12:13]
	v_mov_b64_e32 v[26:27], v[10:11]
	v_mov_b64_e32 v[24:25], v[8:9]
	v_mov_b64_e32 v[22:23], v[6:7]
	v_mov_b64_e32 v[20:21], v[4:5]
	v_mov_b64_e32 v[18:19], v[2:3]
	v_mov_b32_e32 v163, v162
	v_mov_b32_e32 v164, v162
	v_mov_b32_e32 v165, v162
	v_mov_b32_e32 v166, v162
	v_mov_b32_e32 v167, v162
	v_mov_b32_e32 v168, v162
	v_mov_b32_e32 v169, v162
	s_branch .LBB0_1380

.LBB0_1407:
	s_ashr_i32 s95, s94, 31
	s_lshl_b64 s[38:39], s[94:95], 10
	s_add_u32 s38, s16, s38
	s_addc_u32 s39, s17, s39
	v_lshl_add_u64 v[130:131], s[38:39], 0, v[180:181]
	v_mov_b32_e32 v183, v181
	v_lshl_add_u64 v[130:131], v[130:131], 0, s[28:29]
	s_mov_b64 s[28:29], 0x2030000
	s_mov_b32 m0, s49
	v_lshl_add_u64 v[130:131], v[130:131], 0, s[28:29]
	v_lshl_add_u64 v[170:171], s[90:91], 0, v[182:183]
	s_mov_b64 s[28:29], 0x204000
	global_load_lds_dwordx4 v[130:131], off
	v_lshl_add_u64 v[130:131], v[170:171], 0, s[28:29]
	s_mov_b32 m0, s47
	s_mov_b64 s[28:29], 0x205000
	global_load_lds_dwordx4 v[130:131], off
	v_lshl_add_u64 v[130:131], v[170:171], 0, s[28:29]
	s_mov_b32 m0, s48
	v_cvt_pk_fp8_f32 v162, v114, v115
	global_load_lds_dwordx4 v[130:131], off
	v_cvt_pk_fp8_f32 v163, v118, v119
	ds_read_b128 v[130:133], v205 offset:0
	ds_read_b128 v[134:137], v206 offset:0
	ds_read_b128 v[210:213], v205 offset:0x800
	ds_read_b128 v[214:217], v206 offset:0x800
	v_cvt_pk_fp8_f32 v162, v116, v117 op_sel:[0,0,1]
	v_cvt_pk_fp8_f32 v163, v120, v121 op_sel:[0,0,1]
	s_waitcnt lgkmcnt(2)
	v_cvt_pk_fp8_f32 v164, v122, v123
	v_cvt_pk_fp8_f32 v165, v126, v127
	ds_read_b128 v[218:221], v188 offset:0
	ds_read_b128 v[222:225], v189 offset:0
	v_cvt_pk_fp8_f32 v164, v124, v125 op_sel:[0,0,1]
	v_cvt_pk_fp8_f32 v165, v128, v129 op_sel:[0,0,1]
	v_mfma_f32_32x32x64_f8f6f4 v[114:129], v[130:137], v[154:161], v[82:97]
	s_waitcnt lgkmcnt(2)
	v_mfma_f32_32x32x64_f8f6f4 v[130:145], v[210:217], v[154:161], v[82:97]
	v_cvt_pk_fp8_f32 v166, v98, v99
	v_cvt_pk_fp8_f32 v167, v102, v103
	v_cvt_pk_fp8_f32 v168, v106, v107
	v_cvt_pk_fp8_f32 v169, v110, v111
	v_cvt_pk_fp8_f32 v166, v100, v101 op_sel:[0,0,1]
	v_cvt_pk_fp8_f32 v167, v104, v105 op_sel:[0,0,1]
	v_cvt_pk_fp8_f32 v168, v108, v109 op_sel:[0,0,1]
	v_cvt_pk_fp8_f32 v169, v112, v113 op_sel:[0,0,1]
	s_nop 0
	ds_read_b128 v[106:109], v188 offset:0x800
	ds_read_b128 v[110:113], v189 offset:0x800
	s_nop 0
	v_mfma_f32_16x16x128_f8f6f4 v[18:21], v[162:169], v[146:153], v[18:21]
	s_waitcnt lgkmcnt(2)
	v_mfma_f32_32x32x64_f8f6f4 v[2:17], v[162:169], v[218:225], v[2:17]
	ds_read_b128 v[98:101], v188 offset:0x1000
	ds_read_b128 v[102:105], v189 offset:0x1000
	v_max3_f32 v172, v114, v115, v116
	v_max3_f32 v172, v172, v117, v118
	v_max3_f32 v172, v172, v119, v120
	v_max3_f32 v172, v172, v121, v122
	v_max3_f32 v172, v172, v123, v124
	v_max3_f32 v172, v172, v125, v126
	v_max3_f32 v172, v172, v127, v128
	v_max_f32 v172, v172, v129
	s_nop 0
	v_max3_f32 v172, v172, v130, v131
	v_max3_f32 v172, v172, v132, v133
	v_max3_f32 v172, v172, v134, v135
	v_max3_f32 v172, v172, v136, v137
	v_max3_f32 v172, v172, v138, v139
	v_max3_f32 v172, v172, v140, v141
	v_max3_f32 v172, v172, v142, v143
	v_max3_f32 v172, v172, v144, v145
	v_mov_b32 v173, v172
	s_nop 1
	v_permlane32_swap_b32 v172, v173
	v_max_f32 v172, v172, v173
	s_nop 0
	v_cmp_ge_f32_e32 vcc, s54, v172
	s_cmp_lg_u64 vcc, exec
	s_cselect_b64 s[28:29], -1, 0
	s_cmp_eq_u64 vcc, exec
	s_cbranch_scc1 .LBB0_1409
	v_add_f32_e32 v82, 0xc0c00000, v172
	v_max_f32_e32 v82, 0, v82
	v_exp_f32_e64 v172, -v82
	v_add_f32_e32 v198, v198, v82
	v_sub_f32_e32 v114, v114, v82
	v_sub_f32_e32 v130, v130, v82
	v_sub_f32_e32 v115, v115, v82
	v_sub_f32_e32 v131, v131, v82
	v_sub_f32_e32 v116, v116, v82
	v_sub_f32_e32 v132, v132, v82
	v_sub_f32_e32 v117, v117, v82
	v_sub_f32_e32 v133, v133, v82
	v_sub_f32_e32 v118, v118, v82
	v_sub_f32_e32 v134, v134, v82
	v_sub_f32_e32 v119, v119, v82
	v_sub_f32_e32 v135, v135, v82
	v_sub_f32_e32 v120, v120, v82
	v_sub_f32_e32 v136, v136, v82
	v_sub_f32_e32 v121, v121, v82
	v_sub_f32_e32 v137, v137, v82
	v_sub_f32_e32 v122, v122, v82
	v_sub_f32_e32 v138, v138, v82
	v_sub_f32_e32 v123, v123, v82
	v_sub_f32_e32 v139, v139, v82
	v_sub_f32_e32 v124, v124, v82
	v_sub_f32_e32 v140, v140, v82
	v_sub_f32_e32 v125, v125, v82
	v_sub_f32_e32 v141, v141, v82
	v_sub_f32_e32 v126, v126, v82
	v_sub_f32_e32 v142, v142, v82
	v_sub_f32_e32 v127, v127, v82
	v_sub_f32_e32 v143, v143, v82
	v_sub_f32_e32 v128, v128, v82
	v_sub_f32_e32 v144, v144, v82
	v_sub_f32_e32 v129, v129, v82
	v_sub_f32_e32 v145, v145, v82
	v_xor_b32_e32 v82, 0x80000000, v198
	v_mov_b32_e32 v83, v82
	v_mov_b32_e32 v84, v82
	v_mov_b32_e32 v85, v82
	v_mov_b32_e32 v86, v82
	v_mov_b32_e32 v87, v82
	v_mov_b32_e32 v88, v82
	v_mov_b32_e32 v89, v82
	v_mov_b32_e32 v90, v82
	v_mov_b32_e32 v91, v82
	v_mov_b32_e32 v92, v82
	v_mov_b32_e32 v93, v82
	v_mov_b32_e32 v94, v82
	v_mov_b32_e32 v95, v82
	v_mov_b32_e32 v96, v82
	v_mov_b32_e32 v97, v82
	s_branch .LBB0_1410

	.amdhsa_kernel _Z6mk_fwd4Args
		.amdhsa_group_segment_fixed_size 0
		.amdhsa_private_segment_fixed_size 0
		.amdhsa_kernarg_size 488
		.amdhsa_user_sgpr_count 2
		.amdhsa_user_sgpr_dispatch_ptr 0
		.amdhsa_user_sgpr_queue_ptr 0
		.amdhsa_user_sgpr_kernarg_segment_ptr 1
		.amdhsa_user_sgpr_dispatch_id 0
		.amdhsa_user_sgpr_kernarg_preload_length 0
		.amdhsa_user_sgpr_kernarg_preload_offset 0
		.amdhsa_user_sgpr_private_segment_size 0
		.amdhsa_uses_dynamic_stack 0
		.amdhsa_enable_private_segment 0
		.amdhsa_system_sgpr_workgroup_id_x 1
		.amdhsa_system_sgpr_workgroup_id_y 0
		.amdhsa_system_sgpr_workgroup_id_z 0
		.amdhsa_system_sgpr_workgroup_info 0
		.amdhsa_system_vgpr_workitem_id 0
		.amdhsa_next_free_vgpr 256
		.amdhsa_next_free_sgpr 102
		.amdhsa_accum_offset 256
		.amdhsa_reserve_vcc 1
		.amdhsa_float_round_mode_32 0
		.amdhsa_float_round_mode_16_64 0
		.amdhsa_float_denorm_mode_32 3
		.amdhsa_float_denorm_mode_16_64 3
		.amdhsa_dx10_clamp 1
		.amdhsa_ieee_mode 1
		.amdhsa_fp16_overflow 0
		.amdhsa_tg_split 0
		.amdhsa_exception_fp_ieee_invalid_op 0
		.amdhsa_exception_fp_denorm_src 0
		.amdhsa_exception_fp_ieee_div_zero 0
		.amdhsa_exception_fp_ieee_overflow 0
		.amdhsa_exception_fp_ieee_underflow 0
		.amdhsa_exception_fp_ieee_inexact 0
		.amdhsa_exception_int_div_zero 0
	.end_amdhsa_kernel

amdhsa.kernels:
  - .agpr_count:     0
    .args:
      - .offset:         0
        .size:           232
        .value_kind:     by_value
      - .offset:         232
        .size:           4
        .value_kind:     hidden_block_count_x
      - .offset:         236
        .size:           4
        .value_kind:     hidden_block_count_y
      - .offset:         240
        .size:           4
        .value_kind:     hidden_block_count_z
      - .offset:         244
        .size:           2
        .value_kind:     hidden_group_size_x
      - .offset:         246
        .size:           2
        .value_kind:     hidden_group_size_y
      - .offset:         248
        .size:           2
        .value_kind:     hidden_group_size_z
      - .offset:         250
        .size:           2
        .value_kind:     hidden_remainder_x
      - .offset:         252
        .size:           2
        .value_kind:     hidden_remainder_y
      - .offset:         254
        .size:           2
        .value_kind:     hidden_remainder_z
      - .offset:         272
        .size:           8
        .value_kind:     hidden_global_offset_x
      - .offset:         280
        .size:           8
        .value_kind:     hidden_global_offset_y
      - .offset:         288
        .size:           8
        .value_kind:     hidden_global_offset_z
      - .offset:         296
        .size:           2
        .value_kind:     hidden_grid_dims
      - .offset:         352
        .size:           4
        .value_kind:     hidden_dynamic_lds_size
    .group_segment_fixed_size: 0
    .kernarg_segment_align: 8
    .kernarg_segment_size: 488
    .language:       OpenCL C
    .language_version:
      - 2
      - 0
    .max_flat_workgroup_size: 512
    .name:           _Z6mk_fwd4Args
    .private_segment_fixed_size: 0
    .sgpr_count:     108
    .sgpr_spill_count: 41
    .symbol:         _Z6mk_fwd4Args.kd
    .uniform_work_group_size: 1
    .uses_dynamic_stack: false
    .vgpr_count:     256
    .vgpr_spill_count: 0
    .wavefront_size: 64
